# re-measure of c13 (peel + PRO transpose + non-scaled fp8 MFMA + nop trim + setprio pair removal)
# baseline (speedup 1.0000x reference)
; #define LAS __attribute__((address_space(3)))
; __device__ __forceinline__ unsigned xb_xcc_id() { return (unsigned)__builtin_amdgcn_s_getreg((3 << 11) | 20) & 0xFu; }
; __global__ void __launch_bounds__(NTHREADS, 2) fwd(Args args) {
;     extern __shared__ __attribute__((aligned(16))) unsigned char lds[];
;     Frame F;
;     F.lds = (LAS unsigned char*)lds; F.MISC = (volatile LAS unsigned*)(F.lds + MISC_OFF);
;     F.tid = threadIdx.x; F.lane = F.tid & 63; F.wave = __builtin_amdgcn_readfirstlane(F.tid >> 6); F.bid = blockIdx.x;
;     ...
;     for (int u = F.tid; u < (LDS_BYTES - RING_BYTES) / 4; u += NTHREADS) ((LAS unsigned*)(F.lds + RING_BYTES))[u] = 0u;
;     __syncthreads();
;     XcdBarrier bar; bar.bar = (unsigned*)(ws + WS_CTL) + CW_BAR; bar.x = 0; bar.st = nullptr;
;     if (!MK_PER_PHASE) bar = xcd_barrier_post((unsigned*)(ws + WS_CTL) + CW_BAR, F.MISC + 8);
;     if (F.tid == 0) __hip_atomic_store((unsigned*)(ws + WS_CTL) + CW_XCC + F.bid, xb_xcc_id() + 1u, RLX_AGENT);
_Z3fwd4Args:
	s_mov_b32 s98, 0
	s_mov_b64 s[100:101], s[0:1]
	s_mov_b32 s99, s2
	v_mov_b32_e32 v249, v0
.Lprobe_reentry:
	v_lshl_add_u32 v163, v0, 2, 0
	v_mov_b32_e32 v2, 0
	v_add_u32_e32 v1, 0x20000, v163
	s_mov_b64 s[66:67], s[0:1]
	v_readfirstlane_b32 s14, v0
	ds_write2st64_b32 v1, v2, v2 offset1:8
	ds_write2st64_b32 v1, v2, v2 offset0:16 offset1:24
	v_or_b32_e32 v1, 0x800, v0
	s_mov_b64 s[4:5], -1
	s_and_saveexec_b64 s[6:7], s[4:5]
	v_lshl_add_u32 v3, v1, 2, 0
	v_add_u32_e32 v3, 0x20000, v3
	ds_write_b32 v3, v2
	s_or_b64 exec, exec, s[6:7]
	s_load_dwordx2 s[34:35], s[66:67], 0xb0
	s_load_dwordx4 s[60:63], s[66:67], 0xa0
	s_load_dwordx8 s[52:59], s[66:67], 0x80
	s_and_saveexec_b64 s[6:7], s[4:5]
	s_add_i32 s0, 0, 0x20000
	v_lshl_add_u32 v1, v1, 2, s0
	v_mov_b32_e32 v2, 0
	ds_write_b32 v1, v2 offset:2048
	s_or_b64 exec, exec, s[6:7]
	v_or_b32_e32 v1, 0xc00, v0
	v_cmp_gt_u32_e64 s[4:5], 7, 6
	v_cmp_gt_u32_e64 s[0:1], 7, 5
	s_and_saveexec_b64 s[6:7], s[0:1]
	v_lshl_add_u32 v2, v1, 2, 0
	v_add_u32_e32 v2, 0x20000, v2
	v_mov_b32_e32 v3, 0
	ds_write_b32 v2, v3
	s_or_b64 exec, exec, s[6:7]
	s_and_saveexec_b64 s[6:7], s[4:5]
	s_add_i32 s0, 0, 0x20000
	v_lshl_add_u32 v1, v1, 2, s0
	v_mov_b32_e32 v2, 0
	ds_write_b32 v1, v2 offset:2048
	s_or_b64 exec, exec, s[6:7]
	s_waitcnt lgkmcnt(0)
	s_add_u32 s0, s34, 0x4000
	s_addc_u32 s1, s35, 0
	s_load_dwordx2 s[64:65], s[66:67], 0xb8
	v_writelane_b32 v248, s0, 0
	s_waitcnt lgkmcnt(0)
	s_cmp_eq_u32 s98, 0
	s_cbranch_scc1 .Lprobe_sel_done
	s_cmp_eq_u32 s98, 1
	s_cbranch_scc0 .Lprobe_sel_n0
	s_mov_b32 s64, 4
	s_mov_b32 s65, 5
	s_branch .Lprobe_sel_done
.Lprobe_sel_n0:
.Lprobe_sel_done:
	s_barrier
	v_writelane_b32 v248, s1, 1
	s_getreg_b32 s0, hwreg(HW_REG_XCC_ID, 0, 4)
	s_and_b32 s94, s0, 15
	v_cmp_ne_u32_e64 s[0:1], 0, v0
	s_nop 1
	v_writelane_b32 v248, s0, 2
	s_nop 1
	v_writelane_b32 v248, s1, 3
	v_cmp_eq_u32_e64 s[0:1], 0, v0
	s_nop 1
	v_writelane_b32 v248, s0, 4
	s_nop 1
	v_writelane_b32 v248, s1, 5
	s_and_saveexec_b64 s[8:9], s[0:1]
	s_cbranch_execz .LBB0_12
	s_mov_b64 s[12:13], exec
	v_mbcnt_lo_u32_b32 v1, s12, 0
	v_mbcnt_hi_u32_b32 v1, s13, v1
	v_cmp_eq_u32_e32 vcc, 0, v1
	s_and_saveexec_b64 s[10:11], vcc
	s_cbranch_execz .LBB0_11
	s_lshl_b32 s3, s94, 8
	s_bcnt1_i32_b64 s4, s[12:13]
	v_readlane_b32 s0, v248, 0
	v_mov_b32_e32 v1, s3
	v_mov_b32_e32 v2, s4
	v_readlane_b32 s1, v248, 1
	s_nop 4
	global_atomic_add v1, v2, s[0:1] offset:1024

; #define PG8_STAGE(bufoff, gbase, voff) do { _Pragma("unroll") for (int _i = 0; _i < 2; ++_i) \
;         __builtin_amdgcn_global_load_lds((const unsigned*)((const char*)(gbase) + (voff)[_i]), (PG8_LAS unsigned*)(lds + (bufoff) + ldsw + _i * 8192), 16, 0, 0); } while (0)
; #define PG8_LDA(dst, b, h) do { _Pragma("unroll") for (int m = 0; m < 4; ++m) Frag<F8>::load(dst[m], lds + PG8_SA(b, h) + aoff + m * 2048); } while (0)
; #define PG8_BAR __builtin_amdgcn_s_barrier()
; template <class Epi, class Sched, bool ALIGN_EPI = false, bool SP2 = false, bool F8 = false>
; __device__ __forceinline__ void gemm_phase(PG8_LAS unsigned char* lds, const Gemm g, const Sched& S, const Epi& E) {
;     ...
;         const bool has_next = S.next(ui + 1, nxt);
;         const char* nA = has_next ? (const char*)g.A + (size_t)nxt.pm * tstep + nxt.ko : cA; const char* nB = has_next ? (const char*)g.Bt + (size_t)nxt.pn * tstep + nxt.ko : cB;
;         for (int t = 0; t < nt; t += 2) {
;             const bool last = (t == nt - 2);
;             const char* a1 = cA + (size_t)(t + 1) * kstep;
;             const char* a2 = last ? nA : cA + (size_t)(t + 2) * kstep; const char* b2 = last ? nB : cB + (size_t)(t + 2) * kstep;
;             const char* a3 = a2 + kstep; const char* b3 = b2 + kstep;
;             if (last && has_next) S.a_ready(nxt);
;             if constexpr (SP2) {
;             PG8_LDB(B0, 0, 0); PG8_LDB(B1, 0, 1); PG8_SCHED; PG8_LDA(At, 0, 0); PG8_STAGE(PG8_SA(1, 1), a1 + hstep, voffA);
;             PG8_WAIT_V(8); PG8_WAIT_L(0); PG8_BAR; PG8_MMA(0, 0, At, B0); PG8_MMA(0, 1, At, B1); PG8_BAR; PG8_SCHED;
;             PG8_LDA(At, 0, 1); PG8_STAGE(PG8_SB(0, 0), b2, voffB); PG8_STAGE(PG8_SB(0, 1), b2 + hstep, voffB); PG8_STAGE(PG8_SA(0, 0), a2, voffA);
;             PG8_WAIT_V(8); PG8_WAIT_L(0); PG8_BAR; PG8_MMA(1, 0, At, B0); PG8_MMA(1, 1, At, B1); PG8_BAR; PG8_SCHED;
;             PG8_LDB(B0, 1, 0); PG8_LDB(B1, 1, 1); PG8_SCHED; PG8_LDA(At, 1, 0); PG8_STAGE(PG8_SA(0, 1), a2 + hstep, voffA);
;             PG8_WAIT_V(8); PG8_WAIT_L(0); PG8_BAR; PG8_MMA(0, 0, At, B0); PG8_MMA(0, 1, At, B1); PG8_BAR; PG8_SCHED;
;             PG8_LDA(At, 1, 1); PG8_STAGE(PG8_SB(1, 0), b3, voffB); PG8_STAGE(PG8_SB(1, 1), b3 + hstep, voffB); PG8_STAGE(PG8_SA(1, 0), a3, voffA);
;             PG8_WAIT_V(8); PG8_WAIT_L(0); PG8_BAR; PG8_MMA(1, 0, At, B0); PG8_MMA(1, 1, At, B1); PG8_BAR; PG8_SCHED;
.LBB0_150:
	s_ashr_i32 s25, s24, 31
	s_lshl_b64 s[4:5], s[24:25], 18
	s_add_u32 s38, s77, s4
	s_addc_u32 s39, s78, s5
	s_and_b64 s[4:5], s[8:9], exec
	s_cselect_b32 s25, s39, s71
	s_cselect_b32 s91, s38, s70
	s_ashr_i32 s31, s30, 31
	s_lshl_b64 s[4:5], s[30:31], 18
	s_add_u32 s42, s79, s4
	s_addc_u32 s43, s80, s5
	s_and_b64 s[4:5], s[8:9], exec
	s_cselect_b32 s31, s43, s73
	s_cselect_b32 s92, s42, s72
	s_add_u32 s70, s70, 0x20080
	s_addc_u32 s71, s71, 0
	s_add_u32 s93, s72, 0x100
	s_addc_u32 s95, s73, 0
	s_mov_b32 s96, -2
	ds_read_b128 v[18:21], v194
	ds_read_b128 v[22:25], v194 offset:1024
	ds_read_b128 v[26:29], v194 offset:2048
	ds_read_b128 v[30:33], v194 offset:3072
	ds_read_b128 v[2:5], v195
	ds_read_b128 v[6:9], v195 offset:1024
	ds_read_b128 v[10:13], v195 offset:2048
	ds_read_b128 v[14:17], v195 offset:3072
	s_add_u32 s0, s70, 0xfffe0080
	s_addc_u32 s1, s71, -1
	s_cmp_eq_u32 s96, 4
	s_cselect_b32 s75, s25, s1
	s_cselect_b32 s74, s91, s0
	s_cselect_b32 s73, s31, s95
	s_cselect_b32 s72, s92, s93
	v_lshl_add_u64 v[224:225], s[70:71], 0, v[174:175]
	s_add_i32 m0, s45, 0xc000
	ds_read_b128 v[182:185], v196
	ds_read_b128 v[186:189], v196 offset:1024
	ds_read_b128 v[200:203], v196 offset:2048
	ds_read_b128 v[204:207], v196 offset:3072
	ds_read_b128 v[208:211], v196 offset:4096
	ds_read_b128 v[212:215], v196 offset:5120
	ds_read_b128 v[216:219], v196 offset:6144
	ds_read_b128 v[220:223], v196 offset:7168
	global_load_lds_dwordx4 v[224:225], off
	v_lshl_add_u64 v[224:225], s[70:71], 0, v[176:177]
	s_add_i32 m0, s45, 0xe000
	s_nop 0
	global_load_lds_dwordx4 v[224:225], off
	s_waitcnt vmcnt(8)
	s_waitcnt lgkmcnt(0)
	s_barrier
	s_setprio 3
	v_mfma_f32_16x16x128_f8f6f4 v[158:161], v[18:25], v[182:189], 0
	v_mfma_f32_16x16x128_f8f6f4 v[154:157], v[26:33], v[182:189], 0
	v_mfma_f32_16x16x128_f8f6f4 v[150:153], v[18:25], v[200:207], 0
	v_mfma_f32_16x16x128_f8f6f4 v[142:145], v[26:33], v[200:207], 0
	v_mfma_f32_16x16x128_f8f6f4 v[130:133], v[18:25], v[208:215], 0
	v_mfma_f32_16x16x128_f8f6f4 v[122:125], v[26:33], v[208:215], 0
	v_mfma_f32_16x16x128_f8f6f4 v[118:121], v[18:25], v[216:223], 0
	v_mfma_f32_16x16x128_f8f6f4 v[110:113], v[26:33], v[216:223], 0
	v_mfma_f32_16x16x128_f8f6f4 v[146:149], v[2:9], v[182:189], 0
	v_mfma_f32_16x16x128_f8f6f4 v[138:141], v[10:17], v[182:189], 0
	v_mfma_f32_16x16x128_f8f6f4 v[134:137], v[2:9], v[200:207], 0
	v_mfma_f32_16x16x128_f8f6f4 v[126:129], v[10:17], v[200:207], 0
	v_mfma_f32_16x16x128_f8f6f4 v[114:117], v[2:9], v[208:215], 0
	v_mfma_f32_16x16x128_f8f6f4 v[106:109], v[10:17], v[208:215], 0
	v_mfma_f32_16x16x128_f8f6f4 v[102:105], v[2:9], v[216:223], 0
	v_mfma_f32_16x16x128_f8f6f4 v[98:101], v[10:17], v[216:223], 0
	s_setprio 0
	s_barrier
	s_add_i32 s0, s87, s76
	v_lshl_add_u64 v[182:183], s[72:73], 0, v[170:171]
	s_mov_b32 m0, s0
	ds_read_b128 v[200:203], v196 offset:16384
	ds_read_b128 v[204:207], v196 offset:17408
	ds_read_b128 v[208:211], v196 offset:18432
	ds_read_b128 v[212:215], v196 offset:19456
	ds_read_b128 v[216:219], v196 offset:20480
	ds_read_b128 v[220:223], v196 offset:21504
	ds_read_b128 v[224:227], v196 offset:22528
	ds_read_b128 v[228:231], v196 offset:23552
	global_load_lds_dwordx4 v[182:183], off
	s_add_i32 m0, s0, 0x2000
	s_add_u32 s4, s72, 0x20000
	v_lshl_add_u64 v[184:185], s[72:73], 0, v[166:167]
	s_addc_u32 s5, s73, 0
	s_add_i32 s0, s88, s76
	global_load_lds_dwordx4 v[184:185], off
	v_lshl_add_u64 v[186:187], s[4:5], 0, v[170:171]
	s_mov_b32 m0, s0
	v_lshl_add_u64 v[188:189], s[74:75], 0, v[168:169]
	global_load_lds_dwordx4 v[186:187], off
	v_lshl_add_u64 v[186:187], s[4:5], 0, v[166:167]
	s_add_i32 m0, s0, 0x2000
	s_nop 0
	global_load_lds_dwordx4 v[186:187], off
	v_lshl_add_u64 v[186:187], s[74:75], 0, v[172:173]
	s_mov_b32 m0, s45
	s_nop 0
	global_load_lds_dwordx4 v[186:187], off
	s_mov_b32 m0, s82
	s_nop 0
	global_load_lds_dwordx4 v[188:189], off
	s_waitcnt vmcnt(8)
	s_waitcnt lgkmcnt(0)
	s_barrier
	s_setprio 3
	v_mfma_f32_16x16x128_f8f6f4 v[94:97], v[18:25], v[200:207], 0
	v_mfma_f32_16x16x128_f8f6f4 v[90:93], v[26:33], v[200:207], 0
	v_mfma_f32_16x16x128_f8f6f4 v[86:89], v[18:25], v[208:215], 0
	v_mfma_f32_16x16x128_f8f6f4 v[82:85], v[26:33], v[208:215], 0
	v_mfma_f32_16x16x128_f8f6f4 v[70:73], v[18:25], v[216:223], 0
	v_mfma_f32_16x16x128_f8f6f4 v[66:69], v[26:33], v[216:223], 0
	v_mfma_f32_16x16x128_f8f6f4 v[54:57], v[18:25], v[224:231], 0
	v_mfma_f32_16x16x128_f8f6f4 v[50:53], v[26:33], v[224:231], 0
	v_mfma_f32_16x16x128_f8f6f4 v[78:81], v[2:9], v[200:207], 0
	v_mfma_f32_16x16x128_f8f6f4 v[74:77], v[10:17], v[200:207], 0
	v_mfma_f32_16x16x128_f8f6f4 v[62:65], v[2:9], v[208:215], 0
	v_mfma_f32_16x16x128_f8f6f4 v[58:61], v[10:17], v[208:215], 0
	v_mfma_f32_16x16x128_f8f6f4 v[46:49], v[2:9], v[216:223], 0
	v_mfma_f32_16x16x128_f8f6f4 v[42:45], v[10:17], v[216:223], 0
	v_mfma_f32_16x16x128_f8f6f4 v[38:41], v[2:9], v[224:231], 0
	v_mfma_f32_16x16x128_f8f6f4 v[34:37], v[10:17], v[224:231], 0
	s_setprio 0
	s_barrier
	s_add_i32 s0, 0, 0x18000
	s_add_i32 s1, 0, 0x1c000
	v_add_u32_e32 v14, s0, v190
	v_add_u32_e32 v30, s1, v190
	ds_read_b128 v[2:5], v14
	ds_read_b128 v[6:9], v14 offset:1024
	ds_read_b128 v[10:13], v14 offset:2048
	ds_read_b128 v[14:17], v14 offset:3072
	ds_read_b128 v[18:21], v30
	ds_read_b128 v[22:25], v30 offset:1024
	ds_read_b128 v[26:29], v30 offset:2048
	ds_read_b128 v[30:33], v30 offset:3072
	s_add_u32 s4, s74, 0x20000
	s_addc_u32 s5, s75, 0
	s_mov_b32 m0, s83
	v_lshl_add_u64 v[232:233], s[4:5], 0, v[172:173]
	ds_read_b128 v[200:203], v196 offset:32768
	ds_read_b128 v[204:207], v196 offset:33792
	ds_read_b128 v[208:211], v196 offset:34816
	ds_read_b128 v[212:215], v196 offset:35840
	ds_read_b128 v[216:219], v196 offset:36864
	ds_read_b128 v[220:223], v196 offset:37888
	ds_read_b128 v[224:227], v196 offset:38912
	ds_read_b128 v[228:231], v196 offset:39936
	global_load_lds_dwordx4 v[232:233], off
	v_lshl_add_u64 v[232:233], s[4:5], 0, v[168:169]
	s_mov_b32 m0, s84
	s_nop 0
	global_load_lds_dwordx4 v[232:233], off
	s_waitcnt vmcnt(8)
	s_waitcnt lgkmcnt(0)
	s_barrier
; #define PG8_STAGE(bufoff, gbase, voff) do { _Pragma("unroll") for (int _i = 0; _i < 2; ++_i) \
;         __builtin_amdgcn_global_load_lds((const unsigned*)((const char*)(gbase) + (voff)[_i]), (PG8_LAS unsigned*)(lds + (bufoff) + ldsw + _i * 8192), 16, 0, 0); } while (0)
; #define PG8_LDA(dst, b, h) do { _Pragma("unroll") for (int m = 0; m < 4; ++m) Frag<F8>::load(dst[m], lds + PG8_SA(b, h) + aoff + m * 2048); } while (0)
; #define PG8_LDB(dst, b, h) do { _Pragma("unroll") for (int n = 0; n < 2; ++n) Frag<F8>::load(dst[n], lds + PG8_SB(b, h) + boff + n * 2048); } while (0)
; #define PG8_MMA(ai, bj, At, Bt) do { __builtin_amdgcn_s_setprio(3); _Pragma("unroll") for (int m = 0; m < 4; ++m) _Pragma("unroll") for (int n = 0; n < 2; ++n) Frag<F8>::mma(acc[ai][bj][m][n], Bt[n], At[m]); \
;         __builtin_amdgcn_s_setprio(0); } while (0)
; #define PG8_WAIT_V(n) asm volatile("s_waitcnt vmcnt(" #n ")" ::: "memory")
; #define PG8_WAIT_L(n) asm volatile("s_waitcnt lgkmcnt(" #n ")" ::: "memory")
; #define PG8_BAR __builtin_amdgcn_s_barrier()
; #define PG8_SCHED __builtin_amdgcn_sched_barrier(0)
; template <class Epi, class Sched, bool ALIGN_EPI = false, bool SP2 = false, bool F8 = false>
; __device__ __forceinline__ void gemm_phase(PG8_LAS unsigned char* lds, const Gemm g, const Sched& S, const Epi& E) {
;     ...
;             PG8_WAIT_V(8); PG8_WAIT_L(0); PG8_BAR; PG8_MMA(1, 0, At, B0); PG8_MMA(1, 1, At, B1); PG8_BAR; PG8_SCHED;
;             PG8_LDB(B0, 1, 0); PG8_LDB(B1, 1, 1); PG8_SCHED; PG8_LDA(At, 1, 0); PG8_STAGE(PG8_SA(0, 1), a2 + hstep, voffA);
;             PG8_WAIT_V(8); PG8_WAIT_L(0); PG8_BAR; PG8_MMA(0, 0, At, B0); PG8_MMA(0, 1, At, B1); PG8_BAR; PG8_SCHED;
;             PG8_LDA(At, 1, 1); PG8_STAGE(PG8_SB(1, 0), b3, voffB); PG8_STAGE(PG8_SB(1, 1), b3 + hstep, voffB); PG8_STAGE(PG8_SA(1, 0), a3, voffA);
;             PG8_WAIT_V(8); PG8_WAIT_L(0); PG8_BAR; PG8_MMA(1, 0, At, B0); PG8_MMA(1, 1, At, B1); PG8_BAR; PG8_SCHED;
	s_setprio 3
	v_mfma_f32_16x16x128_f8f6f4 v[158:161], v[2:9], v[200:207], v[158:161]
	v_mfma_f32_16x16x128_f8f6f4 v[154:157], v[10:17], v[200:207], v[154:157]
	v_mfma_f32_16x16x128_f8f6f4 v[150:153], v[2:9], v[208:215], v[150:153]
	v_mfma_f32_16x16x128_f8f6f4 v[142:145], v[10:17], v[208:215], v[142:145]
	v_mfma_f32_16x16x128_f8f6f4 v[130:133], v[2:9], v[216:223], v[130:133]
	v_mfma_f32_16x16x128_f8f6f4 v[122:125], v[10:17], v[216:223], v[122:125]
	v_mfma_f32_16x16x128_f8f6f4 v[118:121], v[2:9], v[224:231], v[118:121]
	v_mfma_f32_16x16x128_f8f6f4 v[110:113], v[10:17], v[224:231], v[110:113]
	v_mfma_f32_16x16x128_f8f6f4 v[146:149], v[18:25], v[200:207], v[146:149]
	v_mfma_f32_16x16x128_f8f6f4 v[138:141], v[26:33], v[200:207], v[138:141]
	v_mfma_f32_16x16x128_f8f6f4 v[134:137], v[18:25], v[208:215], v[134:137]
	v_mfma_f32_16x16x128_f8f6f4 v[126:129], v[26:33], v[208:215], v[126:129]
	v_mfma_f32_16x16x128_f8f6f4 v[114:117], v[18:25], v[216:223], v[114:117]
	v_mfma_f32_16x16x128_f8f6f4 v[106:109], v[26:33], v[216:223], v[106:109]
	v_mfma_f32_16x16x128_f8f6f4 v[102:105], v[18:25], v[224:231], v[102:105]
	v_mfma_f32_16x16x128_f8f6f4 v[98:101], v[26:33], v[224:231], v[98:101]
	s_setprio 0
	s_barrier
	s_add_i32 s0, s0, s76
	v_lshl_add_u64 v[182:183], v[182:183], 0, s[18:19]
	s_mov_b32 m0, s0
	ds_read_b128 v[200:203], v196 offset:49152
	ds_read_b128 v[204:207], v196 offset:50176
	ds_read_b128 v[208:211], v196 offset:51200
	ds_read_b128 v[212:215], v196 offset:52224
	ds_read_b128 v[216:219], v196 offset:53248
	ds_read_b128 v[220:223], v196 offset:54272
	ds_read_b128 v[224:227], v196 offset:55296
	ds_read_b128 v[228:231], v196 offset:56320
	global_load_lds_dwordx4 v[182:183], off
	s_add_i32 m0, s0, 0x2000
	s_add_u32 s4, s72, 0x20080
	v_lshl_add_u64 v[182:183], v[184:185], 0, s[18:19]
	s_addc_u32 s5, s73, 0
	s_add_i32 s0, s1, s76
	global_load_lds_dwordx4 v[182:183], off
	v_lshl_add_u64 v[182:183], s[4:5], 0, v[170:171]
	s_mov_b32 m0, s0
	s_nop 0
	global_load_lds_dwordx4 v[182:183], off
	v_lshl_add_u64 v[182:183], s[4:5], 0, v[166:167]
	s_add_i32 m0, s0, 0x2000
	s_nop 0
	global_load_lds_dwordx4 v[182:183], off
	v_lshl_add_u64 v[182:183], v[186:187], 0, s[18:19]
	s_mov_b32 m0, s85
	s_nop 0
	global_load_lds_dwordx4 v[182:183], off
	v_lshl_add_u64 v[182:183], v[188:189], 0, s[18:19]
	s_mov_b32 m0, s86
	s_nop 0
	global_load_lds_dwordx4 v[182:183], off
	s_waitcnt vmcnt(8)
	s_waitcnt lgkmcnt(0)
	s_barrier
	s_setprio 3
	v_mfma_f32_16x16x128_f8f6f4 v[94:97], v[2:9], v[200:207], v[94:97]
	v_mfma_f32_16x16x128_f8f6f4 v[90:93], v[10:17], v[200:207], v[90:93]
	v_mfma_f32_16x16x128_f8f6f4 v[86:89], v[2:9], v[208:215], v[86:89]
	v_mfma_f32_16x16x128_f8f6f4 v[82:85], v[10:17], v[208:215], v[82:85]
	v_mfma_f32_16x16x128_f8f6f4 v[70:73], v[2:9], v[216:223], v[70:73]
	v_mfma_f32_16x16x128_f8f6f4 v[66:69], v[10:17], v[216:223], v[66:69]
	v_mfma_f32_16x16x128_f8f6f4 v[54:57], v[2:9], v[224:231], v[54:57]
	v_mfma_f32_16x16x128_f8f6f4 v[50:53], v[10:17], v[224:231], v[50:53]
	v_mfma_f32_16x16x128_f8f6f4 v[78:81], v[18:25], v[200:207], v[78:81]
	v_mfma_f32_16x16x128_f8f6f4 v[74:77], v[26:33], v[200:207], v[74:77]
	v_mfma_f32_16x16x128_f8f6f4 v[62:65], v[18:25], v[208:215], v[62:65]
	v_mfma_f32_16x16x128_f8f6f4 v[58:61], v[26:33], v[208:215], v[58:61]
	v_mfma_f32_16x16x128_f8f6f4 v[46:49], v[18:25], v[216:223], v[46:49]
	v_mfma_f32_16x16x128_f8f6f4 v[42:45], v[26:33], v[216:223], v[42:45]
	v_mfma_f32_16x16x128_f8f6f4 v[38:41], v[18:25], v[224:231], v[38:41]
	v_mfma_f32_16x16x128_f8f6f4 v[34:37], v[26:33], v[224:231], v[34:37]
	s_setprio 0
	s_barrier
	s_add_i32 s96, s96, 2
	s_add_u32 s70, s70, 0x100
	s_addc_u32 s71, s71, 0
	s_add_u32 s93, s93, 0x100
	s_addc_u32 s95, s95, 0
	s_cmp_gt_u32 s96, 5
	s_cbranch_scc1 .Lpeel_exit_0
.LBB0_151:
	ds_read_b128 v[18:21], v194
	ds_read_b128 v[22:25], v194 offset:1024
	ds_read_b128 v[26:29], v194 offset:2048
	ds_read_b128 v[30:33], v194 offset:3072
	ds_read_b128 v[2:5], v195
	ds_read_b128 v[6:9], v195 offset:1024
	ds_read_b128 v[10:13], v195 offset:2048
	ds_read_b128 v[14:17], v195 offset:3072
	s_add_u32 s0, s70, 0xfffe0080
	s_addc_u32 s1, s71, -1
	s_cmp_eq_u32 s96, 4
	s_cselect_b32 s75, s25, s1
	s_cselect_b32 s74, s91, s0
	s_cselect_b32 s73, s31, s95
	s_cselect_b32 s72, s92, s93
	v_lshl_add_u64 v[224:225], s[70:71], 0, v[174:175]
	s_add_i32 m0, s45, 0xc000
	ds_read_b128 v[182:185], v196
	ds_read_b128 v[186:189], v196 offset:1024
	ds_read_b128 v[200:203], v196 offset:2048
	ds_read_b128 v[204:207], v196 offset:3072
	ds_read_b128 v[208:211], v196 offset:4096
	ds_read_b128 v[212:215], v196 offset:5120
	ds_read_b128 v[216:219], v196 offset:6144
	ds_read_b128 v[220:223], v196 offset:7168
	global_load_lds_dwordx4 v[224:225], off
	v_lshl_add_u64 v[224:225], s[70:71], 0, v[176:177]
	s_add_i32 m0, s45, 0xe000
	s_nop 0
	global_load_lds_dwordx4 v[224:225], off
	s_waitcnt vmcnt(8)
	s_waitcnt lgkmcnt(0)
	s_barrier
	s_setprio 3
	v_mfma_f32_16x16x128_f8f6f4 v[158:161], v[18:25], v[182:189], v[158:161]
	v_mfma_f32_16x16x128_f8f6f4 v[154:157], v[26:33], v[182:189], v[154:157]
	v_mfma_f32_16x16x128_f8f6f4 v[150:153], v[18:25], v[200:207], v[150:153]
	v_mfma_f32_16x16x128_f8f6f4 v[142:145], v[26:33], v[200:207], v[142:145]
	v_mfma_f32_16x16x128_f8f6f4 v[130:133], v[18:25], v[208:215], v[130:133]
	v_mfma_f32_16x16x128_f8f6f4 v[122:125], v[26:33], v[208:215], v[122:125]
	v_mfma_f32_16x16x128_f8f6f4 v[118:121], v[18:25], v[216:223], v[118:121]
	v_mfma_f32_16x16x128_f8f6f4 v[110:113], v[26:33], v[216:223], v[110:113]
	v_mfma_f32_16x16x128_f8f6f4 v[146:149], v[2:9], v[182:189], v[146:149]
	v_mfma_f32_16x16x128_f8f6f4 v[138:141], v[10:17], v[182:189], v[138:141]
	v_mfma_f32_16x16x128_f8f6f4 v[134:137], v[2:9], v[200:207], v[134:137]
	v_mfma_f32_16x16x128_f8f6f4 v[126:129], v[10:17], v[200:207], v[126:129]
	v_mfma_f32_16x16x128_f8f6f4 v[114:117], v[2:9], v[208:215], v[114:117]
	v_mfma_f32_16x16x128_f8f6f4 v[106:109], v[10:17], v[208:215], v[106:109]
	v_mfma_f32_16x16x128_f8f6f4 v[102:105], v[2:9], v[216:223], v[102:105]
	v_mfma_f32_16x16x128_f8f6f4 v[98:101], v[10:17], v[216:223], v[98:101]
	s_setprio 0
	s_barrier
; #define PG8_STAGE(bufoff, gbase, voff) do { _Pragma("unroll") for (int _i = 0; _i < 2; ++_i) \
;         __builtin_amdgcn_global_load_lds((const unsigned*)((const char*)(gbase) + (voff)[_i]), (PG8_LAS unsigned*)(lds + (bufoff) + ldsw + _i * 8192), 16, 0, 0); } while (0)
; #define PG8_LDA(dst, b, h) do { _Pragma("unroll") for (int m = 0; m < 4; ++m) Frag<F8>::load(dst[m], lds + PG8_SA(b, h) + aoff + m * 2048); } while (0)
; #define PG8_LDB(dst, b, h) do { _Pragma("unroll") for (int n = 0; n < 2; ++n) Frag<F8>::load(dst[n], lds + PG8_SB(b, h) + boff + n * 2048); } while (0)
; #define PG8_MMA(ai, bj, At, Bt) do { __builtin_amdgcn_s_setprio(3); _Pragma("unroll") for (int m = 0; m < 4; ++m) _Pragma("unroll") for (int n = 0; n < 2; ++n) Frag<F8>::mma(acc[ai][bj][m][n], Bt[n], At[m]); \
;         __builtin_amdgcn_s_setprio(0); } while (0)
; #define PG8_WAIT_V(n) asm volatile("s_waitcnt vmcnt(" #n ")" ::: "memory")
; #define PG8_WAIT_L(n) asm volatile("s_waitcnt lgkmcnt(" #n ")" ::: "memory")
; #define PG8_BAR __builtin_amdgcn_s_barrier()
; #define PG8_SCHED __builtin_amdgcn_sched_barrier(0)
; template <class Epi, class Sched, bool ALIGN_EPI = false, bool SP2 = false, bool F8 = false>
; __device__ __forceinline__ void gemm_phase(PG8_LAS unsigned char* lds, const Gemm g, const Sched& S, const Epi& E) {
;     ...
;             PG8_LDB(B0, 1, 0); PG8_LDB(B1, 1, 1); PG8_SCHED; PG8_LDA(At, 1, 0); PG8_STAGE(PG8_SA(0, 1), a2 + hstep, voffA);
;             PG8_WAIT_V(8); PG8_WAIT_L(0); PG8_BAR; PG8_MMA(0, 0, At, B0); PG8_MMA(0, 1, At, B1); PG8_BAR; PG8_SCHED;
;             PG8_LDA(At, 1, 1); PG8_STAGE(PG8_SB(1, 0), b3, voffB); PG8_STAGE(PG8_SB(1, 1), b3 + hstep, voffB); PG8_STAGE(PG8_SA(1, 0), a3, voffA);
;             PG8_WAIT_V(8); PG8_WAIT_L(0); PG8_BAR; PG8_MMA(1, 0, At, B0); PG8_MMA(1, 1, At, B1); PG8_BAR; PG8_SCHED;
	s_add_i32 s0, s87, s76
	v_lshl_add_u64 v[182:183], s[72:73], 0, v[170:171]
	s_mov_b32 m0, s0
	ds_read_b128 v[200:203], v196 offset:16384
	ds_read_b128 v[204:207], v196 offset:17408
	ds_read_b128 v[208:211], v196 offset:18432
	ds_read_b128 v[212:215], v196 offset:19456
	ds_read_b128 v[216:219], v196 offset:20480
	ds_read_b128 v[220:223], v196 offset:21504
	ds_read_b128 v[224:227], v196 offset:22528
	ds_read_b128 v[228:231], v196 offset:23552
	global_load_lds_dwordx4 v[182:183], off
	s_add_i32 m0, s0, 0x2000
	s_add_u32 s4, s72, 0x20000
	v_lshl_add_u64 v[184:185], s[72:73], 0, v[166:167]
	s_addc_u32 s5, s73, 0
	s_add_i32 s0, s88, s76
	global_load_lds_dwordx4 v[184:185], off
	v_lshl_add_u64 v[186:187], s[4:5], 0, v[170:171]
	s_mov_b32 m0, s0
	v_lshl_add_u64 v[188:189], s[74:75], 0, v[168:169]
	global_load_lds_dwordx4 v[186:187], off
	v_lshl_add_u64 v[186:187], s[4:5], 0, v[166:167]
	s_add_i32 m0, s0, 0x2000
	s_nop 0
	global_load_lds_dwordx4 v[186:187], off
	v_lshl_add_u64 v[186:187], s[74:75], 0, v[172:173]
	s_mov_b32 m0, s45
	s_nop 0
	global_load_lds_dwordx4 v[186:187], off
	s_mov_b32 m0, s82
	s_nop 0
	global_load_lds_dwordx4 v[188:189], off
	s_waitcnt vmcnt(8)
	s_waitcnt lgkmcnt(0)
	s_barrier
	s_setprio 3
	v_mfma_f32_16x16x128_f8f6f4 v[94:97], v[18:25], v[200:207], v[94:97]
	v_mfma_f32_16x16x128_f8f6f4 v[90:93], v[26:33], v[200:207], v[90:93]
	v_mfma_f32_16x16x128_f8f6f4 v[86:89], v[18:25], v[208:215], v[86:89]
	v_mfma_f32_16x16x128_f8f6f4 v[82:85], v[26:33], v[208:215], v[82:85]
	v_mfma_f32_16x16x128_f8f6f4 v[70:73], v[18:25], v[216:223], v[70:73]
	v_mfma_f32_16x16x128_f8f6f4 v[66:69], v[26:33], v[216:223], v[66:69]
	v_mfma_f32_16x16x128_f8f6f4 v[54:57], v[18:25], v[224:231], v[54:57]
	v_mfma_f32_16x16x128_f8f6f4 v[50:53], v[26:33], v[224:231], v[50:53]
	v_mfma_f32_16x16x128_f8f6f4 v[78:81], v[2:9], v[200:207], v[78:81]
	v_mfma_f32_16x16x128_f8f6f4 v[74:77], v[10:17], v[200:207], v[74:77]
	v_mfma_f32_16x16x128_f8f6f4 v[62:65], v[2:9], v[208:215], v[62:65]
	v_mfma_f32_16x16x128_f8f6f4 v[58:61], v[10:17], v[208:215], v[58:61]
	v_mfma_f32_16x16x128_f8f6f4 v[46:49], v[2:9], v[216:223], v[46:49]
	v_mfma_f32_16x16x128_f8f6f4 v[42:45], v[10:17], v[216:223], v[42:45]
	v_mfma_f32_16x16x128_f8f6f4 v[38:41], v[2:9], v[224:231], v[38:41]
	v_mfma_f32_16x16x128_f8f6f4 v[34:37], v[10:17], v[224:231], v[34:37]
	s_setprio 0
	s_barrier
	s_add_i32 s0, 0, 0x18000
	s_add_i32 s1, 0, 0x1c000
	v_add_u32_e32 v14, s0, v190
	v_add_u32_e32 v30, s1, v190
	ds_read_b128 v[2:5], v14
	ds_read_b128 v[6:9], v14 offset:1024
	ds_read_b128 v[10:13], v14 offset:2048
	ds_read_b128 v[14:17], v14 offset:3072
	ds_read_b128 v[18:21], v30
	ds_read_b128 v[22:25], v30 offset:1024
	ds_read_b128 v[26:29], v30 offset:2048
	ds_read_b128 v[30:33], v30 offset:3072
	s_add_u32 s4, s74, 0x20000
	s_addc_u32 s5, s75, 0
	s_mov_b32 m0, s83
	v_lshl_add_u64 v[232:233], s[4:5], 0, v[172:173]
	ds_read_b128 v[200:203], v196 offset:32768
	ds_read_b128 v[204:207], v196 offset:33792
	ds_read_b128 v[208:211], v196 offset:34816
	ds_read_b128 v[212:215], v196 offset:35840
	ds_read_b128 v[216:219], v196 offset:36864
	ds_read_b128 v[220:223], v196 offset:37888
	ds_read_b128 v[224:227], v196 offset:38912
	ds_read_b128 v[228:231], v196 offset:39936
	global_load_lds_dwordx4 v[232:233], off
	v_lshl_add_u64 v[232:233], s[4:5], 0, v[168:169]
	s_mov_b32 m0, s84
	s_nop 0
	global_load_lds_dwordx4 v[232:233], off
	s_waitcnt vmcnt(8)
	s_waitcnt lgkmcnt(0)
	s_barrier
; #define PG8_STAGE(bufoff, gbase, voff) do { _Pragma("unroll") for (int _i = 0; _i < 2; ++_i) \
;         __builtin_amdgcn_global_load_lds((const unsigned*)((const char*)(gbase) + (voff)[_i]), (PG8_LAS unsigned*)(lds + (bufoff) + ldsw + _i * 8192), 16, 0, 0); } while (0)
; #define PG8_LDA(dst, b, h) do { _Pragma("unroll") for (int m = 0; m < 4; ++m) Frag<F8>::load(dst[m], lds + PG8_SA(b, h) + aoff + m * 2048); } while (0)
; #define PG8_MMA(ai, bj, At, Bt) do { __builtin_amdgcn_s_setprio(3); _Pragma("unroll") for (int m = 0; m < 4; ++m) _Pragma("unroll") for (int n = 0; n < 2; ++n) Frag<F8>::mma(acc[ai][bj][m][n], Bt[n], At[m]); \
;         __builtin_amdgcn_s_setprio(0); } while (0)
; #define PG8_WAIT_V(n) asm volatile("s_waitcnt vmcnt(" #n ")" ::: "memory")
; #define PG8_WAIT_L(n) asm volatile("s_waitcnt lgkmcnt(" #n ")" ::: "memory")
; #define PG8_BAR __builtin_amdgcn_s_barrier()
; #define PG8_SCHED __builtin_amdgcn_sched_barrier(0)
; template <class Epi, class Sched, bool ALIGN_EPI = false, bool SP2 = false, bool F8 = false>
; __device__ __forceinline__ void gemm_phase(PG8_LAS unsigned char* lds, const Gemm g, const Sched& S, const Epi& E) {
;     ...
;         for (int t = 0; t < nt; t += 2) {
;     ...
;             PG8_LDA(At, 1, 1); PG8_STAGE(PG8_SB(1, 0), b3, voffB); PG8_STAGE(PG8_SB(1, 1), b3 + hstep, voffB); PG8_STAGE(PG8_SA(1, 0), a3, voffA);
;             PG8_WAIT_V(8); PG8_WAIT_L(0); PG8_BAR; PG8_MMA(1, 0, At, B0); PG8_MMA(1, 1, At, B1); PG8_BAR; PG8_SCHED;
	s_setprio 3
	v_mfma_f32_16x16x128_f8f6f4 v[158:161], v[2:9], v[200:207], v[158:161]
	v_mfma_f32_16x16x128_f8f6f4 v[154:157], v[10:17], v[200:207], v[154:157]
	v_mfma_f32_16x16x128_f8f6f4 v[150:153], v[2:9], v[208:215], v[150:153]
	v_mfma_f32_16x16x128_f8f6f4 v[142:145], v[10:17], v[208:215], v[142:145]
	v_mfma_f32_16x16x128_f8f6f4 v[130:133], v[2:9], v[216:223], v[130:133]
	v_mfma_f32_16x16x128_f8f6f4 v[122:125], v[10:17], v[216:223], v[122:125]
	v_mfma_f32_16x16x128_f8f6f4 v[118:121], v[2:9], v[224:231], v[118:121]
	v_mfma_f32_16x16x128_f8f6f4 v[110:113], v[10:17], v[224:231], v[110:113]
	v_mfma_f32_16x16x128_f8f6f4 v[146:149], v[18:25], v[200:207], v[146:149]
	v_mfma_f32_16x16x128_f8f6f4 v[138:141], v[26:33], v[200:207], v[138:141]
	v_mfma_f32_16x16x128_f8f6f4 v[134:137], v[18:25], v[208:215], v[134:137]
	v_mfma_f32_16x16x128_f8f6f4 v[126:129], v[26:33], v[208:215], v[126:129]
	v_mfma_f32_16x16x128_f8f6f4 v[114:117], v[18:25], v[216:223], v[114:117]
	v_mfma_f32_16x16x128_f8f6f4 v[106:109], v[26:33], v[216:223], v[106:109]
	v_mfma_f32_16x16x128_f8f6f4 v[102:105], v[18:25], v[224:231], v[102:105]
	v_mfma_f32_16x16x128_f8f6f4 v[98:101], v[26:33], v[224:231], v[98:101]
	s_setprio 0
	s_barrier
	s_add_i32 s0, s0, s76
	v_lshl_add_u64 v[182:183], v[182:183], 0, s[18:19]
	s_mov_b32 m0, s0
	ds_read_b128 v[200:203], v196 offset:49152
	ds_read_b128 v[204:207], v196 offset:50176
	ds_read_b128 v[208:211], v196 offset:51200
	ds_read_b128 v[212:215], v196 offset:52224
	ds_read_b128 v[216:219], v196 offset:53248
	ds_read_b128 v[220:223], v196 offset:54272
	ds_read_b128 v[224:227], v196 offset:55296
	ds_read_b128 v[228:231], v196 offset:56320
	global_load_lds_dwordx4 v[182:183], off
	s_add_i32 m0, s0, 0x2000
	s_add_u32 s4, s72, 0x20080
	v_lshl_add_u64 v[182:183], v[184:185], 0, s[18:19]
	s_addc_u32 s5, s73, 0
	s_add_i32 s0, s1, s76
	global_load_lds_dwordx4 v[182:183], off
	v_lshl_add_u64 v[182:183], s[4:5], 0, v[170:171]
	s_mov_b32 m0, s0
	s_nop 0
	global_load_lds_dwordx4 v[182:183], off
	v_lshl_add_u64 v[182:183], s[4:5], 0, v[166:167]
	s_add_i32 m0, s0, 0x2000
	s_nop 0
	global_load_lds_dwordx4 v[182:183], off
	v_lshl_add_u64 v[182:183], v[186:187], 0, s[18:19]
	s_mov_b32 m0, s85
	s_nop 0
	global_load_lds_dwordx4 v[182:183], off
	v_lshl_add_u64 v[182:183], v[188:189], 0, s[18:19]
	s_mov_b32 m0, s86
	s_nop 0
	global_load_lds_dwordx4 v[182:183], off
	s_waitcnt vmcnt(8)
	s_waitcnt lgkmcnt(0)
	s_barrier
	s_setprio 3
	v_mfma_f32_16x16x128_f8f6f4 v[94:97], v[2:9], v[200:207], v[94:97]
	v_mfma_f32_16x16x128_f8f6f4 v[90:93], v[10:17], v[200:207], v[90:93]
	v_mfma_f32_16x16x128_f8f6f4 v[86:89], v[2:9], v[208:215], v[86:89]
	v_mfma_f32_16x16x128_f8f6f4 v[82:85], v[10:17], v[208:215], v[82:85]
	v_mfma_f32_16x16x128_f8f6f4 v[70:73], v[2:9], v[216:223], v[70:73]
	v_mfma_f32_16x16x128_f8f6f4 v[66:69], v[10:17], v[216:223], v[66:69]
	v_mfma_f32_16x16x128_f8f6f4 v[54:57], v[2:9], v[224:231], v[54:57]
	v_mfma_f32_16x16x128_f8f6f4 v[50:53], v[10:17], v[224:231], v[50:53]
	v_mfma_f32_16x16x128_f8f6f4 v[78:81], v[18:25], v[200:207], v[78:81]
	v_mfma_f32_16x16x128_f8f6f4 v[74:77], v[26:33], v[200:207], v[74:77]
	v_mfma_f32_16x16x128_f8f6f4 v[62:65], v[18:25], v[208:215], v[62:65]
	v_mfma_f32_16x16x128_f8f6f4 v[58:61], v[26:33], v[208:215], v[58:61]
	v_mfma_f32_16x16x128_f8f6f4 v[46:49], v[18:25], v[216:223], v[46:49]
	v_mfma_f32_16x16x128_f8f6f4 v[42:45], v[26:33], v[216:223], v[42:45]
	v_mfma_f32_16x16x128_f8f6f4 v[38:41], v[18:25], v[224:231], v[38:41]
	v_mfma_f32_16x16x128_f8f6f4 v[34:37], v[26:33], v[224:231], v[34:37]
	s_setprio 0
	s_barrier
	s_add_i32 s96, s96, 2
	s_add_u32 s70, s70, 0x100
	s_addc_u32 s71, s71, 0
	s_add_u32 s93, s93, 0x100
	s_addc_u32 s95, s95, 0
	s_cmp_gt_u32 s96, 5
	s_cbranch_scc0 .LBB0_151

; #define PG8_STAGE(bufoff, gbase, voff) do { _Pragma("unroll") for (int _i = 0; _i < 2; ++_i) \
;         __builtin_amdgcn_global_load_lds((const unsigned*)((const char*)(gbase) + (voff)[_i]), (PG8_LAS unsigned*)(lds + (bufoff) + ldsw + _i * 8192), 16, 0, 0); } while (0)
; #define PG8_LDA(dst, b, h) do { _Pragma("unroll") for (int m = 0; m < 4; ++m) Frag<F8>::load(dst[m], lds + PG8_SA(b, h) + aoff + m * 2048); } while (0)
; #define PG8_LDB(dst, b, h) do { _Pragma("unroll") for (int n = 0; n < 2; ++n) Frag<F8>::load(dst[n], lds + PG8_SB(b, h) + boff + n * 2048); } while (0)
; #define PG8_MMA(ai, bj, At, Bt) do { __builtin_amdgcn_s_setprio(3); _Pragma("unroll") for (int m = 0; m < 4; ++m) _Pragma("unroll") for (int n = 0; n < 2; ++n) Frag<F8>::mma(acc[ai][bj][m][n], Bt[n], At[m]); \
;         __builtin_amdgcn_s_setprio(0); } while (0)
; #define PG8_WAIT_V(n) asm volatile("s_waitcnt vmcnt(" #n ")" ::: "memory")
; #define PG8_WAIT_L(n) asm volatile("s_waitcnt lgkmcnt(" #n ")" ::: "memory")
; #define PG8_BAR __builtin_amdgcn_s_barrier()
; #define PG8_SCHED __builtin_amdgcn_sched_barrier(0)
; template <class Epi, class Sched, bool ALIGN_EPI = false, bool SP2 = false, bool F8 = false>
; __device__ __forceinline__ void gemm_phase(PG8_LAS unsigned char* lds, const Gemm g, const Sched& S, const Epi& E) {
;     ...
;             PG8_LDB(B0, 0, 0); PG8_LDB(B1, 0, 1); PG8_SCHED; PG8_LDA(At, 0, 0); PG8_STAGE(PG8_SA(1, 1), a1 + hstep, voffA);
;             PG8_WAIT_V(8); PG8_WAIT_L(0); PG8_BAR; PG8_MMA(0, 0, At, B0); PG8_MMA(0, 1, At, B1); PG8_BAR; PG8_SCHED;
;             PG8_LDA(At, 0, 1); PG8_STAGE(PG8_SB(0, 0), b2, voffB); PG8_STAGE(PG8_SB(0, 1), b2 + hstep, voffB); PG8_STAGE(PG8_SA(0, 0), a2, voffA);
;             PG8_WAIT_V(8); PG8_WAIT_L(0); PG8_BAR; PG8_MMA(1, 0, At, B0); PG8_MMA(1, 1, At, B1); PG8_BAR; PG8_SCHED;
;             PG8_LDB(B0, 1, 0); PG8_LDB(B1, 1, 1); PG8_SCHED; PG8_LDA(At, 1, 0); PG8_STAGE(PG8_SA(0, 1), a2 + hstep, voffA);
;             PG8_WAIT_V(8); PG8_WAIT_L(0); PG8_BAR; PG8_MMA(0, 0, At, B0); PG8_MMA(0, 1, At, B1); PG8_BAR; PG8_SCHED;
;             PG8_LDA(At, 1, 1); PG8_STAGE(PG8_SB(1, 0), b3, voffB); PG8_STAGE(PG8_SB(1, 1), b3 + hstep, voffB); PG8_STAGE(PG8_SA(1, 0), a3, voffA);
;             PG8_WAIT_V(8); PG8_WAIT_L(0); PG8_BAR; PG8_MMA(1, 0, At, B0); PG8_MMA(1, 1, At, B1); PG8_BAR; PG8_SCHED;
.LBB0_162:
	ds_read_b128 v[18:21], v167
	ds_read_b128 v[22:25], v167 offset:1024
	ds_read_b128 v[26:29], v167 offset:2048
	ds_read_b128 v[30:33], v167 offset:3072
	ds_read_b128 v[2:5], v188
	ds_read_b128 v[6:9], v188 offset:1024
	ds_read_b128 v[10:13], v188 offset:2048
	ds_read_b128 v[14:17], v188 offset:3072
	s_add_u32 s0, s16, 0x100100
	s_addc_u32 s1, s17, 0
	s_add_u32 s3, s16, s45
	s_addc_u32 s4, s17, s70
	s_cmp_eq_u32 s71, 4
	s_cselect_b32 s23, s9, s1
	s_cselect_b32 s22, s8, s0
	s_cselect_b32 s19, s13, s4
	s_cselect_b32 s18, s12, s3
	s_mov_b32 m0, s72
	v_lshl_add_u64 v[218:219], s[16:17], 0, v[176:177]
	ds_read_b128 v[180:183], v189
	ds_read_b128 v[184:187], v189 offset:1024
	ds_read_b128 v[194:197], v189 offset:2048
	ds_read_b128 v[198:201], v189 offset:3072
	ds_read_b128 v[202:205], v189 offset:4096
	ds_read_b128 v[206:209], v189 offset:5120
	ds_read_b128 v[210:213], v189 offset:6144
	ds_read_b128 v[214:217], v189 offset:7168
	global_load_lds_dwordx4 v[218:219], off
	v_lshl_add_u64 v[218:219], s[16:17], 0, v[178:179]
	s_mov_b32 m0, s73
	s_nop 0
	global_load_lds_dwordx4 v[218:219], off
	s_waitcnt vmcnt(8)
	s_waitcnt lgkmcnt(0)
	s_barrier
	s_setprio 3
	v_mfma_f32_16x16x128_f8f6f4 v[158:161], v[18:25], v[180:187], v[158:161]
	v_mfma_f32_16x16x128_f8f6f4 v[154:157], v[26:33], v[180:187], v[154:157]
	v_mfma_f32_16x16x128_f8f6f4 v[150:153], v[18:25], v[194:201], v[150:153]
	v_mfma_f32_16x16x128_f8f6f4 v[142:145], v[26:33], v[194:201], v[142:145]
	v_mfma_f32_16x16x128_f8f6f4 v[134:137], v[18:25], v[202:209], v[134:137]
	v_mfma_f32_16x16x128_f8f6f4 v[126:129], v[26:33], v[202:209], v[126:129]
	v_mfma_f32_16x16x128_f8f6f4 v[118:121], v[18:25], v[210:217], v[118:121]
	v_mfma_f32_16x16x128_f8f6f4 v[110:113], v[26:33], v[210:217], v[110:113]
	v_mfma_f32_16x16x128_f8f6f4 v[146:149], v[2:9], v[180:187], v[146:149]
	v_mfma_f32_16x16x128_f8f6f4 v[138:141], v[10:17], v[180:187], v[138:141]
	v_mfma_f32_16x16x128_f8f6f4 v[130:133], v[2:9], v[194:201], v[130:133]
	v_mfma_f32_16x16x128_f8f6f4 v[122:125], v[10:17], v[194:201], v[122:125]
	v_mfma_f32_16x16x128_f8f6f4 v[114:117], v[2:9], v[202:209], v[114:117]
	v_mfma_f32_16x16x128_f8f6f4 v[106:109], v[10:17], v[202:209], v[106:109]
	v_mfma_f32_16x16x128_f8f6f4 v[102:105], v[2:9], v[210:217], v[102:105]
	v_mfma_f32_16x16x128_f8f6f4 v[98:101], v[10:17], v[210:217], v[98:101]
	s_setprio 0
	s_barrier
	s_mov_b32 m0, s74
	v_lshl_add_u64 v[180:181], s[18:19], 0, v[172:173]
	s_add_u32 s4, s18, 0x20000
	ds_read_b128 v[194:197], v189 offset:16384
	ds_read_b128 v[198:201], v189 offset:17408
	ds_read_b128 v[202:205], v189 offset:18432
	ds_read_b128 v[206:209], v189 offset:19456
	ds_read_b128 v[210:213], v189 offset:20480
	ds_read_b128 v[214:217], v189 offset:21504
	ds_read_b128 v[218:221], v189 offset:22528
	ds_read_b128 v[222:225], v189 offset:23552
	global_load_lds_dwordx4 v[180:181], off
	v_lshl_add_u64 v[182:183], s[18:19], 0, v[168:169]
	s_mov_b32 m0, s75
	s_addc_u32 s5, s19, 0
	global_load_lds_dwordx4 v[182:183], off
	v_lshl_add_u64 v[184:185], s[4:5], 0, v[172:173]
	s_mov_b32 m0, s76
	v_lshl_add_u64 v[186:187], s[22:23], 0, v[170:171]
	global_load_lds_dwordx4 v[184:185], off
	v_lshl_add_u64 v[184:185], s[4:5], 0, v[168:169]
	s_mov_b32 m0, s77
	s_nop 0
	global_load_lds_dwordx4 v[184:185], off
	v_lshl_add_u64 v[184:185], s[22:23], 0, v[174:175]
	s_mov_b32 m0, s30
	s_nop 0
	global_load_lds_dwordx4 v[184:185], off
	s_mov_b32 m0, s31
	s_nop 0
	global_load_lds_dwordx4 v[186:187], off
	s_waitcnt vmcnt(8)
	s_waitcnt lgkmcnt(0)
	s_barrier
	s_setprio 3
	v_mfma_f32_16x16x128_f8f6f4 v[94:97], v[18:25], v[194:201], v[94:97]
	v_mfma_f32_16x16x128_f8f6f4 v[90:93], v[26:33], v[194:201], v[90:93]
	v_mfma_f32_16x16x128_f8f6f4 v[86:89], v[18:25], v[202:209], v[86:89]
	v_mfma_f32_16x16x128_f8f6f4 v[78:81], v[26:33], v[202:209], v[78:81]
	v_mfma_f32_16x16x128_f8f6f4 v[70:73], v[18:25], v[210:217], v[70:73]
	v_mfma_f32_16x16x128_f8f6f4 v[62:65], v[26:33], v[210:217], v[62:65]
	v_mfma_f32_16x16x128_f8f6f4 v[54:57], v[18:25], v[218:225], v[54:57]
	v_mfma_f32_16x16x128_f8f6f4 v[46:49], v[26:33], v[218:225], v[46:49]
	v_mfma_f32_16x16x128_f8f6f4 v[82:85], v[2:9], v[194:201], v[82:85]
	v_mfma_f32_16x16x128_f8f6f4 v[74:77], v[10:17], v[194:201], v[74:77]
	v_mfma_f32_16x16x128_f8f6f4 v[66:69], v[2:9], v[202:209], v[66:69]
	v_mfma_f32_16x16x128_f8f6f4 v[58:61], v[10:17], v[202:209], v[58:61]
	v_mfma_f32_16x16x128_f8f6f4 v[50:53], v[2:9], v[210:217], v[50:53]
	v_mfma_f32_16x16x128_f8f6f4 v[42:45], v[10:17], v[210:217], v[42:45]
	v_mfma_f32_16x16x128_f8f6f4 v[38:41], v[2:9], v[218:225], v[38:41]
	v_mfma_f32_16x16x128_f8f6f4 v[34:37], v[10:17], v[218:225], v[34:37]
	s_setprio 0
	s_barrier
; #define PG8_STAGE(bufoff, gbase, voff) do { _Pragma("unroll") for (int _i = 0; _i < 2; ++_i) \
;         __builtin_amdgcn_global_load_lds((const unsigned*)((const char*)(gbase) + (voff)[_i]), (PG8_LAS unsigned*)(lds + (bufoff) + ldsw + _i * 8192), 16, 0, 0); } while (0)
; #define PG8_BAR __builtin_amdgcn_s_barrier()
; template <class Epi, class Sched, bool ALIGN_EPI = false, bool SP2 = false, bool F8 = false>
; __device__ __forceinline__ void gemm_phase(PG8_LAS unsigned char* lds, const Gemm g, const Sched& S, const Epi& E) {
;     ...
;             PG8_LDB(B0, 1, 0); PG8_LDB(B1, 1, 1); PG8_SCHED; PG8_LDA(At, 1, 0); PG8_STAGE(PG8_SA(0, 1), a2 + hstep, voffA);
;             PG8_WAIT_V(8); PG8_WAIT_L(0); PG8_BAR; PG8_MMA(0, 0, At, B0); PG8_MMA(0, 1, At, B1); PG8_BAR; PG8_SCHED;
;             PG8_LDA(At, 1, 1); PG8_STAGE(PG8_SB(1, 0), b3, voffB); PG8_STAGE(PG8_SB(1, 1), b3 + hstep, voffB); PG8_STAGE(PG8_SA(1, 0), a3, voffA);
;             PG8_WAIT_V(8); PG8_WAIT_L(0); PG8_BAR; PG8_MMA(1, 0, At, B0); PG8_MMA(1, 1, At, B1); PG8_BAR; PG8_SCHED;
;             } else {
;             PG8_LDB(B0, 0, 0); PG8_SCHED; PG8_LDA(At, 0, 0); PG8_STAGE(PG8_SA(1, 1), a1 + hstep, voffA);
;             PG8_WAIT_L(8); PG8_BAR; PG8_WAIT_L(0); PG8_MMA(0, 0, At, B0); PG8_BAR; PG8_SCHED;
;             PG8_LDB(B1, 0, 1); PG8_STAGE(PG8_SB(0, 0), b2, voffB);
;             PG8_BAR; PG8_WAIT_L(0); PG8_MMA(0, 1, At, B1); PG8_BAR;
;             PG8_LDA(At, 0, 1); PG8_STAGE(PG8_SA(0, 0), a2, voffA);
;             PG8_BAR; PG8_WAIT_L(0); PG8_MMA(1, 0, At, B0); PG8_BAR; PG8_SCHED;
;             PG8_STAGE(PG8_SB(0, 1), b2 + hstep, voffB);
;             PG8_WAIT_V(6); PG8_BAR; PG8_MMA(1, 1, At, B1); PG8_BAR;
;             PG8_LDB(B0, 1, 0); PG8_SCHED; PG8_LDA(At, 1, 0); PG8_STAGE(PG8_SA(0, 1), a2 + hstep, voffA);
;             PG8_WAIT_L(8); PG8_BAR; PG8_WAIT_L(0); PG8_MMA(0, 0, At, B0); PG8_BAR; PG8_SCHED;
;             PG8_LDB(B1, 1, 1); PG8_STAGE(PG8_SB(1, 0), b3, voffB);
;             PG8_BAR; PG8_WAIT_L(0); PG8_MMA(0, 1, At, B1); PG8_BAR;
;             PG8_LDA(At, 1, 1); PG8_STAGE(PG8_SA(1, 0), a3, voffA);
;             PG8_BAR; PG8_WAIT_L(0); PG8_MMA(1, 0, At, B0); PG8_BAR; PG8_SCHED;
;             PG8_STAGE(PG8_SB(1, 1), b3 + hstep, voffB);
;             PG8_WAIT_V(6); PG8_BAR; PG8_MMA(1, 1, At, B1); PG8_BAR;
;             }
;         }
;         if constexpr (ALIGN_EPI) { if (wr == 0) PG8_BAR; }
	ds_read_b128 v[2:5], v191
	ds_read_b128 v[6:9], v191 offset:1024
	ds_read_b128 v[10:13], v191 offset:2048
	ds_read_b128 v[14:17], v191 offset:3072
	ds_read_b128 v[18:21], v192
	ds_read_b128 v[22:25], v192 offset:1024
	ds_read_b128 v[26:29], v192 offset:2048
	ds_read_b128 v[30:33], v192 offset:3072
	s_add_u32 s4, s22, 0x20000
	s_addc_u32 s5, s23, 0
	s_mov_b32 m0, s38
	v_lshl_add_u64 v[226:227], s[4:5], 0, v[174:175]
	ds_read_b128 v[194:197], v189 offset:32768
	ds_read_b128 v[198:201], v189 offset:33792
	ds_read_b128 v[202:205], v189 offset:34816
	ds_read_b128 v[206:209], v189 offset:35840
	ds_read_b128 v[210:213], v189 offset:36864
	ds_read_b128 v[214:217], v189 offset:37888
	ds_read_b128 v[218:221], v189 offset:38912
	ds_read_b128 v[222:225], v189 offset:39936
	global_load_lds_dwordx4 v[226:227], off
	v_lshl_add_u64 v[226:227], s[4:5], 0, v[170:171]
	s_mov_b32 m0, s39
	s_nop 0
	global_load_lds_dwordx4 v[226:227], off
	s_waitcnt vmcnt(8)
	s_waitcnt lgkmcnt(0)
	s_barrier
	s_setprio 3
	v_mfma_f32_16x16x128_f8f6f4 v[158:161], v[2:9], v[194:201], v[158:161]
	v_mfma_f32_16x16x128_f8f6f4 v[154:157], v[10:17], v[194:201], v[154:157]
	v_mfma_f32_16x16x128_f8f6f4 v[150:153], v[2:9], v[202:209], v[150:153]
	v_mfma_f32_16x16x128_f8f6f4 v[142:145], v[10:17], v[202:209], v[142:145]
	v_mfma_f32_16x16x128_f8f6f4 v[134:137], v[2:9], v[210:217], v[134:137]
	v_mfma_f32_16x16x128_f8f6f4 v[126:129], v[10:17], v[210:217], v[126:129]
	v_mfma_f32_16x16x128_f8f6f4 v[118:121], v[2:9], v[218:225], v[118:121]
	v_mfma_f32_16x16x128_f8f6f4 v[110:113], v[10:17], v[218:225], v[110:113]
	v_mfma_f32_16x16x128_f8f6f4 v[146:149], v[18:25], v[194:201], v[146:149]
	v_mfma_f32_16x16x128_f8f6f4 v[138:141], v[26:33], v[194:201], v[138:141]
	v_mfma_f32_16x16x128_f8f6f4 v[130:133], v[18:25], v[202:209], v[130:133]
	v_mfma_f32_16x16x128_f8f6f4 v[122:125], v[26:33], v[202:209], v[122:125]
	v_mfma_f32_16x16x128_f8f6f4 v[114:117], v[18:25], v[210:217], v[114:117]
	v_mfma_f32_16x16x128_f8f6f4 v[106:109], v[26:33], v[210:217], v[106:109]
	v_mfma_f32_16x16x128_f8f6f4 v[102:105], v[18:25], v[218:225], v[102:105]
	v_mfma_f32_16x16x128_f8f6f4 v[98:101], v[26:33], v[218:225], v[98:101]
	s_setprio 0
	s_barrier
	s_mov_b32 m0, s78
	v_lshl_add_u64 v[180:181], v[180:181], 0, s[14:15]
	s_add_u32 s4, s18, 0x20080
	ds_read_b128 v[194:197], v189 offset:49152
	ds_read_b128 v[198:201], v189 offset:50176
	ds_read_b128 v[202:205], v189 offset:51200
	ds_read_b128 v[206:209], v189 offset:52224
	ds_read_b128 v[210:213], v189 offset:53248
	ds_read_b128 v[214:217], v189 offset:54272
	ds_read_b128 v[218:221], v189 offset:55296
	ds_read_b128 v[222:225], v189 offset:56320
	global_load_lds_dwordx4 v[180:181], off
	v_lshl_add_u64 v[180:181], v[182:183], 0, s[14:15]
	s_mov_b32 m0, s79
	s_addc_u32 s5, s19, 0
	global_load_lds_dwordx4 v[180:181], off
	v_lshl_add_u64 v[180:181], s[4:5], 0, v[172:173]
	s_mov_b32 m0, s80
	s_nop 0
	global_load_lds_dwordx4 v[180:181], off
	v_lshl_add_u64 v[180:181], s[4:5], 0, v[168:169]
	s_mov_b32 m0, s81
	s_nop 0
	global_load_lds_dwordx4 v[180:181], off
	v_lshl_add_u64 v[180:181], v[184:185], 0, s[14:15]
	s_mov_b32 m0, s43
	s_nop 0
	global_load_lds_dwordx4 v[180:181], off
	v_lshl_add_u64 v[180:181], v[186:187], 0, s[14:15]
	s_mov_b32 m0, s44
	s_nop 0
	global_load_lds_dwordx4 v[180:181], off
	s_waitcnt vmcnt(8)
	s_waitcnt lgkmcnt(0)
	s_barrier
	s_setprio 3
	v_mfma_f32_16x16x128_f8f6f4 v[94:97], v[2:9], v[194:201], v[94:97]
	v_mfma_f32_16x16x128_f8f6f4 v[90:93], v[10:17], v[194:201], v[90:93]
	v_mfma_f32_16x16x128_f8f6f4 v[86:89], v[2:9], v[202:209], v[86:89]
	v_mfma_f32_16x16x128_f8f6f4 v[78:81], v[10:17], v[202:209], v[78:81]
	v_mfma_f32_16x16x128_f8f6f4 v[70:73], v[2:9], v[210:217], v[70:73]
	v_mfma_f32_16x16x128_f8f6f4 v[62:65], v[10:17], v[210:217], v[62:65]
	v_mfma_f32_16x16x128_f8f6f4 v[54:57], v[2:9], v[218:225], v[54:57]
	v_mfma_f32_16x16x128_f8f6f4 v[46:49], v[10:17], v[218:225], v[46:49]
	v_mfma_f32_16x16x128_f8f6f4 v[82:85], v[18:25], v[194:201], v[82:85]
	v_mfma_f32_16x16x128_f8f6f4 v[74:77], v[26:33], v[194:201], v[74:77]
	v_mfma_f32_16x16x128_f8f6f4 v[66:69], v[18:25], v[202:209], v[66:69]
	v_mfma_f32_16x16x128_f8f6f4 v[58:61], v[26:33], v[202:209], v[58:61]
	v_mfma_f32_16x16x128_f8f6f4 v[50:53], v[18:25], v[210:217], v[50:53]
	v_mfma_f32_16x16x128_f8f6f4 v[42:45], v[26:33], v[210:217], v[42:45]
	v_mfma_f32_16x16x128_f8f6f4 v[38:41], v[18:25], v[218:225], v[38:41]
	v_mfma_f32_16x16x128_f8f6f4 v[34:37], v[26:33], v[218:225], v[34:37]
	s_setprio 0
	s_barrier
	s_add_i32 s71, s71, 2
	s_add_u32 s16, s16, 0x100
	s_addc_u32 s17, s17, 0
	s_cmp_gt_u32 s71, 5
	s_cbranch_scc0 .LBB0_162
	s_cmpk_lt_u32 s25, 0x100
	s_cbranch_scc0 .LBB0_165
	s_barrier

; #define PG8_STAGE(bufoff, gbase, voff) do { _Pragma("unroll") for (int _i = 0; _i < 2; ++_i) \
;         __builtin_amdgcn_global_load_lds((const unsigned*)((const char*)(gbase) + (voff)[_i]), (PG8_LAS unsigned*)(lds + (bufoff) + ldsw + _i * 8192), 16, 0, 0); } while (0)
; #define PG8_LDA(dst, b, h) do { _Pragma("unroll") for (int m = 0; m < 4; ++m) Frag<F8>::load(dst[m], lds + PG8_SA(b, h) + aoff + m * 2048); } while (0)
; #define PG8_LDB(dst, b, h) do { _Pragma("unroll") for (int n = 0; n < 2; ++n) Frag<F8>::load(dst[n], lds + PG8_SB(b, h) + boff + n * 2048); } while (0)
; #define PG8_MMA(ai, bj, At, Bt) do { __builtin_amdgcn_s_setprio(3); _Pragma("unroll") for (int m = 0; m < 4; ++m) _Pragma("unroll") for (int n = 0; n < 2; ++n) Frag<F8>::mma(acc[ai][bj][m][n], Bt[n], At[m]); \
;         __builtin_amdgcn_s_setprio(0); } while (0)
; #define PG8_WAIT_V(n) asm volatile("s_waitcnt vmcnt(" #n ")" ::: "memory")
; #define PG8_WAIT_L(n) asm volatile("s_waitcnt lgkmcnt(" #n ")" ::: "memory")
; #define PG8_BAR __builtin_amdgcn_s_barrier()
; #define PG8_SCHED __builtin_amdgcn_sched_barrier(0)
; template <class Epi, class Sched, bool ALIGN_EPI = false, bool SP2 = false, bool F8 = false>
; __device__ __forceinline__ void gemm_phase(PG8_LAS unsigned char* lds, const Gemm g, const Sched& S, const Epi& E) {
;     ...
;         for (int t = 0; t < nt; t += 2) {
;             const bool last = (t == nt - 2);
;             const char* a1 = cA + (size_t)(t + 1) * kstep;
;             const char* a2 = last ? nA : cA + (size_t)(t + 2) * kstep; const char* b2 = last ? nB : cB + (size_t)(t + 2) * kstep;
;             const char* a3 = a2 + kstep; const char* b3 = b2 + kstep;
;             if (last && has_next) S.a_ready(nxt);
;             if constexpr (SP2) {
;             PG8_LDB(B0, 0, 0); PG8_LDB(B1, 0, 1); PG8_SCHED; PG8_LDA(At, 0, 0); PG8_STAGE(PG8_SA(1, 1), a1 + hstep, voffA);
;             PG8_WAIT_V(8); PG8_WAIT_L(0); PG8_BAR; PG8_MMA(0, 0, At, B0); PG8_MMA(0, 1, At, B1); PG8_BAR; PG8_SCHED;
;             PG8_LDA(At, 0, 1); PG8_STAGE(PG8_SB(0, 0), b2, voffB); PG8_STAGE(PG8_SB(0, 1), b2 + hstep, voffB); PG8_STAGE(PG8_SA(0, 0), a2, voffA);
;             PG8_WAIT_V(8); PG8_WAIT_L(0); PG8_BAR; PG8_MMA(1, 0, At, B0); PG8_MMA(1, 1, At, B1); PG8_BAR; PG8_SCHED;
.LBB0_437:
	v_add_u32_e32 v186, s90, v158
	v_add_u32_e32 v202, s91, v158
	s_add_u32 s0, s36, s70
	ds_read_b128 v[174:177], v186
	ds_read_b128 v[178:181], v186 offset:1024
	ds_read_b128 v[182:185], v186 offset:2048
	ds_read_b128 v[186:189], v186 offset:3072
	ds_read_b128 v[190:193], v202
	ds_read_b128 v[194:197], v202 offset:1024
	ds_read_b128 v[198:201], v202 offset:2048
	ds_read_b128 v[202:205], v202 offset:3072
	s_addc_u32 s1, s37, s71
	s_add_u32 s0, s0, 0x100
	s_addc_u32 s1, s1, 0
	s_add_u32 s23, s49, s70
	s_addc_u32 s33, s93, s71
	s_cmpk_eq_i32 s70, 0x700
	s_cselect_b32 s75, s3, s1
	s_cselect_b32 s74, s4, s0
	s_cselect_b32 s73, s5, s33
	s_cselect_b32 s72, s6, s23
	v_lshl_add_u64 v[238:239], v[146:147], 0, s[70:71]
	s_add_i32 m0, s19, 0xc000
	ds_read_b128 v[206:209], v160
	ds_read_b128 v[210:213], v160 offset:1024
	ds_read_b128 v[214:217], v160 offset:2048
	ds_read_b128 v[218:221], v160 offset:3072
	ds_read_b128 v[222:225], v160 offset:4096
	ds_read_b128 v[226:229], v160 offset:5120
	ds_read_b128 v[230:233], v160 offset:6144
	ds_read_b128 v[234:237], v160 offset:7168
	global_load_lds_dwordx4 v[238:239], off
	v_lshl_add_u64 v[238:239], v[148:149], 0, s[70:71]
	s_add_i32 m0, s19, 0xe000
	s_nop 0
	global_load_lds_dwordx4 v[238:239], off
	s_waitcnt vmcnt(8)
	s_waitcnt lgkmcnt(0)
	s_barrier
	s_setprio 3
	v_mfma_f32_16x16x32_bf16 v[22:25], v[174:177], v[206:209], v[22:25]
	v_mfma_f32_16x16x32_bf16 v[30:33], v[182:185], v[206:209], v[30:33]
	v_mfma_f32_16x16x32_bf16 v[46:49], v[174:177], v[214:217], v[46:49]
	v_mfma_f32_16x16x32_bf16 v[54:57], v[182:185], v[214:217], v[54:57]
	v_mfma_f32_16x16x32_bf16 v[78:81], v[174:177], v[222:225], v[78:81]
	v_mfma_f32_16x16x32_bf16 v[86:89], v[182:185], v[222:225], v[86:89]
	v_mfma_f32_16x16x32_bf16 v[98:101], v[174:177], v[230:233], v[98:101]
	v_mfma_f32_16x16x32_bf16 v[102:105], v[182:185], v[230:233], v[102:105]
	v_mfma_f32_16x16x32_bf16 v[22:25], v[178:181], v[210:213], v[22:25]
	v_mfma_f32_16x16x32_bf16 v[30:33], v[186:189], v[210:213], v[30:33]
	v_mfma_f32_16x16x32_bf16 v[46:49], v[178:181], v[218:221], v[46:49]
	v_mfma_f32_16x16x32_bf16 v[54:57], v[186:189], v[218:221], v[54:57]
	v_mfma_f32_16x16x32_bf16 v[78:81], v[178:181], v[226:229], v[78:81]
	v_mfma_f32_16x16x32_bf16 v[86:89], v[186:189], v[226:229], v[86:89]
	v_mfma_f32_16x16x32_bf16 v[98:101], v[178:181], v[234:237], v[98:101]
	v_mfma_f32_16x16x32_bf16 v[102:105], v[186:189], v[234:237], v[102:105]
	v_mfma_f32_16x16x32_bf16 v[2:5], v[190:193], v[206:209], v[2:5]
	v_mfma_f32_16x16x32_bf16 v[6:9], v[198:201], v[206:209], v[6:9]
	v_mfma_f32_16x16x32_bf16 v[10:13], v[190:193], v[214:217], v[10:13]
	v_mfma_f32_16x16x32_bf16 v[14:17], v[198:201], v[214:217], v[14:17]
	v_mfma_f32_16x16x32_bf16 v[34:37], v[190:193], v[222:225], v[34:37]
	v_mfma_f32_16x16x32_bf16 v[38:41], v[198:201], v[222:225], v[38:41]
	v_mfma_f32_16x16x32_bf16 v[58:61], v[190:193], v[230:233], v[58:61]
	v_mfma_f32_16x16x32_bf16 v[62:65], v[198:201], v[230:233], v[62:65]
	v_mfma_f32_16x16x32_bf16 v[2:5], v[194:197], v[210:213], v[2:5]
	v_mfma_f32_16x16x32_bf16 v[6:9], v[202:205], v[210:213], v[6:9]
	v_mfma_f32_16x16x32_bf16 v[10:13], v[194:197], v[218:221], v[10:13]
	v_mfma_f32_16x16x32_bf16 v[14:17], v[202:205], v[218:221], v[14:17]
	v_mfma_f32_16x16x32_bf16 v[34:37], v[194:197], v[226:229], v[34:37]
	v_mfma_f32_16x16x32_bf16 v[38:41], v[202:205], v[226:229], v[38:41]
	v_mfma_f32_16x16x32_bf16 v[58:61], v[194:197], v[234:237], v[58:61]
	v_mfma_f32_16x16x32_bf16 v[62:65], v[202:205], v[234:237], v[62:65]
	s_setprio 0
	s_barrier
	s_add_i32 s0, s90, s83
	v_lshl_add_u64 v[238:239], s[72:73], 0, v[132:133]
	s_mov_b32 m0, s0
	ds_read_b128 v[206:209], v160 offset:16384
	ds_read_b128 v[210:213], v160 offset:17408
	ds_read_b128 v[214:217], v160 offset:18432
	ds_read_b128 v[218:221], v160 offset:19456
	ds_read_b128 v[222:225], v160 offset:20480
	ds_read_b128 v[226:229], v160 offset:21504
	ds_read_b128 v[230:233], v160 offset:22528
	ds_read_b128 v[234:237], v160 offset:23552
	global_load_lds_dwordx4 v[238:239], off
	s_add_i32 m0, s0, 0x2000
	s_add_u32 s68, s72, 0x40000
	v_lshl_add_u64 v[240:241], s[72:73], 0, v[136:137]
	s_addc_u32 s69, s73, 0
	s_add_i32 s0, s91, s83
	global_load_lds_dwordx4 v[240:241], off
	v_lshl_add_u64 v[242:243], s[68:69], 0, v[132:133]
	s_mov_b32 m0, s0
	v_lshl_add_u64 v[244:245], s[74:75], 0, v[134:135]
	global_load_lds_dwordx4 v[242:243], off
	v_lshl_add_u64 v[242:243], s[68:69], 0, v[136:137]
	s_add_i32 m0, s0, 0x2000
	s_nop 0
	global_load_lds_dwordx4 v[242:243], off
	v_lshl_add_u64 v[242:243], s[74:75], 0, v[130:131]
	s_mov_b32 m0, s19
	s_nop 0
	global_load_lds_dwordx4 v[242:243], off
	s_mov_b32 m0, s84
	s_nop 0
	global_load_lds_dwordx4 v[244:245], off
	s_waitcnt vmcnt(8)
	s_waitcnt lgkmcnt(0)
	s_barrier
; #define PG8_STAGE(bufoff, gbase, voff) do { _Pragma("unroll") for (int _i = 0; _i < 2; ++_i) \
;         __builtin_amdgcn_global_load_lds((const unsigned*)((const char*)(gbase) + (voff)[_i]), (PG8_LAS unsigned*)(lds + (bufoff) + ldsw + _i * 8192), 16, 0, 0); } while (0)
; #define PG8_LDA(dst, b, h) do { _Pragma("unroll") for (int m = 0; m < 4; ++m) Frag<F8>::load(dst[m], lds + PG8_SA(b, h) + aoff + m * 2048); } while (0)
; #define PG8_LDB(dst, b, h) do { _Pragma("unroll") for (int n = 0; n < 2; ++n) Frag<F8>::load(dst[n], lds + PG8_SB(b, h) + boff + n * 2048); } while (0)
; #define PG8_MMA(ai, bj, At, Bt) do { __builtin_amdgcn_s_setprio(3); _Pragma("unroll") for (int m = 0; m < 4; ++m) _Pragma("unroll") for (int n = 0; n < 2; ++n) Frag<F8>::mma(acc[ai][bj][m][n], Bt[n], At[m]); \
;         __builtin_amdgcn_s_setprio(0); } while (0)
; #define PG8_WAIT_V(n) asm volatile("s_waitcnt vmcnt(" #n ")" ::: "memory")
; #define PG8_WAIT_L(n) asm volatile("s_waitcnt lgkmcnt(" #n ")" ::: "memory")
; #define PG8_BAR __builtin_amdgcn_s_barrier()
; #define PG8_SCHED __builtin_amdgcn_sched_barrier(0)
; template <class Epi, class Sched, bool ALIGN_EPI = false, bool SP2 = false, bool F8 = false>
; __device__ __forceinline__ void gemm_phase(PG8_LAS unsigned char* lds, const Gemm g, const Sched& S, const Epi& E) {
;     ...
;             PG8_WAIT_V(8); PG8_WAIT_L(0); PG8_BAR; PG8_MMA(1, 0, At, B0); PG8_MMA(1, 1, At, B1); PG8_BAR; PG8_SCHED;
;             PG8_LDB(B0, 1, 0); PG8_LDB(B1, 1, 1); PG8_SCHED; PG8_LDA(At, 1, 0); PG8_STAGE(PG8_SA(0, 1), a2 + hstep, voffA);
;             PG8_WAIT_V(8); PG8_WAIT_L(0); PG8_BAR; PG8_MMA(0, 0, At, B0); PG8_MMA(0, 1, At, B1); PG8_BAR; PG8_SCHED;
	s_setprio 3
	v_mfma_f32_16x16x32_bf16 v[66:69], v[174:177], v[206:209], v[66:69]
	v_mfma_f32_16x16x32_bf16 v[70:73], v[182:185], v[206:209], v[70:73]
	v_mfma_f32_16x16x32_bf16 v[90:93], v[174:177], v[214:217], v[90:93]
	v_mfma_f32_16x16x32_bf16 v[94:97], v[182:185], v[214:217], v[94:97]
	v_mfma_f32_16x16x32_bf16 v[106:109], v[174:177], v[222:225], v[106:109]
	v_mfma_f32_16x16x32_bf16 v[110:113], v[182:185], v[222:225], v[110:113]
	v_mfma_f32_16x16x32_bf16 v[114:117], v[174:177], v[230:233], v[114:117]
	v_mfma_f32_16x16x32_bf16 v[126:129], v[182:185], v[230:233], v[126:129]
	v_mfma_f32_16x16x32_bf16 v[66:69], v[178:181], v[210:213], v[66:69]
	v_mfma_f32_16x16x32_bf16 v[70:73], v[186:189], v[210:213], v[70:73]
	v_mfma_f32_16x16x32_bf16 v[90:93], v[178:181], v[218:221], v[90:93]
	v_mfma_f32_16x16x32_bf16 v[94:97], v[186:189], v[218:221], v[94:97]
	v_mfma_f32_16x16x32_bf16 v[106:109], v[178:181], v[226:229], v[106:109]
	v_mfma_f32_16x16x32_bf16 v[110:113], v[186:189], v[226:229], v[110:113]
	v_mfma_f32_16x16x32_bf16 v[114:117], v[178:181], v[234:237], v[114:117]
	v_mfma_f32_16x16x32_bf16 v[126:129], v[186:189], v[234:237], v[126:129]
	v_mfma_f32_16x16x32_bf16 v[18:21], v[190:193], v[206:209], v[18:21]
	v_mfma_f32_16x16x32_bf16 v[26:29], v[198:201], v[206:209], v[26:29]
	v_mfma_f32_16x16x32_bf16 v[42:45], v[190:193], v[214:217], v[42:45]
	v_mfma_f32_16x16x32_bf16 v[50:53], v[198:201], v[214:217], v[50:53]
	v_mfma_f32_16x16x32_bf16 v[74:77], v[190:193], v[222:225], v[74:77]
	v_mfma_f32_16x16x32_bf16 v[82:85], v[198:201], v[222:225], v[82:85]
	v_mfma_f32_16x16x32_bf16 v[122:125], v[190:193], v[230:233], v[122:125]
	v_mfma_f32_16x16x32_bf16 v[118:121], v[198:201], v[230:233], v[118:121]
	v_mfma_f32_16x16x32_bf16 v[18:21], v[194:197], v[210:213], v[18:21]
	v_mfma_f32_16x16x32_bf16 v[26:29], v[202:205], v[210:213], v[26:29]
	v_mfma_f32_16x16x32_bf16 v[42:45], v[194:197], v[218:221], v[42:45]
	v_mfma_f32_16x16x32_bf16 v[50:53], v[202:205], v[218:221], v[50:53]
	v_mfma_f32_16x16x32_bf16 v[74:77], v[194:197], v[226:229], v[74:77]
	v_mfma_f32_16x16x32_bf16 v[82:85], v[202:205], v[226:229], v[82:85]
	v_mfma_f32_16x16x32_bf16 v[122:125], v[194:197], v[234:237], v[122:125]
	v_mfma_f32_16x16x32_bf16 v[118:121], v[202:205], v[234:237], v[118:121]
	s_setprio 0
	s_barrier
	s_add_i32 s0, 0, 0x18000
	s_add_i32 s1, 0, 0x1c000
	v_add_u32_e32 v186, s0, v158
	v_add_u32_e32 v202, s1, v158
	ds_read_b128 v[174:177], v186
	ds_read_b128 v[178:181], v186 offset:1024
	ds_read_b128 v[182:185], v186 offset:2048
	ds_read_b128 v[186:189], v186 offset:3072
	ds_read_b128 v[190:193], v202
	ds_read_b128 v[194:197], v202 offset:1024
	ds_read_b128 v[198:201], v202 offset:2048
	ds_read_b128 v[202:205], v202 offset:3072
	s_add_u32 s68, s74, 0x40000
	s_addc_u32 s69, s75, 0
	s_mov_b32 m0, s85
	v_lshl_add_u64 v[246:247], s[68:69], 0, v[130:131]
	ds_read_b128 v[206:209], v160 offset:32768
	ds_read_b128 v[210:213], v160 offset:33792
	ds_read_b128 v[214:217], v160 offset:34816
	ds_read_b128 v[218:221], v160 offset:35840
	ds_read_b128 v[222:225], v160 offset:36864
	ds_read_b128 v[226:229], v160 offset:37888
	ds_read_b128 v[230:233], v160 offset:38912
	ds_read_b128 v[234:237], v160 offset:39936
	global_load_lds_dwordx4 v[246:247], off
	v_lshl_add_u64 v[246:247], s[68:69], 0, v[134:135]
	s_mov_b32 m0, s86
	s_nop 0
	global_load_lds_dwordx4 v[246:247], off
	s_waitcnt vmcnt(8)
	s_waitcnt lgkmcnt(0)
	s_barrier
	s_setprio 3
	v_mfma_f32_16x16x32_bf16 v[22:25], v[174:177], v[206:209], v[22:25]
	v_mfma_f32_16x16x32_bf16 v[30:33], v[182:185], v[206:209], v[30:33]
	v_mfma_f32_16x16x32_bf16 v[46:49], v[174:177], v[214:217], v[46:49]
	v_mfma_f32_16x16x32_bf16 v[54:57], v[182:185], v[214:217], v[54:57]
	v_mfma_f32_16x16x32_bf16 v[78:81], v[174:177], v[222:225], v[78:81]
	v_mfma_f32_16x16x32_bf16 v[86:89], v[182:185], v[222:225], v[86:89]
	v_mfma_f32_16x16x32_bf16 v[98:101], v[174:177], v[230:233], v[98:101]
	v_mfma_f32_16x16x32_bf16 v[102:105], v[182:185], v[230:233], v[102:105]
	v_mfma_f32_16x16x32_bf16 v[22:25], v[178:181], v[210:213], v[22:25]
	v_mfma_f32_16x16x32_bf16 v[30:33], v[186:189], v[210:213], v[30:33]
	v_mfma_f32_16x16x32_bf16 v[46:49], v[178:181], v[218:221], v[46:49]
	v_mfma_f32_16x16x32_bf16 v[54:57], v[186:189], v[218:221], v[54:57]
	v_mfma_f32_16x16x32_bf16 v[78:81], v[178:181], v[226:229], v[78:81]
	v_mfma_f32_16x16x32_bf16 v[86:89], v[186:189], v[226:229], v[86:89]
	v_mfma_f32_16x16x32_bf16 v[98:101], v[178:181], v[234:237], v[98:101]
	v_mfma_f32_16x16x32_bf16 v[102:105], v[186:189], v[234:237], v[102:105]
	v_mfma_f32_16x16x32_bf16 v[2:5], v[190:193], v[206:209], v[2:5]
	v_mfma_f32_16x16x32_bf16 v[6:9], v[198:201], v[206:209], v[6:9]
	v_mfma_f32_16x16x32_bf16 v[10:13], v[190:193], v[214:217], v[10:13]
	v_mfma_f32_16x16x32_bf16 v[14:17], v[198:201], v[214:217], v[14:17]
	v_mfma_f32_16x16x32_bf16 v[34:37], v[190:193], v[222:225], v[34:37]
	v_mfma_f32_16x16x32_bf16 v[38:41], v[198:201], v[222:225], v[38:41]
	v_mfma_f32_16x16x32_bf16 v[58:61], v[190:193], v[230:233], v[58:61]
	v_mfma_f32_16x16x32_bf16 v[62:65], v[198:201], v[230:233], v[62:65]
	v_mfma_f32_16x16x32_bf16 v[2:5], v[194:197], v[210:213], v[2:5]
	v_mfma_f32_16x16x32_bf16 v[6:9], v[202:205], v[210:213], v[6:9]
	v_mfma_f32_16x16x32_bf16 v[10:13], v[194:197], v[218:221], v[10:13]
	v_mfma_f32_16x16x32_bf16 v[14:17], v[202:205], v[218:221], v[14:17]
	v_mfma_f32_16x16x32_bf16 v[34:37], v[194:197], v[226:229], v[34:37]
	v_mfma_f32_16x16x32_bf16 v[38:41], v[202:205], v[226:229], v[38:41]
	v_mfma_f32_16x16x32_bf16 v[58:61], v[194:197], v[234:237], v[58:61]
	v_mfma_f32_16x16x32_bf16 v[62:65], v[202:205], v[234:237], v[62:65]
	s_setprio 0
	s_barrier
; #define PG8_STAGE(bufoff, gbase, voff) do { _Pragma("unroll") for (int _i = 0; _i < 2; ++_i) \
;         __builtin_amdgcn_global_load_lds((const unsigned*)((const char*)(gbase) + (voff)[_i]), (PG8_LAS unsigned*)(lds + (bufoff) + ldsw + _i * 8192), 16, 0, 0); } while (0)
; #define PG8_LDA(dst, b, h) do { _Pragma("unroll") for (int m = 0; m < 4; ++m) Frag<F8>::load(dst[m], lds + PG8_SA(b, h) + aoff + m * 2048); } while (0)
; #define PG8_MMA(ai, bj, At, Bt) do { __builtin_amdgcn_s_setprio(3); _Pragma("unroll") for (int m = 0; m < 4; ++m) _Pragma("unroll") for (int n = 0; n < 2; ++n) Frag<F8>::mma(acc[ai][bj][m][n], Bt[n], At[m]); \
;         __builtin_amdgcn_s_setprio(0); } while (0)
; #define PG8_WAIT_V(n) asm volatile("s_waitcnt vmcnt(" #n ")" ::: "memory")
; #define PG8_WAIT_L(n) asm volatile("s_waitcnt lgkmcnt(" #n ")" ::: "memory")
; #define PG8_BAR __builtin_amdgcn_s_barrier()
; #define PG8_SCHED __builtin_amdgcn_sched_barrier(0)
; template <class Epi, class Sched, bool ALIGN_EPI = false, bool SP2 = false, bool F8 = false>
; __device__ __forceinline__ void gemm_phase(PG8_LAS unsigned char* lds, const Gemm g, const Sched& S, const Epi& E) {
;     ...
;             PG8_LDA(At, 1, 1); PG8_STAGE(PG8_SB(1, 0), b3, voffB); PG8_STAGE(PG8_SB(1, 1), b3 + hstep, voffB); PG8_STAGE(PG8_SA(1, 0), a3, voffA);
;             PG8_WAIT_V(8); PG8_WAIT_L(0); PG8_BAR; PG8_MMA(1, 0, At, B0); PG8_MMA(1, 1, At, B1); PG8_BAR; PG8_SCHED;
;     ...
;         if constexpr (ALIGN_EPI) { if (wr == 0) PG8_BAR; }
	s_add_i32 s0, s0, s83
	v_lshl_add_u64 v[238:239], v[238:239], 0, s[40:41]
	s_mov_b32 m0, s0
	ds_read_b128 v[206:209], v160 offset:49152
	ds_read_b128 v[210:213], v160 offset:50176
	ds_read_b128 v[214:217], v160 offset:51200
	ds_read_b128 v[218:221], v160 offset:52224
	ds_read_b128 v[222:225], v160 offset:53248
	ds_read_b128 v[226:229], v160 offset:54272
	ds_read_b128 v[230:233], v160 offset:55296
	ds_read_b128 v[234:237], v160 offset:56320
	global_load_lds_dwordx4 v[238:239], off
	s_add_i32 m0, s0, 0x2000
	s_add_u32 s68, s72, 0x40080
	v_lshl_add_u64 v[238:239], v[240:241], 0, s[40:41]
	s_addc_u32 s69, s73, 0
	s_add_i32 s0, s1, s83
	global_load_lds_dwordx4 v[238:239], off
	v_lshl_add_u64 v[238:239], s[68:69], 0, v[132:133]
	s_mov_b32 m0, s0
	s_nop 0
	global_load_lds_dwordx4 v[238:239], off
	v_lshl_add_u64 v[238:239], s[68:69], 0, v[136:137]
	s_add_i32 m0, s0, 0x2000
	s_nop 0
	global_load_lds_dwordx4 v[238:239], off
	v_lshl_add_u64 v[238:239], v[242:243], 0, s[40:41]
	s_mov_b32 m0, s87
	s_nop 0
	global_load_lds_dwordx4 v[238:239], off
	v_lshl_add_u64 v[238:239], v[244:245], 0, s[40:41]
	s_mov_b32 m0, s88
	s_nop 0
	global_load_lds_dwordx4 v[238:239], off
	s_waitcnt vmcnt(8)
	s_waitcnt lgkmcnt(0)
	s_barrier
	s_setprio 3
	v_mfma_f32_16x16x32_bf16 v[66:69], v[174:177], v[206:209], v[66:69]
	v_mfma_f32_16x16x32_bf16 v[70:73], v[182:185], v[206:209], v[70:73]
	v_mfma_f32_16x16x32_bf16 v[90:93], v[174:177], v[214:217], v[90:93]
	v_mfma_f32_16x16x32_bf16 v[94:97], v[182:185], v[214:217], v[94:97]
	v_mfma_f32_16x16x32_bf16 v[106:109], v[174:177], v[222:225], v[106:109]
	v_mfma_f32_16x16x32_bf16 v[110:113], v[182:185], v[222:225], v[110:113]
	v_mfma_f32_16x16x32_bf16 v[114:117], v[174:177], v[230:233], v[114:117]
	v_mfma_f32_16x16x32_bf16 v[126:129], v[182:185], v[230:233], v[126:129]
	v_mfma_f32_16x16x32_bf16 v[66:69], v[178:181], v[210:213], v[66:69]
	v_mfma_f32_16x16x32_bf16 v[70:73], v[186:189], v[210:213], v[70:73]
	v_mfma_f32_16x16x32_bf16 v[90:93], v[178:181], v[218:221], v[90:93]
	v_mfma_f32_16x16x32_bf16 v[94:97], v[186:189], v[218:221], v[94:97]
	v_mfma_f32_16x16x32_bf16 v[106:109], v[178:181], v[226:229], v[106:109]
	v_mfma_f32_16x16x32_bf16 v[110:113], v[186:189], v[226:229], v[110:113]
	v_mfma_f32_16x16x32_bf16 v[114:117], v[178:181], v[234:237], v[114:117]
	v_mfma_f32_16x16x32_bf16 v[126:129], v[186:189], v[234:237], v[126:129]
	v_mfma_f32_16x16x32_bf16 v[18:21], v[190:193], v[206:209], v[18:21]
	v_mfma_f32_16x16x32_bf16 v[26:29], v[198:201], v[206:209], v[26:29]
	v_mfma_f32_16x16x32_bf16 v[42:45], v[190:193], v[214:217], v[42:45]
	v_mfma_f32_16x16x32_bf16 v[50:53], v[198:201], v[214:217], v[50:53]
	v_mfma_f32_16x16x32_bf16 v[74:77], v[190:193], v[222:225], v[74:77]
	v_mfma_f32_16x16x32_bf16 v[82:85], v[198:201], v[222:225], v[82:85]
	v_mfma_f32_16x16x32_bf16 v[122:125], v[190:193], v[230:233], v[122:125]
	v_mfma_f32_16x16x32_bf16 v[118:121], v[198:201], v[230:233], v[118:121]
	v_mfma_f32_16x16x32_bf16 v[18:21], v[194:197], v[210:213], v[18:21]
	v_mfma_f32_16x16x32_bf16 v[26:29], v[202:205], v[210:213], v[26:29]
	v_mfma_f32_16x16x32_bf16 v[42:45], v[194:197], v[218:221], v[42:45]
	v_mfma_f32_16x16x32_bf16 v[50:53], v[202:205], v[218:221], v[50:53]
	v_mfma_f32_16x16x32_bf16 v[74:77], v[194:197], v[226:229], v[74:77]
	v_mfma_f32_16x16x32_bf16 v[82:85], v[202:205], v[226:229], v[82:85]
	v_mfma_f32_16x16x32_bf16 v[122:125], v[194:197], v[234:237], v[122:125]
	v_mfma_f32_16x16x32_bf16 v[118:121], v[202:205], v[234:237], v[118:121]
	s_setprio 0
	s_barrier
	s_add_i32 s7, s7, 2
	s_add_u32 s70, s70, 0x100
	s_addc_u32 s71, s71, 0
	s_cmp_gt_u32 s7, 13
	s_cbranch_scc0 .LBB0_437
	s_and_b64 vcc, exec, s[42:43]
	s_cbranch_vccz .LBB0_440
	s_barrier

; #define PG8_STAGE(bufoff, gbase, voff) do { _Pragma("unroll") for (int _i = 0; _i < 2; ++_i) \
;         __builtin_amdgcn_global_load_lds((const unsigned*)((const char*)(gbase) + (voff)[_i]), (PG8_LAS unsigned*)(lds + (bufoff) + ldsw + _i * 8192), 16, 0, 0); } while (0)
; #define PG8_LDA(dst, b, h) do { _Pragma("unroll") for (int m = 0; m < 4; ++m) Frag<F8>::load(dst[m], lds + PG8_SA(b, h) + aoff + m * 2048); } while (0)
; #define PG8_LDB(dst, b, h) do { _Pragma("unroll") for (int n = 0; n < 2; ++n) Frag<F8>::load(dst[n], lds + PG8_SB(b, h) + boff + n * 2048); } while (0)
; #define PG8_MMA(ai, bj, At, Bt) do { __builtin_amdgcn_s_setprio(3); _Pragma("unroll") for (int m = 0; m < 4; ++m) _Pragma("unroll") for (int n = 0; n < 2; ++n) Frag<F8>::mma(acc[ai][bj][m][n], Bt[n], At[m]); \
;         __builtin_amdgcn_s_setprio(0); } while (0)
; #define PG8_WAIT_V(n) asm volatile("s_waitcnt vmcnt(" #n ")" ::: "memory")
; #define PG8_WAIT_L(n) asm volatile("s_waitcnt lgkmcnt(" #n ")" ::: "memory")
; #define PG8_BAR __builtin_amdgcn_s_barrier()
; template <class Epi, class Sched, bool ALIGN_EPI = false, bool SP2 = false, bool F8 = false>
; __device__ __forceinline__ void gemm_phase(PG8_LAS unsigned char* lds, const Gemm g, const Sched& S, const Epi& E) {
;     ...
;         const char* nA = has_next ? (const char*)g.A + (size_t)nxt.pm * tstep + nxt.ko : cA; const char* nB = has_next ? (const char*)g.Bt + (size_t)nxt.pn * tstep + nxt.ko : cB;
;         for (int t = 0; t < nt; t += 2) {
;             const bool last = (t == nt - 2);
;             const char* a1 = cA + (size_t)(t + 1) * kstep;
;             const char* a2 = last ? nA : cA + (size_t)(t + 2) * kstep; const char* b2 = last ? nB : cB + (size_t)(t + 2) * kstep;
;             const char* a3 = a2 + kstep; const char* b3 = b2 + kstep;
;             if (last && has_next) S.a_ready(nxt);
;             if constexpr (SP2) {
;             PG8_LDB(B0, 0, 0); PG8_LDB(B1, 0, 1); PG8_SCHED; PG8_LDA(At, 0, 0); PG8_STAGE(PG8_SA(1, 1), a1 + hstep, voffA);
;             PG8_WAIT_V(8); PG8_WAIT_L(0); PG8_BAR; PG8_MMA(0, 0, At, B0); PG8_MMA(0, 1, At, B1); PG8_BAR; PG8_SCHED;
;             PG8_LDA(At, 0, 1); PG8_STAGE(PG8_SB(0, 0), b2, voffB); PG8_STAGE(PG8_SB(0, 1), b2 + hstep, voffB); PG8_STAGE(PG8_SA(0, 0), a2, voffA);
;             PG8_WAIT_V(8); PG8_WAIT_L(0); PG8_BAR; PG8_MMA(1, 0, At, B0); PG8_MMA(1, 1, At, B1); PG8_BAR; PG8_SCHED;
.LBB0_561:
	s_ashr_i32 s25, s24, 31
	s_lshl_b64 s[4:5], s[24:25], 19
	s_add_u32 s36, s50, s4
	s_addc_u32 s37, s51, s5
	s_and_b64 s[4:5], s[8:9], exec
	s_cselect_b32 s6, s37, s43
	s_cselect_b32 s7, s36, s42
	s_ashr_i32 s31, s30, 31
	s_lshl_b64 s[4:5], s[30:31], 19
	s_add_u32 s38, s52, s4
	s_addc_u32 s39, s53, s5
	s_and_b64 s[4:5], s[8:9], exec
	s_cselect_b32 s25, s39, s45
	s_cselect_b32 s31, s38, s44
	s_add_u32 s42, s42, 0x40080
	s_addc_u32 s43, s43, 0
	s_add_u32 s84, s44, 0x100
	s_addc_u32 s85, s45, 0
	s_mov_b32 s86, -2
	ds_read_b128 v[146:149], v155
	ds_read_b128 v[158:161], v155 offset:1024
	ds_read_b128 v[166:169], v155 offset:2048
	ds_read_b128 v[170:173], v155 offset:3072
	ds_read_b128 v[174:177], v156
	ds_read_b128 v[178:181], v156 offset:1024
	ds_read_b128 v[182:185], v156 offset:2048
	ds_read_b128 v[186:189], v156 offset:3072
	s_add_u32 s0, s42, 0xfffc0080
	s_addc_u32 s1, s43, -1
	s_cmp_eq_u32 s86, 12
	s_cselect_b32 s47, s6, s1
	s_cselect_b32 s46, s7, s0
	s_cselect_b32 s45, s25, s85
	s_cselect_b32 s44, s31, s84
	v_lshl_add_u64 v[222:223], s[42:43], 0, v[138:139]
	s_add_i32 m0, s41, 0xc000
	ds_read_b128 v[190:193], v157
	ds_read_b128 v[194:197], v157 offset:1024
	ds_read_b128 v[198:201], v157 offset:2048
	ds_read_b128 v[202:205], v157 offset:3072
	ds_read_b128 v[206:209], v157 offset:4096
	ds_read_b128 v[210:213], v157 offset:5120
	ds_read_b128 v[214:217], v157 offset:6144
	ds_read_b128 v[218:221], v157 offset:7168
	global_load_lds_dwordx4 v[222:223], off
	v_lshl_add_u64 v[222:223], s[42:43], 0, v[140:141]
	s_add_i32 m0, s41, 0xe000
	s_nop 0
	global_load_lds_dwordx4 v[222:223], off
	s_waitcnt vmcnt(8)
	s_waitcnt lgkmcnt(0)
	s_barrier
	s_setprio 3
	v_mfma_f32_16x16x32_bf16 v[126:129], v[146:149], v[190:193], 0
	v_mfma_f32_16x16x32_bf16 v[118:121], v[166:169], v[190:193], 0
	v_mfma_f32_16x16x32_bf16 v[110:113], v[146:149], v[198:201], 0
	v_mfma_f32_16x16x32_bf16 v[102:105], v[166:169], v[198:201], 0
	v_mfma_f32_16x16x32_bf16 v[94:97], v[146:149], v[206:209], 0
	v_mfma_f32_16x16x32_bf16 v[86:89], v[166:169], v[206:209], 0
	v_mfma_f32_16x16x32_bf16 v[78:81], v[146:149], v[214:217], 0
	v_mfma_f32_16x16x32_bf16 v[70:73], v[166:169], v[214:217], 0
	v_mfma_f32_16x16x32_bf16 v[126:129], v[158:161], v[194:197], v[126:129]
	v_mfma_f32_16x16x32_bf16 v[118:121], v[170:173], v[194:197], v[118:121]
	v_mfma_f32_16x16x32_bf16 v[110:113], v[158:161], v[202:205], v[110:113]
	v_mfma_f32_16x16x32_bf16 v[102:105], v[170:173], v[202:205], v[102:105]
	v_mfma_f32_16x16x32_bf16 v[94:97], v[158:161], v[210:213], v[94:97]
	v_mfma_f32_16x16x32_bf16 v[86:89], v[170:173], v[210:213], v[86:89]
	v_mfma_f32_16x16x32_bf16 v[78:81], v[158:161], v[218:221], v[78:81]
	v_mfma_f32_16x16x32_bf16 v[70:73], v[170:173], v[218:221], v[70:73]
	v_mfma_f32_16x16x32_bf16 v[122:125], v[174:177], v[190:193], 0
	v_mfma_f32_16x16x32_bf16 v[114:117], v[182:185], v[190:193], 0
	v_mfma_f32_16x16x32_bf16 v[106:109], v[174:177], v[198:201], 0
	v_mfma_f32_16x16x32_bf16 v[98:101], v[182:185], v[198:201], 0
	v_mfma_f32_16x16x32_bf16 v[90:93], v[174:177], v[206:209], 0
	v_mfma_f32_16x16x32_bf16 v[82:85], v[182:185], v[206:209], 0
	v_mfma_f32_16x16x32_bf16 v[74:77], v[174:177], v[214:217], 0
	v_mfma_f32_16x16x32_bf16 v[66:69], v[182:185], v[214:217], 0
	v_mfma_f32_16x16x32_bf16 v[122:125], v[178:181], v[194:197], v[122:125]
	v_mfma_f32_16x16x32_bf16 v[114:117], v[186:189], v[194:197], v[114:117]
	v_mfma_f32_16x16x32_bf16 v[106:109], v[178:181], v[202:205], v[106:109]
	v_mfma_f32_16x16x32_bf16 v[98:101], v[186:189], v[202:205], v[98:101]
	v_mfma_f32_16x16x32_bf16 v[90:93], v[178:181], v[210:213], v[90:93]
	v_mfma_f32_16x16x32_bf16 v[82:85], v[186:189], v[210:213], v[82:85]
	v_mfma_f32_16x16x32_bf16 v[74:77], v[178:181], v[218:221], v[74:77]
	v_mfma_f32_16x16x32_bf16 v[66:69], v[186:189], v[218:221], v[66:69]
	s_setprio 0
	s_barrier
	s_add_i32 s0, s80, s49
	v_lshl_add_u64 v[222:223], s[44:45], 0, v[134:135]
	s_mov_b32 m0, s0
	ds_read_b128 v[190:193], v157 offset:16384
	ds_read_b128 v[194:197], v157 offset:17408
	ds_read_b128 v[198:201], v157 offset:18432
	ds_read_b128 v[202:205], v157 offset:19456
	ds_read_b128 v[206:209], v157 offset:20480
	ds_read_b128 v[210:213], v157 offset:21504
	ds_read_b128 v[214:217], v157 offset:22528
	ds_read_b128 v[218:221], v157 offset:23552
	global_load_lds_dwordx4 v[222:223], off
	s_add_i32 m0, s0, 0x2000
	s_add_u32 s4, s44, 0x40000
	v_lshl_add_u64 v[224:225], s[44:45], 0, v[130:131]
	s_addc_u32 s5, s45, 0
	s_add_i32 s0, s81, s49
	global_load_lds_dwordx4 v[224:225], off
	v_lshl_add_u64 v[226:227], s[4:5], 0, v[134:135]
	s_mov_b32 m0, s0
	v_lshl_add_u64 v[228:229], s[46:47], 0, v[132:133]
	global_load_lds_dwordx4 v[226:227], off
	v_lshl_add_u64 v[226:227], s[4:5], 0, v[130:131]
	s_add_i32 m0, s0, 0x2000
	s_nop 0
	global_load_lds_dwordx4 v[226:227], off
	v_lshl_add_u64 v[226:227], s[46:47], 0, v[136:137]
	s_mov_b32 m0, s41
	s_nop 0
	global_load_lds_dwordx4 v[226:227], off
	s_mov_b32 m0, s72
	s_nop 0
	global_load_lds_dwordx4 v[228:229], off
	s_waitcnt vmcnt(8)
	s_waitcnt lgkmcnt(0)
	s_barrier
; #define PG8_STAGE(bufoff, gbase, voff) do { _Pragma("unroll") for (int _i = 0; _i < 2; ++_i) \
;         __builtin_amdgcn_global_load_lds((const unsigned*)((const char*)(gbase) + (voff)[_i]), (PG8_LAS unsigned*)(lds + (bufoff) + ldsw + _i * 8192), 16, 0, 0); } while (0)
; #define PG8_LDA(dst, b, h) do { _Pragma("unroll") for (int m = 0; m < 4; ++m) Frag<F8>::load(dst[m], lds + PG8_SA(b, h) + aoff + m * 2048); } while (0)
; #define PG8_LDB(dst, b, h) do { _Pragma("unroll") for (int n = 0; n < 2; ++n) Frag<F8>::load(dst[n], lds + PG8_SB(b, h) + boff + n * 2048); } while (0)
; #define PG8_MMA(ai, bj, At, Bt) do { __builtin_amdgcn_s_setprio(3); _Pragma("unroll") for (int m = 0; m < 4; ++m) _Pragma("unroll") for (int n = 0; n < 2; ++n) Frag<F8>::mma(acc[ai][bj][m][n], Bt[n], At[m]); \
;         __builtin_amdgcn_s_setprio(0); } while (0)
; #define PG8_WAIT_V(n) asm volatile("s_waitcnt vmcnt(" #n ")" ::: "memory")
; #define PG8_WAIT_L(n) asm volatile("s_waitcnt lgkmcnt(" #n ")" ::: "memory")
; #define PG8_BAR __builtin_amdgcn_s_barrier()
; #define PG8_SCHED __builtin_amdgcn_sched_barrier(0)
; template <class Epi, class Sched, bool ALIGN_EPI = false, bool SP2 = false, bool F8 = false>
; __device__ __forceinline__ void gemm_phase(PG8_LAS unsigned char* lds, const Gemm g, const Sched& S, const Epi& E) {
;     ...
;             PG8_WAIT_V(8); PG8_WAIT_L(0); PG8_BAR; PG8_MMA(1, 0, At, B0); PG8_MMA(1, 1, At, B1); PG8_BAR; PG8_SCHED;
;             PG8_LDB(B0, 1, 0); PG8_LDB(B1, 1, 1); PG8_SCHED; PG8_LDA(At, 1, 0); PG8_STAGE(PG8_SA(0, 1), a2 + hstep, voffA);
;             PG8_WAIT_V(8); PG8_WAIT_L(0); PG8_BAR; PG8_MMA(0, 0, At, B0); PG8_MMA(0, 1, At, B1); PG8_BAR; PG8_SCHED;
	s_setprio 3
	v_mfma_f32_16x16x32_bf16 v[62:65], v[146:149], v[190:193], 0
	v_mfma_f32_16x16x32_bf16 v[58:61], v[166:169], v[190:193], 0
	v_mfma_f32_16x16x32_bf16 v[50:53], v[146:149], v[198:201], 0
	v_mfma_f32_16x16x32_bf16 v[42:45], v[166:169], v[198:201], 0
	v_mfma_f32_16x16x32_bf16 v[34:37], v[146:149], v[206:209], 0
	v_mfma_f32_16x16x32_bf16 v[26:29], v[166:169], v[206:209], 0
	v_mfma_f32_16x16x32_bf16 v[14:17], v[146:149], v[214:217], 0
	v_mfma_f32_16x16x32_bf16 v[6:9], v[166:169], v[214:217], 0
	v_mfma_f32_16x16x32_bf16 v[62:65], v[158:161], v[194:197], v[62:65]
	v_mfma_f32_16x16x32_bf16 v[58:61], v[170:173], v[194:197], v[58:61]
	v_mfma_f32_16x16x32_bf16 v[50:53], v[158:161], v[202:205], v[50:53]
	v_mfma_f32_16x16x32_bf16 v[42:45], v[170:173], v[202:205], v[42:45]
	v_mfma_f32_16x16x32_bf16 v[34:37], v[158:161], v[210:213], v[34:37]
	v_mfma_f32_16x16x32_bf16 v[26:29], v[170:173], v[210:213], v[26:29]
	v_mfma_f32_16x16x32_bf16 v[14:17], v[158:161], v[218:221], v[14:17]
	v_mfma_f32_16x16x32_bf16 v[6:9], v[170:173], v[218:221], v[6:9]
	v_mfma_f32_16x16x32_bf16 v[54:57], v[174:177], v[190:193], 0
	v_mfma_f32_16x16x32_bf16 v[46:49], v[182:185], v[190:193], 0
	v_mfma_f32_16x16x32_bf16 v[38:41], v[174:177], v[198:201], 0
	v_mfma_f32_16x16x32_bf16 v[30:33], v[182:185], v[198:201], 0
	v_mfma_f32_16x16x32_bf16 v[22:25], v[174:177], v[206:209], 0
	v_mfma_f32_16x16x32_bf16 v[18:21], v[182:185], v[206:209], 0
	v_mfma_f32_16x16x32_bf16 v[10:13], v[174:177], v[214:217], 0
	v_mfma_f32_16x16x32_bf16 v[2:5], v[182:185], v[214:217], 0
	v_mfma_f32_16x16x32_bf16 v[54:57], v[178:181], v[194:197], v[54:57]
	v_mfma_f32_16x16x32_bf16 v[46:49], v[186:189], v[194:197], v[46:49]
	v_mfma_f32_16x16x32_bf16 v[38:41], v[178:181], v[202:205], v[38:41]
	v_mfma_f32_16x16x32_bf16 v[30:33], v[186:189], v[202:205], v[30:33]
	v_mfma_f32_16x16x32_bf16 v[22:25], v[178:181], v[210:213], v[22:25]
	v_mfma_f32_16x16x32_bf16 v[18:21], v[186:189], v[210:213], v[18:21]
	v_mfma_f32_16x16x32_bf16 v[10:13], v[178:181], v[218:221], v[10:13]
	v_mfma_f32_16x16x32_bf16 v[2:5], v[186:189], v[218:221], v[2:5]
	s_setprio 0
	s_barrier
	s_add_i32 s0, 0, 0x18000
	v_add_u32_e32 v165, s0, v151
	s_add_i32 s1, 0, 0x1c000
	ds_read_b128 v[146:149], v165
	ds_read_b128 v[158:161], v165 offset:1024
	ds_read_b128 v[166:169], v165 offset:2048
	ds_read_b128 v[170:173], v165 offset:3072
	v_add_u32_e32 v165, s1, v151
	ds_read_b128 v[174:177], v165
	ds_read_b128 v[178:181], v165 offset:1024
	ds_read_b128 v[182:185], v165 offset:2048
	ds_read_b128 v[186:189], v165 offset:3072
	s_add_u32 s4, s46, 0x40000
	s_addc_u32 s5, s47, 0
	s_mov_b32 m0, s73
	v_lshl_add_u64 v[230:231], s[4:5], 0, v[136:137]
	ds_read_b128 v[190:193], v157 offset:32768
	ds_read_b128 v[194:197], v157 offset:33792
	ds_read_b128 v[198:201], v157 offset:34816
	ds_read_b128 v[202:205], v157 offset:35840
	ds_read_b128 v[206:209], v157 offset:36864
	ds_read_b128 v[210:213], v157 offset:37888
	ds_read_b128 v[214:217], v157 offset:38912
	ds_read_b128 v[218:221], v157 offset:39936
	global_load_lds_dwordx4 v[230:231], off
	v_lshl_add_u64 v[230:231], s[4:5], 0, v[132:133]
	s_mov_b32 m0, s74
	s_nop 0
	global_load_lds_dwordx4 v[230:231], off
	s_waitcnt vmcnt(8)
	s_waitcnt lgkmcnt(0)
	s_barrier
	s_setprio 3
	v_mfma_f32_16x16x32_bf16 v[126:129], v[146:149], v[190:193], v[126:129]
	v_mfma_f32_16x16x32_bf16 v[118:121], v[166:169], v[190:193], v[118:121]
	v_mfma_f32_16x16x32_bf16 v[110:113], v[146:149], v[198:201], v[110:113]
	v_mfma_f32_16x16x32_bf16 v[102:105], v[166:169], v[198:201], v[102:105]
	v_mfma_f32_16x16x32_bf16 v[94:97], v[146:149], v[206:209], v[94:97]
	v_mfma_f32_16x16x32_bf16 v[86:89], v[166:169], v[206:209], v[86:89]
	v_mfma_f32_16x16x32_bf16 v[78:81], v[146:149], v[214:217], v[78:81]
	v_mfma_f32_16x16x32_bf16 v[70:73], v[166:169], v[214:217], v[70:73]
	v_mfma_f32_16x16x32_bf16 v[126:129], v[158:161], v[194:197], v[126:129]
	v_mfma_f32_16x16x32_bf16 v[118:121], v[170:173], v[194:197], v[118:121]
	v_mfma_f32_16x16x32_bf16 v[110:113], v[158:161], v[202:205], v[110:113]
	v_mfma_f32_16x16x32_bf16 v[102:105], v[170:173], v[202:205], v[102:105]
	v_mfma_f32_16x16x32_bf16 v[94:97], v[158:161], v[210:213], v[94:97]
	v_mfma_f32_16x16x32_bf16 v[86:89], v[170:173], v[210:213], v[86:89]
	v_mfma_f32_16x16x32_bf16 v[78:81], v[158:161], v[218:221], v[78:81]
	v_mfma_f32_16x16x32_bf16 v[70:73], v[170:173], v[218:221], v[70:73]
	v_mfma_f32_16x16x32_bf16 v[122:125], v[174:177], v[190:193], v[122:125]
	v_mfma_f32_16x16x32_bf16 v[114:117], v[182:185], v[190:193], v[114:117]
	v_mfma_f32_16x16x32_bf16 v[106:109], v[174:177], v[198:201], v[106:109]
	v_mfma_f32_16x16x32_bf16 v[98:101], v[182:185], v[198:201], v[98:101]
	v_mfma_f32_16x16x32_bf16 v[90:93], v[174:177], v[206:209], v[90:93]
	v_mfma_f32_16x16x32_bf16 v[82:85], v[182:185], v[206:209], v[82:85]
	v_mfma_f32_16x16x32_bf16 v[74:77], v[174:177], v[214:217], v[74:77]
	v_mfma_f32_16x16x32_bf16 v[66:69], v[182:185], v[214:217], v[66:69]
	v_mfma_f32_16x16x32_bf16 v[122:125], v[178:181], v[194:197], v[122:125]
	v_mfma_f32_16x16x32_bf16 v[114:117], v[186:189], v[194:197], v[114:117]
	v_mfma_f32_16x16x32_bf16 v[106:109], v[178:181], v[202:205], v[106:109]
	v_mfma_f32_16x16x32_bf16 v[98:101], v[186:189], v[202:205], v[98:101]
	v_mfma_f32_16x16x32_bf16 v[90:93], v[178:181], v[210:213], v[90:93]
	v_mfma_f32_16x16x32_bf16 v[82:85], v[186:189], v[210:213], v[82:85]
	v_mfma_f32_16x16x32_bf16 v[74:77], v[178:181], v[218:221], v[74:77]
	v_mfma_f32_16x16x32_bf16 v[66:69], v[186:189], v[218:221], v[66:69]
	s_setprio 0
	s_barrier
; #define PG8_STAGE(bufoff, gbase, voff) do { _Pragma("unroll") for (int _i = 0; _i < 2; ++_i) \
;         __builtin_amdgcn_global_load_lds((const unsigned*)((const char*)(gbase) + (voff)[_i]), (PG8_LAS unsigned*)(lds + (bufoff) + ldsw + _i * 8192), 16, 0, 0); } while (0)
; #define PG8_LDA(dst, b, h) do { _Pragma("unroll") for (int m = 0; m < 4; ++m) Frag<F8>::load(dst[m], lds + PG8_SA(b, h) + aoff + m * 2048); } while (0)
; #define PG8_LDB(dst, b, h) do { _Pragma("unroll") for (int n = 0; n < 2; ++n) Frag<F8>::load(dst[n], lds + PG8_SB(b, h) + boff + n * 2048); } while (0)
; #define PG8_MMA(ai, bj, At, Bt) do { __builtin_amdgcn_s_setprio(3); _Pragma("unroll") for (int m = 0; m < 4; ++m) _Pragma("unroll") for (int n = 0; n < 2; ++n) Frag<F8>::mma(acc[ai][bj][m][n], Bt[n], At[m]); \
;         __builtin_amdgcn_s_setprio(0); } while (0)
; #define PG8_WAIT_V(n) asm volatile("s_waitcnt vmcnt(" #n ")" ::: "memory")
; #define PG8_WAIT_L(n) asm volatile("s_waitcnt lgkmcnt(" #n ")" ::: "memory")
; #define PG8_BAR __builtin_amdgcn_s_barrier()
; #define PG8_SCHED __builtin_amdgcn_sched_barrier(0)
; template <class Epi, class Sched, bool ALIGN_EPI = false, bool SP2 = false, bool F8 = false>
; __device__ __forceinline__ void gemm_phase(PG8_LAS unsigned char* lds, const Gemm g, const Sched& S, const Epi& E) {
;     ...
;             PG8_LDB(B0, 0, 0); PG8_LDB(B1, 0, 1); PG8_SCHED; PG8_LDA(At, 0, 0); PG8_STAGE(PG8_SA(1, 1), a1 + hstep, voffA);
;             PG8_WAIT_V(8); PG8_WAIT_L(0); PG8_BAR; PG8_MMA(0, 0, At, B0); PG8_MMA(0, 1, At, B1); PG8_BAR; PG8_SCHED;
;     ...
;             PG8_LDA(At, 1, 1); PG8_STAGE(PG8_SB(1, 0), b3, voffB); PG8_STAGE(PG8_SB(1, 1), b3 + hstep, voffB); PG8_STAGE(PG8_SA(1, 0), a3, voffA);
;             PG8_WAIT_V(8); PG8_WAIT_L(0); PG8_BAR; PG8_MMA(1, 0, At, B0); PG8_MMA(1, 1, At, B1); PG8_BAR; PG8_SCHED;
	s_add_i32 s0, s0, s49
	v_lshl_add_u64 v[222:223], v[222:223], 0, s[18:19]
	s_mov_b32 m0, s0
	ds_read_b128 v[190:193], v157 offset:49152
	ds_read_b128 v[194:197], v157 offset:50176
	ds_read_b128 v[198:201], v157 offset:51200
	ds_read_b128 v[202:205], v157 offset:52224
	ds_read_b128 v[206:209], v157 offset:53248
	ds_read_b128 v[210:213], v157 offset:54272
	ds_read_b128 v[214:217], v157 offset:55296
	ds_read_b128 v[218:221], v157 offset:56320
	global_load_lds_dwordx4 v[222:223], off
	s_add_i32 m0, s0, 0x2000
	s_add_u32 s4, s44, 0x40080
	v_lshl_add_u64 v[222:223], v[224:225], 0, s[18:19]
	s_addc_u32 s5, s45, 0
	s_add_i32 s0, s1, s49
	global_load_lds_dwordx4 v[222:223], off
	v_lshl_add_u64 v[222:223], s[4:5], 0, v[134:135]
	s_mov_b32 m0, s0
	s_nop 0
	global_load_lds_dwordx4 v[222:223], off
	v_lshl_add_u64 v[222:223], s[4:5], 0, v[130:131]
	s_add_i32 m0, s0, 0x2000
	s_nop 0
	global_load_lds_dwordx4 v[222:223], off
	v_lshl_add_u64 v[222:223], v[226:227], 0, s[18:19]
	s_mov_b32 m0, s75
	s_nop 0
	global_load_lds_dwordx4 v[222:223], off
	v_lshl_add_u64 v[222:223], v[228:229], 0, s[18:19]
	s_mov_b32 m0, s79
	s_nop 0
	global_load_lds_dwordx4 v[222:223], off
	s_waitcnt vmcnt(8)
	s_waitcnt lgkmcnt(0)
	s_barrier
	s_setprio 3
	v_mfma_f32_16x16x32_bf16 v[62:65], v[146:149], v[190:193], v[62:65]
	v_mfma_f32_16x16x32_bf16 v[58:61], v[166:169], v[190:193], v[58:61]
	v_mfma_f32_16x16x32_bf16 v[50:53], v[146:149], v[198:201], v[50:53]
	v_mfma_f32_16x16x32_bf16 v[42:45], v[166:169], v[198:201], v[42:45]
	v_mfma_f32_16x16x32_bf16 v[34:37], v[146:149], v[206:209], v[34:37]
	v_mfma_f32_16x16x32_bf16 v[26:29], v[166:169], v[206:209], v[26:29]
	v_mfma_f32_16x16x32_bf16 v[14:17], v[146:149], v[214:217], v[14:17]
	v_mfma_f32_16x16x32_bf16 v[6:9], v[166:169], v[214:217], v[6:9]
	v_mfma_f32_16x16x32_bf16 v[62:65], v[158:161], v[194:197], v[62:65]
	v_mfma_f32_16x16x32_bf16 v[58:61], v[170:173], v[194:197], v[58:61]
	v_mfma_f32_16x16x32_bf16 v[50:53], v[158:161], v[202:205], v[50:53]
	v_mfma_f32_16x16x32_bf16 v[42:45], v[170:173], v[202:205], v[42:45]
	v_mfma_f32_16x16x32_bf16 v[34:37], v[158:161], v[210:213], v[34:37]
	v_mfma_f32_16x16x32_bf16 v[26:29], v[170:173], v[210:213], v[26:29]
	v_mfma_f32_16x16x32_bf16 v[14:17], v[158:161], v[218:221], v[14:17]
	v_mfma_f32_16x16x32_bf16 v[6:9], v[170:173], v[218:221], v[6:9]
	v_mfma_f32_16x16x32_bf16 v[54:57], v[174:177], v[190:193], v[54:57]
	v_mfma_f32_16x16x32_bf16 v[46:49], v[182:185], v[190:193], v[46:49]
	v_mfma_f32_16x16x32_bf16 v[38:41], v[174:177], v[198:201], v[38:41]
	v_mfma_f32_16x16x32_bf16 v[30:33], v[182:185], v[198:201], v[30:33]
	v_mfma_f32_16x16x32_bf16 v[22:25], v[174:177], v[206:209], v[22:25]
	v_mfma_f32_16x16x32_bf16 v[18:21], v[182:185], v[206:209], v[18:21]
	v_mfma_f32_16x16x32_bf16 v[10:13], v[174:177], v[214:217], v[10:13]
	v_mfma_f32_16x16x32_bf16 v[2:5], v[182:185], v[214:217], v[2:5]
	v_mfma_f32_16x16x32_bf16 v[54:57], v[178:181], v[194:197], v[54:57]
	v_mfma_f32_16x16x32_bf16 v[46:49], v[186:189], v[194:197], v[46:49]
	v_mfma_f32_16x16x32_bf16 v[38:41], v[178:181], v[202:205], v[38:41]
	v_mfma_f32_16x16x32_bf16 v[30:33], v[186:189], v[202:205], v[30:33]
	v_mfma_f32_16x16x32_bf16 v[22:25], v[178:181], v[210:213], v[22:25]
	v_mfma_f32_16x16x32_bf16 v[18:21], v[186:189], v[210:213], v[18:21]
	v_mfma_f32_16x16x32_bf16 v[10:13], v[178:181], v[218:221], v[10:13]
	v_mfma_f32_16x16x32_bf16 v[2:5], v[186:189], v[218:221], v[2:5]
	s_setprio 0
	s_barrier
	s_add_i32 s86, s86, 2
	s_add_u32 s42, s42, 0x100
	s_addc_u32 s43, s43, 0
	s_add_u32 s84, s84, 0x100
	s_addc_u32 s85, s85, 0
	s_cmp_gt_u32 s86, 13
	s_cbranch_scc1 .Lpeel_exit_1
.LBB0_562:
	ds_read_b128 v[146:149], v155
	ds_read_b128 v[158:161], v155 offset:1024
	ds_read_b128 v[166:169], v155 offset:2048
	ds_read_b128 v[170:173], v155 offset:3072
	ds_read_b128 v[174:177], v156
	ds_read_b128 v[178:181], v156 offset:1024
	ds_read_b128 v[182:185], v156 offset:2048
	ds_read_b128 v[186:189], v156 offset:3072
	s_add_u32 s0, s42, 0xfffc0080
	s_addc_u32 s1, s43, -1
	s_cmp_eq_u32 s86, 12
	s_cselect_b32 s47, s6, s1
	s_cselect_b32 s46, s7, s0
	s_cselect_b32 s45, s25, s85
	s_cselect_b32 s44, s31, s84
	v_lshl_add_u64 v[222:223], s[42:43], 0, v[138:139]
	s_add_i32 m0, s41, 0xc000
	ds_read_b128 v[190:193], v157
	ds_read_b128 v[194:197], v157 offset:1024
	ds_read_b128 v[198:201], v157 offset:2048
	ds_read_b128 v[202:205], v157 offset:3072
	ds_read_b128 v[206:209], v157 offset:4096
	ds_read_b128 v[210:213], v157 offset:5120
	ds_read_b128 v[214:217], v157 offset:6144
	ds_read_b128 v[218:221], v157 offset:7168
	global_load_lds_dwordx4 v[222:223], off
	v_lshl_add_u64 v[222:223], s[42:43], 0, v[140:141]
	s_add_i32 m0, s41, 0xe000
	s_nop 0
	global_load_lds_dwordx4 v[222:223], off
	s_waitcnt vmcnt(8)
	s_waitcnt lgkmcnt(0)
	s_barrier
; #define PG8_STAGE(bufoff, gbase, voff) do { _Pragma("unroll") for (int _i = 0; _i < 2; ++_i) \
;         __builtin_amdgcn_global_load_lds((const unsigned*)((const char*)(gbase) + (voff)[_i]), (PG8_LAS unsigned*)(lds + (bufoff) + ldsw + _i * 8192), 16, 0, 0); } while (0)
; #define PG8_LDA(dst, b, h) do { _Pragma("unroll") for (int m = 0; m < 4; ++m) Frag<F8>::load(dst[m], lds + PG8_SA(b, h) + aoff + m * 2048); } while (0)
; #define PG8_MMA(ai, bj, At, Bt) do { __builtin_amdgcn_s_setprio(3); _Pragma("unroll") for (int m = 0; m < 4; ++m) _Pragma("unroll") for (int n = 0; n < 2; ++n) Frag<F8>::mma(acc[ai][bj][m][n], Bt[n], At[m]); \
;         __builtin_amdgcn_s_setprio(0); } while (0)
; #define PG8_WAIT_V(n) asm volatile("s_waitcnt vmcnt(" #n ")" ::: "memory")
; #define PG8_WAIT_L(n) asm volatile("s_waitcnt lgkmcnt(" #n ")" ::: "memory")
; #define PG8_BAR __builtin_amdgcn_s_barrier()
; #define PG8_SCHED __builtin_amdgcn_sched_barrier(0)
; template <class Epi, class Sched, bool ALIGN_EPI = false, bool SP2 = false, bool F8 = false>
; __device__ __forceinline__ void gemm_phase(PG8_LAS unsigned char* lds, const Gemm g, const Sched& S, const Epi& E) {
;     ...
;             PG8_WAIT_V(8); PG8_WAIT_L(0); PG8_BAR; PG8_MMA(0, 0, At, B0); PG8_MMA(0, 1, At, B1); PG8_BAR; PG8_SCHED;
;             PG8_LDA(At, 0, 1); PG8_STAGE(PG8_SB(0, 0), b2, voffB); PG8_STAGE(PG8_SB(0, 1), b2 + hstep, voffB); PG8_STAGE(PG8_SA(0, 0), a2, voffA);
;             PG8_WAIT_V(8); PG8_WAIT_L(0); PG8_BAR; PG8_MMA(1, 0, At, B0); PG8_MMA(1, 1, At, B1); PG8_BAR; PG8_SCHED;
	s_setprio 3
	v_mfma_f32_16x16x32_bf16 v[126:129], v[146:149], v[190:193], v[126:129]
	v_mfma_f32_16x16x32_bf16 v[118:121], v[166:169], v[190:193], v[118:121]
	v_mfma_f32_16x16x32_bf16 v[110:113], v[146:149], v[198:201], v[110:113]
	v_mfma_f32_16x16x32_bf16 v[102:105], v[166:169], v[198:201], v[102:105]
	v_mfma_f32_16x16x32_bf16 v[94:97], v[146:149], v[206:209], v[94:97]
	v_mfma_f32_16x16x32_bf16 v[86:89], v[166:169], v[206:209], v[86:89]
	v_mfma_f32_16x16x32_bf16 v[78:81], v[146:149], v[214:217], v[78:81]
	v_mfma_f32_16x16x32_bf16 v[70:73], v[166:169], v[214:217], v[70:73]
	v_mfma_f32_16x16x32_bf16 v[126:129], v[158:161], v[194:197], v[126:129]
	v_mfma_f32_16x16x32_bf16 v[118:121], v[170:173], v[194:197], v[118:121]
	v_mfma_f32_16x16x32_bf16 v[110:113], v[158:161], v[202:205], v[110:113]
	v_mfma_f32_16x16x32_bf16 v[102:105], v[170:173], v[202:205], v[102:105]
	v_mfma_f32_16x16x32_bf16 v[94:97], v[158:161], v[210:213], v[94:97]
	v_mfma_f32_16x16x32_bf16 v[86:89], v[170:173], v[210:213], v[86:89]
	v_mfma_f32_16x16x32_bf16 v[78:81], v[158:161], v[218:221], v[78:81]
	v_mfma_f32_16x16x32_bf16 v[70:73], v[170:173], v[218:221], v[70:73]
	v_mfma_f32_16x16x32_bf16 v[122:125], v[174:177], v[190:193], v[122:125]
	v_mfma_f32_16x16x32_bf16 v[114:117], v[182:185], v[190:193], v[114:117]
	v_mfma_f32_16x16x32_bf16 v[106:109], v[174:177], v[198:201], v[106:109]
	v_mfma_f32_16x16x32_bf16 v[98:101], v[182:185], v[198:201], v[98:101]
	v_mfma_f32_16x16x32_bf16 v[90:93], v[174:177], v[206:209], v[90:93]
	v_mfma_f32_16x16x32_bf16 v[82:85], v[182:185], v[206:209], v[82:85]
	v_mfma_f32_16x16x32_bf16 v[74:77], v[174:177], v[214:217], v[74:77]
	v_mfma_f32_16x16x32_bf16 v[66:69], v[182:185], v[214:217], v[66:69]
	v_mfma_f32_16x16x32_bf16 v[122:125], v[178:181], v[194:197], v[122:125]
	v_mfma_f32_16x16x32_bf16 v[114:117], v[186:189], v[194:197], v[114:117]
	v_mfma_f32_16x16x32_bf16 v[106:109], v[178:181], v[202:205], v[106:109]
	v_mfma_f32_16x16x32_bf16 v[98:101], v[186:189], v[202:205], v[98:101]
	v_mfma_f32_16x16x32_bf16 v[90:93], v[178:181], v[210:213], v[90:93]
	v_mfma_f32_16x16x32_bf16 v[82:85], v[186:189], v[210:213], v[82:85]
	v_mfma_f32_16x16x32_bf16 v[74:77], v[178:181], v[218:221], v[74:77]
	v_mfma_f32_16x16x32_bf16 v[66:69], v[186:189], v[218:221], v[66:69]
	s_setprio 0
	s_barrier
	s_add_i32 s0, s80, s49
	v_lshl_add_u64 v[222:223], s[44:45], 0, v[134:135]
	s_mov_b32 m0, s0
	ds_read_b128 v[190:193], v157 offset:16384
	ds_read_b128 v[194:197], v157 offset:17408
	ds_read_b128 v[198:201], v157 offset:18432
	ds_read_b128 v[202:205], v157 offset:19456
	ds_read_b128 v[206:209], v157 offset:20480
	ds_read_b128 v[210:213], v157 offset:21504
	ds_read_b128 v[214:217], v157 offset:22528
	ds_read_b128 v[218:221], v157 offset:23552
	global_load_lds_dwordx4 v[222:223], off
	s_add_i32 m0, s0, 0x2000
	s_add_u32 s4, s44, 0x40000
	v_lshl_add_u64 v[224:225], s[44:45], 0, v[130:131]
	s_addc_u32 s5, s45, 0
	s_add_i32 s0, s81, s49
	global_load_lds_dwordx4 v[224:225], off
	v_lshl_add_u64 v[226:227], s[4:5], 0, v[134:135]
	s_mov_b32 m0, s0
	v_lshl_add_u64 v[228:229], s[46:47], 0, v[132:133]
	global_load_lds_dwordx4 v[226:227], off
	v_lshl_add_u64 v[226:227], s[4:5], 0, v[130:131]
	s_add_i32 m0, s0, 0x2000
	s_nop 0
	global_load_lds_dwordx4 v[226:227], off
	v_lshl_add_u64 v[226:227], s[46:47], 0, v[136:137]
	s_mov_b32 m0, s41
	s_nop 0
	global_load_lds_dwordx4 v[226:227], off
	s_mov_b32 m0, s72
	s_nop 0
	global_load_lds_dwordx4 v[228:229], off
	s_waitcnt vmcnt(8)
	s_waitcnt lgkmcnt(0)
	s_barrier
	s_setprio 3
	v_mfma_f32_16x16x32_bf16 v[62:65], v[146:149], v[190:193], v[62:65]
	v_mfma_f32_16x16x32_bf16 v[58:61], v[166:169], v[190:193], v[58:61]
	v_mfma_f32_16x16x32_bf16 v[50:53], v[146:149], v[198:201], v[50:53]
	v_mfma_f32_16x16x32_bf16 v[42:45], v[166:169], v[198:201], v[42:45]
	v_mfma_f32_16x16x32_bf16 v[34:37], v[146:149], v[206:209], v[34:37]
	v_mfma_f32_16x16x32_bf16 v[26:29], v[166:169], v[206:209], v[26:29]
	v_mfma_f32_16x16x32_bf16 v[14:17], v[146:149], v[214:217], v[14:17]
	v_mfma_f32_16x16x32_bf16 v[6:9], v[166:169], v[214:217], v[6:9]
	v_mfma_f32_16x16x32_bf16 v[62:65], v[158:161], v[194:197], v[62:65]
	v_mfma_f32_16x16x32_bf16 v[58:61], v[170:173], v[194:197], v[58:61]
	v_mfma_f32_16x16x32_bf16 v[50:53], v[158:161], v[202:205], v[50:53]
	v_mfma_f32_16x16x32_bf16 v[42:45], v[170:173], v[202:205], v[42:45]
	v_mfma_f32_16x16x32_bf16 v[34:37], v[158:161], v[210:213], v[34:37]
	v_mfma_f32_16x16x32_bf16 v[26:29], v[170:173], v[210:213], v[26:29]
	v_mfma_f32_16x16x32_bf16 v[14:17], v[158:161], v[218:221], v[14:17]
	v_mfma_f32_16x16x32_bf16 v[6:9], v[170:173], v[218:221], v[6:9]
	v_mfma_f32_16x16x32_bf16 v[54:57], v[174:177], v[190:193], v[54:57]
	v_mfma_f32_16x16x32_bf16 v[46:49], v[182:185], v[190:193], v[46:49]
	v_mfma_f32_16x16x32_bf16 v[38:41], v[174:177], v[198:201], v[38:41]
	v_mfma_f32_16x16x32_bf16 v[30:33], v[182:185], v[198:201], v[30:33]
	v_mfma_f32_16x16x32_bf16 v[22:25], v[174:177], v[206:209], v[22:25]
	v_mfma_f32_16x16x32_bf16 v[18:21], v[182:185], v[206:209], v[18:21]
	v_mfma_f32_16x16x32_bf16 v[10:13], v[174:177], v[214:217], v[10:13]
	v_mfma_f32_16x16x32_bf16 v[2:5], v[182:185], v[214:217], v[2:5]
	v_mfma_f32_16x16x32_bf16 v[54:57], v[178:181], v[194:197], v[54:57]
	v_mfma_f32_16x16x32_bf16 v[46:49], v[186:189], v[194:197], v[46:49]
	v_mfma_f32_16x16x32_bf16 v[38:41], v[178:181], v[202:205], v[38:41]
	v_mfma_f32_16x16x32_bf16 v[30:33], v[186:189], v[202:205], v[30:33]
	v_mfma_f32_16x16x32_bf16 v[22:25], v[178:181], v[210:213], v[22:25]
	v_mfma_f32_16x16x32_bf16 v[18:21], v[186:189], v[210:213], v[18:21]
	v_mfma_f32_16x16x32_bf16 v[10:13], v[178:181], v[218:221], v[10:13]
	v_mfma_f32_16x16x32_bf16 v[2:5], v[186:189], v[218:221], v[2:5]
	s_setprio 0
	s_barrier
; #define PG8_STAGE(bufoff, gbase, voff) do { _Pragma("unroll") for (int _i = 0; _i < 2; ++_i) \
;         __builtin_amdgcn_global_load_lds((const unsigned*)((const char*)(gbase) + (voff)[_i]), (PG8_LAS unsigned*)(lds + (bufoff) + ldsw + _i * 8192), 16, 0, 0); } while (0)
; #define PG8_LDA(dst, b, h) do { _Pragma("unroll") for (int m = 0; m < 4; ++m) Frag<F8>::load(dst[m], lds + PG8_SA(b, h) + aoff + m * 2048); } while (0)
; #define PG8_LDB(dst, b, h) do { _Pragma("unroll") for (int n = 0; n < 2; ++n) Frag<F8>::load(dst[n], lds + PG8_SB(b, h) + boff + n * 2048); } while (0)
; #define PG8_MMA(ai, bj, At, Bt) do { __builtin_amdgcn_s_setprio(3); _Pragma("unroll") for (int m = 0; m < 4; ++m) _Pragma("unroll") for (int n = 0; n < 2; ++n) Frag<F8>::mma(acc[ai][bj][m][n], Bt[n], At[m]); \
;         __builtin_amdgcn_s_setprio(0); } while (0)
; #define PG8_WAIT_V(n) asm volatile("s_waitcnt vmcnt(" #n ")" ::: "memory")
; #define PG8_WAIT_L(n) asm volatile("s_waitcnt lgkmcnt(" #n ")" ::: "memory")
; #define PG8_BAR __builtin_amdgcn_s_barrier()
; #define PG8_SCHED __builtin_amdgcn_sched_barrier(0)
; template <class Epi, class Sched, bool ALIGN_EPI = false, bool SP2 = false, bool F8 = false>
; __device__ __forceinline__ void gemm_phase(PG8_LAS unsigned char* lds, const Gemm g, const Sched& S, const Epi& E) {
;     ...
;             PG8_LDB(B0, 1, 0); PG8_LDB(B1, 1, 1); PG8_SCHED; PG8_LDA(At, 1, 0); PG8_STAGE(PG8_SA(0, 1), a2 + hstep, voffA);
;             PG8_WAIT_V(8); PG8_WAIT_L(0); PG8_BAR; PG8_MMA(0, 0, At, B0); PG8_MMA(0, 1, At, B1); PG8_BAR; PG8_SCHED;
;             PG8_LDA(At, 1, 1); PG8_STAGE(PG8_SB(1, 0), b3, voffB); PG8_STAGE(PG8_SB(1, 1), b3 + hstep, voffB); PG8_STAGE(PG8_SA(1, 0), a3, voffA);
;             PG8_WAIT_V(8); PG8_WAIT_L(0); PG8_BAR; PG8_MMA(1, 0, At, B0); PG8_MMA(1, 1, At, B1); PG8_BAR; PG8_SCHED;
	s_add_i32 s0, 0, 0x18000
	v_add_u32_e32 v165, s0, v151
	s_add_i32 s1, 0, 0x1c000
	ds_read_b128 v[146:149], v165
	ds_read_b128 v[158:161], v165 offset:1024
	ds_read_b128 v[166:169], v165 offset:2048
	ds_read_b128 v[170:173], v165 offset:3072
	v_add_u32_e32 v165, s1, v151
	ds_read_b128 v[174:177], v165
	ds_read_b128 v[178:181], v165 offset:1024
	ds_read_b128 v[182:185], v165 offset:2048
	ds_read_b128 v[186:189], v165 offset:3072
	s_add_u32 s4, s46, 0x40000
	s_addc_u32 s5, s47, 0
	s_mov_b32 m0, s73
	v_lshl_add_u64 v[230:231], s[4:5], 0, v[136:137]
	ds_read_b128 v[190:193], v157 offset:32768
	ds_read_b128 v[194:197], v157 offset:33792
	ds_read_b128 v[198:201], v157 offset:34816
	ds_read_b128 v[202:205], v157 offset:35840
	ds_read_b128 v[206:209], v157 offset:36864
	ds_read_b128 v[210:213], v157 offset:37888
	ds_read_b128 v[214:217], v157 offset:38912
	ds_read_b128 v[218:221], v157 offset:39936
	global_load_lds_dwordx4 v[230:231], off
	v_lshl_add_u64 v[230:231], s[4:5], 0, v[132:133]
	s_mov_b32 m0, s74
	s_nop 0
	global_load_lds_dwordx4 v[230:231], off
	s_waitcnt vmcnt(8)
	s_waitcnt lgkmcnt(0)
	s_barrier
	s_setprio 3
	v_mfma_f32_16x16x32_bf16 v[126:129], v[146:149], v[190:193], v[126:129]
	v_mfma_f32_16x16x32_bf16 v[118:121], v[166:169], v[190:193], v[118:121]
	v_mfma_f32_16x16x32_bf16 v[110:113], v[146:149], v[198:201], v[110:113]
	v_mfma_f32_16x16x32_bf16 v[102:105], v[166:169], v[198:201], v[102:105]
	v_mfma_f32_16x16x32_bf16 v[94:97], v[146:149], v[206:209], v[94:97]
	v_mfma_f32_16x16x32_bf16 v[86:89], v[166:169], v[206:209], v[86:89]
	v_mfma_f32_16x16x32_bf16 v[78:81], v[146:149], v[214:217], v[78:81]
	v_mfma_f32_16x16x32_bf16 v[70:73], v[166:169], v[214:217], v[70:73]
	v_mfma_f32_16x16x32_bf16 v[126:129], v[158:161], v[194:197], v[126:129]
	v_mfma_f32_16x16x32_bf16 v[118:121], v[170:173], v[194:197], v[118:121]
	v_mfma_f32_16x16x32_bf16 v[110:113], v[158:161], v[202:205], v[110:113]
	v_mfma_f32_16x16x32_bf16 v[102:105], v[170:173], v[202:205], v[102:105]
	v_mfma_f32_16x16x32_bf16 v[94:97], v[158:161], v[210:213], v[94:97]
	v_mfma_f32_16x16x32_bf16 v[86:89], v[170:173], v[210:213], v[86:89]
	v_mfma_f32_16x16x32_bf16 v[78:81], v[158:161], v[218:221], v[78:81]
	v_mfma_f32_16x16x32_bf16 v[70:73], v[170:173], v[218:221], v[70:73]
	v_mfma_f32_16x16x32_bf16 v[122:125], v[174:177], v[190:193], v[122:125]
	v_mfma_f32_16x16x32_bf16 v[114:117], v[182:185], v[190:193], v[114:117]
	v_mfma_f32_16x16x32_bf16 v[106:109], v[174:177], v[198:201], v[106:109]
	v_mfma_f32_16x16x32_bf16 v[98:101], v[182:185], v[198:201], v[98:101]
	v_mfma_f32_16x16x32_bf16 v[90:93], v[174:177], v[206:209], v[90:93]
	v_mfma_f32_16x16x32_bf16 v[82:85], v[182:185], v[206:209], v[82:85]
	v_mfma_f32_16x16x32_bf16 v[74:77], v[174:177], v[214:217], v[74:77]
	v_mfma_f32_16x16x32_bf16 v[66:69], v[182:185], v[214:217], v[66:69]
	v_mfma_f32_16x16x32_bf16 v[122:125], v[178:181], v[194:197], v[122:125]
	v_mfma_f32_16x16x32_bf16 v[114:117], v[186:189], v[194:197], v[114:117]
	v_mfma_f32_16x16x32_bf16 v[106:109], v[178:181], v[202:205], v[106:109]
	v_mfma_f32_16x16x32_bf16 v[98:101], v[186:189], v[202:205], v[98:101]
	v_mfma_f32_16x16x32_bf16 v[90:93], v[178:181], v[210:213], v[90:93]
	v_mfma_f32_16x16x32_bf16 v[82:85], v[186:189], v[210:213], v[82:85]
	v_mfma_f32_16x16x32_bf16 v[74:77], v[178:181], v[218:221], v[74:77]
	v_mfma_f32_16x16x32_bf16 v[66:69], v[186:189], v[218:221], v[66:69]
	s_setprio 0
	s_barrier
	s_add_i32 s0, s0, s49
	v_lshl_add_u64 v[222:223], v[222:223], 0, s[18:19]
	s_mov_b32 m0, s0
	ds_read_b128 v[190:193], v157 offset:49152
	ds_read_b128 v[194:197], v157 offset:50176
	ds_read_b128 v[198:201], v157 offset:51200
	ds_read_b128 v[202:205], v157 offset:52224
	ds_read_b128 v[206:209], v157 offset:53248
	ds_read_b128 v[210:213], v157 offset:54272
	ds_read_b128 v[214:217], v157 offset:55296
	ds_read_b128 v[218:221], v157 offset:56320
	global_load_lds_dwordx4 v[222:223], off
	s_add_i32 m0, s0, 0x2000
	s_add_u32 s4, s44, 0x40080
	v_lshl_add_u64 v[222:223], v[224:225], 0, s[18:19]
	s_addc_u32 s5, s45, 0
	s_add_i32 s0, s1, s49
	global_load_lds_dwordx4 v[222:223], off
	v_lshl_add_u64 v[222:223], s[4:5], 0, v[134:135]
	s_mov_b32 m0, s0
	s_nop 0
	global_load_lds_dwordx4 v[222:223], off
	v_lshl_add_u64 v[222:223], s[4:5], 0, v[130:131]
	s_add_i32 m0, s0, 0x2000
	s_nop 0
	global_load_lds_dwordx4 v[222:223], off
	v_lshl_add_u64 v[222:223], v[226:227], 0, s[18:19]
	s_mov_b32 m0, s75
	s_nop 0
	global_load_lds_dwordx4 v[222:223], off
	v_lshl_add_u64 v[222:223], v[228:229], 0, s[18:19]
	s_mov_b32 m0, s79
	s_nop 0
	global_load_lds_dwordx4 v[222:223], off
	s_waitcnt vmcnt(8)
	s_waitcnt lgkmcnt(0)
	s_barrier
	s_setprio 3
	v_mfma_f32_16x16x32_bf16 v[62:65], v[146:149], v[190:193], v[62:65]
	v_mfma_f32_16x16x32_bf16 v[58:61], v[166:169], v[190:193], v[58:61]
	v_mfma_f32_16x16x32_bf16 v[50:53], v[146:149], v[198:201], v[50:53]
	v_mfma_f32_16x16x32_bf16 v[42:45], v[166:169], v[198:201], v[42:45]
	v_mfma_f32_16x16x32_bf16 v[34:37], v[146:149], v[206:209], v[34:37]
	v_mfma_f32_16x16x32_bf16 v[26:29], v[166:169], v[206:209], v[26:29]
	v_mfma_f32_16x16x32_bf16 v[14:17], v[146:149], v[214:217], v[14:17]
	v_mfma_f32_16x16x32_bf16 v[6:9], v[166:169], v[214:217], v[6:9]
	v_mfma_f32_16x16x32_bf16 v[62:65], v[158:161], v[194:197], v[62:65]
	v_mfma_f32_16x16x32_bf16 v[58:61], v[170:173], v[194:197], v[58:61]
	v_mfma_f32_16x16x32_bf16 v[50:53], v[158:161], v[202:205], v[50:53]
	v_mfma_f32_16x16x32_bf16 v[42:45], v[170:173], v[202:205], v[42:45]
	v_mfma_f32_16x16x32_bf16 v[34:37], v[158:161], v[210:213], v[34:37]
	v_mfma_f32_16x16x32_bf16 v[26:29], v[170:173], v[210:213], v[26:29]
	v_mfma_f32_16x16x32_bf16 v[14:17], v[158:161], v[218:221], v[14:17]
	v_mfma_f32_16x16x32_bf16 v[6:9], v[170:173], v[218:221], v[6:9]
	v_mfma_f32_16x16x32_bf16 v[54:57], v[174:177], v[190:193], v[54:57]
	v_mfma_f32_16x16x32_bf16 v[46:49], v[182:185], v[190:193], v[46:49]
	v_mfma_f32_16x16x32_bf16 v[38:41], v[174:177], v[198:201], v[38:41]
	v_mfma_f32_16x16x32_bf16 v[30:33], v[182:185], v[198:201], v[30:33]
	v_mfma_f32_16x16x32_bf16 v[22:25], v[174:177], v[206:209], v[22:25]
	v_mfma_f32_16x16x32_bf16 v[18:21], v[182:185], v[206:209], v[18:21]
	v_mfma_f32_16x16x32_bf16 v[10:13], v[174:177], v[214:217], v[10:13]
	v_mfma_f32_16x16x32_bf16 v[2:5], v[182:185], v[214:217], v[2:5]
	v_mfma_f32_16x16x32_bf16 v[54:57], v[178:181], v[194:197], v[54:57]
	v_mfma_f32_16x16x32_bf16 v[46:49], v[186:189], v[194:197], v[46:49]
	v_mfma_f32_16x16x32_bf16 v[38:41], v[178:181], v[202:205], v[38:41]
	v_mfma_f32_16x16x32_bf16 v[30:33], v[186:189], v[202:205], v[30:33]
	v_mfma_f32_16x16x32_bf16 v[22:25], v[178:181], v[210:213], v[22:25]
	v_mfma_f32_16x16x32_bf16 v[18:21], v[186:189], v[210:213], v[18:21]
	v_mfma_f32_16x16x32_bf16 v[10:13], v[178:181], v[218:221], v[10:13]
	v_mfma_f32_16x16x32_bf16 v[2:5], v[186:189], v[218:221], v[2:5]
	s_setprio 0
	s_barrier
	s_add_i32 s86, s86, 2
	s_add_u32 s42, s42, 0x100
	s_addc_u32 s43, s43, 0
	s_add_u32 s84, s84, 0x100
	s_addc_u32 s85, s85, 0
	s_cmp_gt_u32 s86, 13
	s_cbranch_scc0 .LBB0_562

; #define PG8_STAGE(bufoff, gbase, voff) do { _Pragma("unroll") for (int _i = 0; _i < 2; ++_i) \
;         __builtin_amdgcn_global_load_lds((const unsigned*)((const char*)(gbase) + (voff)[_i]), (PG8_LAS unsigned*)(lds + (bufoff) + ldsw + _i * 8192), 16, 0, 0); } while (0)
; #define PG8_LDA(dst, b, h) do { _Pragma("unroll") for (int m = 0; m < 4; ++m) Frag<F8>::load(dst[m], lds + PG8_SA(b, h) + aoff + m * 2048); } while (0)
; #define PG8_LDB(dst, b, h) do { _Pragma("unroll") for (int n = 0; n < 2; ++n) Frag<F8>::load(dst[n], lds + PG8_SB(b, h) + boff + n * 2048); } while (0)
; #define PG8_MMA(ai, bj, At, Bt) do { __builtin_amdgcn_s_setprio(3); _Pragma("unroll") for (int m = 0; m < 4; ++m) _Pragma("unroll") for (int n = 0; n < 2; ++n) Frag<F8>::mma(acc[ai][bj][m][n], Bt[n], At[m]); \
;         __builtin_amdgcn_s_setprio(0); } while (0)
; #define PG8_WAIT_V(n) asm volatile("s_waitcnt vmcnt(" #n ")" ::: "memory")
; #define PG8_WAIT_L(n) asm volatile("s_waitcnt lgkmcnt(" #n ")" ::: "memory")
; #define PG8_BAR __builtin_amdgcn_s_barrier()
; #define PG8_SCHED __builtin_amdgcn_sched_barrier(0)
; template <class Epi, class Sched, bool ALIGN_EPI = false, bool SP2 = false, bool F8 = false>
; __device__ __forceinline__ void gemm_phase(PG8_LAS unsigned char* lds, const Gemm g, const Sched& S, const Epi& E) {
;     ...
;         for (int t = 0; t < nt; t += 2) {
;             const bool last = (t == nt - 2);
;             const char* a1 = cA + (size_t)(t + 1) * kstep;
;             const char* a2 = last ? nA : cA + (size_t)(t + 2) * kstep; const char* b2 = last ? nB : cB + (size_t)(t + 2) * kstep;
;             const char* a3 = a2 + kstep; const char* b3 = b2 + kstep;
;             if (last && has_next) S.a_ready(nxt);
;             if constexpr (SP2) {
;             PG8_LDB(B0, 0, 0); PG8_LDB(B1, 0, 1); PG8_SCHED; PG8_LDA(At, 0, 0); PG8_STAGE(PG8_SA(1, 1), a1 + hstep, voffA);
;             PG8_WAIT_V(8); PG8_WAIT_L(0); PG8_BAR; PG8_MMA(0, 0, At, B0); PG8_MMA(0, 1, At, B1); PG8_BAR; PG8_SCHED;
;             PG8_LDA(At, 0, 1); PG8_STAGE(PG8_SB(0, 0), b2, voffB); PG8_STAGE(PG8_SB(0, 1), b2 + hstep, voffB); PG8_STAGE(PG8_SA(0, 0), a2, voffA);
;             PG8_WAIT_V(8); PG8_WAIT_L(0); PG8_BAR; PG8_MMA(1, 0, At, B0); PG8_MMA(1, 1, At, B1); PG8_BAR; PG8_SCHED;
.LBB0_674:
	v_add_u32_e32 v186, s90, v158
	v_add_u32_e32 v202, s91, v158
	s_add_u32 s0, s36, s50
	ds_read_b128 v[174:177], v186
	ds_read_b128 v[178:181], v186 offset:1024
	ds_read_b128 v[182:185], v186 offset:2048
	ds_read_b128 v[186:189], v186 offset:3072
	ds_read_b128 v[190:193], v202
	ds_read_b128 v[194:197], v202 offset:1024
	ds_read_b128 v[198:201], v202 offset:2048
	ds_read_b128 v[202:205], v202 offset:3072
	s_addc_u32 s1, s37, s51
	s_add_u32 s0, s0, 0x100
	s_addc_u32 s1, s1, 0
	s_add_u32 s4, s47, s50
	s_addc_u32 s5, s96, s51
	s_cmpk_eq_i32 s50, 0x1b00
	s_cselect_b32 s71, s49, s1
	s_cselect_b32 s70, s48, s0
	s_cselect_b32 s53, s17, s5
	s_cselect_b32 s52, s16, s4
	v_lshl_add_u64 v[238:239], v[146:147], 0, s[50:51]
	s_add_i32 m0, s83, 0xc000
	ds_read_b128 v[206:209], v160
	ds_read_b128 v[210:213], v160 offset:1024
	ds_read_b128 v[214:217], v160 offset:2048
	ds_read_b128 v[218:221], v160 offset:3072
	ds_read_b128 v[222:225], v160 offset:4096
	ds_read_b128 v[226:229], v160 offset:5120
	ds_read_b128 v[230:233], v160 offset:6144
	ds_read_b128 v[234:237], v160 offset:7168
	global_load_lds_dwordx4 v[238:239], off
	v_lshl_add_u64 v[238:239], v[148:149], 0, s[50:51]
	s_add_i32 m0, s83, 0xe000
	s_nop 0
	global_load_lds_dwordx4 v[238:239], off
	s_waitcnt vmcnt(8)
	s_waitcnt lgkmcnt(0)
	s_barrier
	s_setprio 3
	v_mfma_f32_16x16x32_bf16 v[22:25], v[174:177], v[206:209], v[22:25]
	v_mfma_f32_16x16x32_bf16 v[30:33], v[182:185], v[206:209], v[30:33]
	v_mfma_f32_16x16x32_bf16 v[46:49], v[174:177], v[214:217], v[46:49]
	v_mfma_f32_16x16x32_bf16 v[54:57], v[182:185], v[214:217], v[54:57]
	v_mfma_f32_16x16x32_bf16 v[78:81], v[174:177], v[222:225], v[78:81]
	v_mfma_f32_16x16x32_bf16 v[86:89], v[182:185], v[222:225], v[86:89]
	v_mfma_f32_16x16x32_bf16 v[98:101], v[174:177], v[230:233], v[98:101]
	v_mfma_f32_16x16x32_bf16 v[102:105], v[182:185], v[230:233], v[102:105]
	v_mfma_f32_16x16x32_bf16 v[22:25], v[178:181], v[210:213], v[22:25]
	v_mfma_f32_16x16x32_bf16 v[30:33], v[186:189], v[210:213], v[30:33]
	v_mfma_f32_16x16x32_bf16 v[46:49], v[178:181], v[218:221], v[46:49]
	v_mfma_f32_16x16x32_bf16 v[54:57], v[186:189], v[218:221], v[54:57]
	v_mfma_f32_16x16x32_bf16 v[78:81], v[178:181], v[226:229], v[78:81]
	v_mfma_f32_16x16x32_bf16 v[86:89], v[186:189], v[226:229], v[86:89]
	v_mfma_f32_16x16x32_bf16 v[98:101], v[178:181], v[234:237], v[98:101]
	v_mfma_f32_16x16x32_bf16 v[102:105], v[186:189], v[234:237], v[102:105]
	v_mfma_f32_16x16x32_bf16 v[2:5], v[190:193], v[206:209], v[2:5]
	v_mfma_f32_16x16x32_bf16 v[6:9], v[198:201], v[206:209], v[6:9]
	v_mfma_f32_16x16x32_bf16 v[10:13], v[190:193], v[214:217], v[10:13]
	v_mfma_f32_16x16x32_bf16 v[14:17], v[198:201], v[214:217], v[14:17]
	v_mfma_f32_16x16x32_bf16 v[34:37], v[190:193], v[222:225], v[34:37]
	v_mfma_f32_16x16x32_bf16 v[38:41], v[198:201], v[222:225], v[38:41]
	v_mfma_f32_16x16x32_bf16 v[58:61], v[190:193], v[230:233], v[58:61]
	v_mfma_f32_16x16x32_bf16 v[62:65], v[198:201], v[230:233], v[62:65]
	v_mfma_f32_16x16x32_bf16 v[2:5], v[194:197], v[210:213], v[2:5]
	v_mfma_f32_16x16x32_bf16 v[6:9], v[202:205], v[210:213], v[6:9]
	v_mfma_f32_16x16x32_bf16 v[10:13], v[194:197], v[218:221], v[10:13]
	v_mfma_f32_16x16x32_bf16 v[14:17], v[202:205], v[218:221], v[14:17]
	v_mfma_f32_16x16x32_bf16 v[34:37], v[194:197], v[226:229], v[34:37]
	v_mfma_f32_16x16x32_bf16 v[38:41], v[202:205], v[226:229], v[38:41]
	v_mfma_f32_16x16x32_bf16 v[58:61], v[194:197], v[234:237], v[58:61]
	v_mfma_f32_16x16x32_bf16 v[62:65], v[202:205], v[234:237], v[62:65]
	s_setprio 0
	s_barrier
	s_add_i32 s0, s90, s75
	v_lshl_add_u64 v[238:239], s[52:53], 0, v[132:133]
	s_mov_b32 m0, s0
	ds_read_b128 v[206:209], v160 offset:16384
	ds_read_b128 v[210:213], v160 offset:17408
	ds_read_b128 v[214:217], v160 offset:18432
	ds_read_b128 v[218:221], v160 offset:19456
	ds_read_b128 v[222:225], v160 offset:20480
	ds_read_b128 v[226:229], v160 offset:21504
	ds_read_b128 v[230:233], v160 offset:22528
	ds_read_b128 v[234:237], v160 offset:23552
	global_load_lds_dwordx4 v[238:239], off
	s_add_i32 m0, s0, 0x2000
	s_add_u32 s4, s52, 0xe0000
	v_lshl_add_u64 v[240:241], s[52:53], 0, v[136:137]
	s_addc_u32 s5, s53, 0
	s_add_i32 s0, s91, s75
	global_load_lds_dwordx4 v[240:241], off
	v_lshl_add_u64 v[242:243], s[4:5], 0, v[132:133]
	s_mov_b32 m0, s0
	v_lshl_add_u64 v[244:245], s[70:71], 0, v[134:135]
	global_load_lds_dwordx4 v[242:243], off
	v_lshl_add_u64 v[242:243], s[4:5], 0, v[136:137]
	s_add_i32 m0, s0, 0x2000
	s_nop 0
	global_load_lds_dwordx4 v[242:243], off
	v_lshl_add_u64 v[242:243], s[70:71], 0, v[130:131]
	s_mov_b32 m0, s83
	s_nop 0
	global_load_lds_dwordx4 v[242:243], off
	s_mov_b32 m0, s84
	s_nop 0
	global_load_lds_dwordx4 v[244:245], off
	s_waitcnt vmcnt(8)
	s_waitcnt lgkmcnt(0)
	s_barrier
; #define PG8_STAGE(bufoff, gbase, voff) do { _Pragma("unroll") for (int _i = 0; _i < 2; ++_i) \
;         __builtin_amdgcn_global_load_lds((const unsigned*)((const char*)(gbase) + (voff)[_i]), (PG8_LAS unsigned*)(lds + (bufoff) + ldsw + _i * 8192), 16, 0, 0); } while (0)
; #define PG8_LDA(dst, b, h) do { _Pragma("unroll") for (int m = 0; m < 4; ++m) Frag<F8>::load(dst[m], lds + PG8_SA(b, h) + aoff + m * 2048); } while (0)
; #define PG8_LDB(dst, b, h) do { _Pragma("unroll") for (int n = 0; n < 2; ++n) Frag<F8>::load(dst[n], lds + PG8_SB(b, h) + boff + n * 2048); } while (0)
; #define PG8_MMA(ai, bj, At, Bt) do { __builtin_amdgcn_s_setprio(3); _Pragma("unroll") for (int m = 0; m < 4; ++m) _Pragma("unroll") for (int n = 0; n < 2; ++n) Frag<F8>::mma(acc[ai][bj][m][n], Bt[n], At[m]); \
;         __builtin_amdgcn_s_setprio(0); } while (0)
; #define PG8_WAIT_V(n) asm volatile("s_waitcnt vmcnt(" #n ")" ::: "memory")
; #define PG8_WAIT_L(n) asm volatile("s_waitcnt lgkmcnt(" #n ")" ::: "memory")
; #define PG8_BAR __builtin_amdgcn_s_barrier()
; #define PG8_SCHED __builtin_amdgcn_sched_barrier(0)
; template <class Epi, class Sched, bool ALIGN_EPI = false, bool SP2 = false, bool F8 = false>
; __device__ __forceinline__ void gemm_phase(PG8_LAS unsigned char* lds, const Gemm g, const Sched& S, const Epi& E) {
;     ...
;             PG8_WAIT_V(8); PG8_WAIT_L(0); PG8_BAR; PG8_MMA(1, 0, At, B0); PG8_MMA(1, 1, At, B1); PG8_BAR; PG8_SCHED;
;             PG8_LDB(B0, 1, 0); PG8_LDB(B1, 1, 1); PG8_SCHED; PG8_LDA(At, 1, 0); PG8_STAGE(PG8_SA(0, 1), a2 + hstep, voffA);
;             PG8_WAIT_V(8); PG8_WAIT_L(0); PG8_BAR; PG8_MMA(0, 0, At, B0); PG8_MMA(0, 1, At, B1); PG8_BAR; PG8_SCHED;
	s_setprio 3
	v_mfma_f32_16x16x32_bf16 v[66:69], v[174:177], v[206:209], v[66:69]
	v_mfma_f32_16x16x32_bf16 v[70:73], v[182:185], v[206:209], v[70:73]
	v_mfma_f32_16x16x32_bf16 v[90:93], v[174:177], v[214:217], v[90:93]
	v_mfma_f32_16x16x32_bf16 v[94:97], v[182:185], v[214:217], v[94:97]
	v_mfma_f32_16x16x32_bf16 v[106:109], v[174:177], v[222:225], v[106:109]
	v_mfma_f32_16x16x32_bf16 v[110:113], v[182:185], v[222:225], v[110:113]
	v_mfma_f32_16x16x32_bf16 v[114:117], v[174:177], v[230:233], v[114:117]
	v_mfma_f32_16x16x32_bf16 v[126:129], v[182:185], v[230:233], v[126:129]
	v_mfma_f32_16x16x32_bf16 v[66:69], v[178:181], v[210:213], v[66:69]
	v_mfma_f32_16x16x32_bf16 v[70:73], v[186:189], v[210:213], v[70:73]
	v_mfma_f32_16x16x32_bf16 v[90:93], v[178:181], v[218:221], v[90:93]
	v_mfma_f32_16x16x32_bf16 v[94:97], v[186:189], v[218:221], v[94:97]
	v_mfma_f32_16x16x32_bf16 v[106:109], v[178:181], v[226:229], v[106:109]
	v_mfma_f32_16x16x32_bf16 v[110:113], v[186:189], v[226:229], v[110:113]
	v_mfma_f32_16x16x32_bf16 v[114:117], v[178:181], v[234:237], v[114:117]
	v_mfma_f32_16x16x32_bf16 v[126:129], v[186:189], v[234:237], v[126:129]
	v_mfma_f32_16x16x32_bf16 v[18:21], v[190:193], v[206:209], v[18:21]
	v_mfma_f32_16x16x32_bf16 v[26:29], v[198:201], v[206:209], v[26:29]
	v_mfma_f32_16x16x32_bf16 v[42:45], v[190:193], v[214:217], v[42:45]
	v_mfma_f32_16x16x32_bf16 v[50:53], v[198:201], v[214:217], v[50:53]
	v_mfma_f32_16x16x32_bf16 v[74:77], v[190:193], v[222:225], v[74:77]
	v_mfma_f32_16x16x32_bf16 v[82:85], v[198:201], v[222:225], v[82:85]
	v_mfma_f32_16x16x32_bf16 v[122:125], v[190:193], v[230:233], v[122:125]
	v_mfma_f32_16x16x32_bf16 v[118:121], v[198:201], v[230:233], v[118:121]
	v_mfma_f32_16x16x32_bf16 v[18:21], v[194:197], v[210:213], v[18:21]
	v_mfma_f32_16x16x32_bf16 v[26:29], v[202:205], v[210:213], v[26:29]
	v_mfma_f32_16x16x32_bf16 v[42:45], v[194:197], v[218:221], v[42:45]
	v_mfma_f32_16x16x32_bf16 v[50:53], v[202:205], v[218:221], v[50:53]
	v_mfma_f32_16x16x32_bf16 v[74:77], v[194:197], v[226:229], v[74:77]
	v_mfma_f32_16x16x32_bf16 v[82:85], v[202:205], v[226:229], v[82:85]
	v_mfma_f32_16x16x32_bf16 v[122:125], v[194:197], v[234:237], v[122:125]
	v_mfma_f32_16x16x32_bf16 v[118:121], v[202:205], v[234:237], v[118:121]
	s_setprio 0
	s_barrier
	s_add_i32 s0, 0, 0x18000
	s_add_i32 s1, 0, 0x1c000
	v_add_u32_e32 v186, s0, v158
	v_add_u32_e32 v202, s1, v158
	ds_read_b128 v[174:177], v186
	ds_read_b128 v[178:181], v186 offset:1024
	ds_read_b128 v[182:185], v186 offset:2048
	ds_read_b128 v[186:189], v186 offset:3072
	ds_read_b128 v[190:193], v202
	ds_read_b128 v[194:197], v202 offset:1024
	ds_read_b128 v[198:201], v202 offset:2048
	ds_read_b128 v[202:205], v202 offset:3072
	s_add_u32 s4, s70, 0xe0000
	s_addc_u32 s5, s71, 0
	s_mov_b32 m0, s85
	v_lshl_add_u64 v[246:247], s[4:5], 0, v[130:131]
	ds_read_b128 v[206:209], v160 offset:32768
	ds_read_b128 v[210:213], v160 offset:33792
	ds_read_b128 v[214:217], v160 offset:34816
	ds_read_b128 v[218:221], v160 offset:35840
	ds_read_b128 v[222:225], v160 offset:36864
	ds_read_b128 v[226:229], v160 offset:37888
	ds_read_b128 v[230:233], v160 offset:38912
	ds_read_b128 v[234:237], v160 offset:39936
	global_load_lds_dwordx4 v[246:247], off
	v_lshl_add_u64 v[246:247], s[4:5], 0, v[134:135]
	s_mov_b32 m0, s86
	s_nop 0
	global_load_lds_dwordx4 v[246:247], off
	s_waitcnt vmcnt(8)
	s_waitcnt lgkmcnt(0)
	s_barrier
	s_setprio 3
	v_mfma_f32_16x16x32_bf16 v[22:25], v[174:177], v[206:209], v[22:25]
	v_mfma_f32_16x16x32_bf16 v[30:33], v[182:185], v[206:209], v[30:33]
	v_mfma_f32_16x16x32_bf16 v[46:49], v[174:177], v[214:217], v[46:49]
	v_mfma_f32_16x16x32_bf16 v[54:57], v[182:185], v[214:217], v[54:57]
	v_mfma_f32_16x16x32_bf16 v[78:81], v[174:177], v[222:225], v[78:81]
	v_mfma_f32_16x16x32_bf16 v[86:89], v[182:185], v[222:225], v[86:89]
	v_mfma_f32_16x16x32_bf16 v[98:101], v[174:177], v[230:233], v[98:101]
	v_mfma_f32_16x16x32_bf16 v[102:105], v[182:185], v[230:233], v[102:105]
	v_mfma_f32_16x16x32_bf16 v[22:25], v[178:181], v[210:213], v[22:25]
	v_mfma_f32_16x16x32_bf16 v[30:33], v[186:189], v[210:213], v[30:33]
	v_mfma_f32_16x16x32_bf16 v[46:49], v[178:181], v[218:221], v[46:49]
	v_mfma_f32_16x16x32_bf16 v[54:57], v[186:189], v[218:221], v[54:57]
	v_mfma_f32_16x16x32_bf16 v[78:81], v[178:181], v[226:229], v[78:81]
	v_mfma_f32_16x16x32_bf16 v[86:89], v[186:189], v[226:229], v[86:89]
	v_mfma_f32_16x16x32_bf16 v[98:101], v[178:181], v[234:237], v[98:101]
	v_mfma_f32_16x16x32_bf16 v[102:105], v[186:189], v[234:237], v[102:105]
	v_mfma_f32_16x16x32_bf16 v[2:5], v[190:193], v[206:209], v[2:5]
	v_mfma_f32_16x16x32_bf16 v[6:9], v[198:201], v[206:209], v[6:9]
	v_mfma_f32_16x16x32_bf16 v[10:13], v[190:193], v[214:217], v[10:13]
	v_mfma_f32_16x16x32_bf16 v[14:17], v[198:201], v[214:217], v[14:17]
	v_mfma_f32_16x16x32_bf16 v[34:37], v[190:193], v[222:225], v[34:37]
	v_mfma_f32_16x16x32_bf16 v[38:41], v[198:201], v[222:225], v[38:41]
	v_mfma_f32_16x16x32_bf16 v[58:61], v[190:193], v[230:233], v[58:61]
	v_mfma_f32_16x16x32_bf16 v[62:65], v[198:201], v[230:233], v[62:65]
	v_mfma_f32_16x16x32_bf16 v[2:5], v[194:197], v[210:213], v[2:5]
	v_mfma_f32_16x16x32_bf16 v[6:9], v[202:205], v[210:213], v[6:9]
	v_mfma_f32_16x16x32_bf16 v[10:13], v[194:197], v[218:221], v[10:13]
	v_mfma_f32_16x16x32_bf16 v[14:17], v[202:205], v[218:221], v[14:17]
	v_mfma_f32_16x16x32_bf16 v[34:37], v[194:197], v[226:229], v[34:37]
	v_mfma_f32_16x16x32_bf16 v[38:41], v[202:205], v[226:229], v[38:41]
	v_mfma_f32_16x16x32_bf16 v[58:61], v[194:197], v[234:237], v[58:61]
	v_mfma_f32_16x16x32_bf16 v[62:65], v[202:205], v[234:237], v[62:65]
	s_setprio 0
	s_barrier
; #define PG8_STAGE(bufoff, gbase, voff) do { _Pragma("unroll") for (int _i = 0; _i < 2; ++_i) \
;         __builtin_amdgcn_global_load_lds((const unsigned*)((const char*)(gbase) + (voff)[_i]), (PG8_LAS unsigned*)(lds + (bufoff) + ldsw + _i * 8192), 16, 0, 0); } while (0)
; #define PG8_LDA(dst, b, h) do { _Pragma("unroll") for (int m = 0; m < 4; ++m) Frag<F8>::load(dst[m], lds + PG8_SA(b, h) + aoff + m * 2048); } while (0)
; #define PG8_MMA(ai, bj, At, Bt) do { __builtin_amdgcn_s_setprio(3); _Pragma("unroll") for (int m = 0; m < 4; ++m) _Pragma("unroll") for (int n = 0; n < 2; ++n) Frag<F8>::mma(acc[ai][bj][m][n], Bt[n], At[m]); \
;         __builtin_amdgcn_s_setprio(0); } while (0)
; #define PG8_WAIT_V(n) asm volatile("s_waitcnt vmcnt(" #n ")" ::: "memory")
; #define PG8_WAIT_L(n) asm volatile("s_waitcnt lgkmcnt(" #n ")" ::: "memory")
; #define PG8_BAR __builtin_amdgcn_s_barrier()
; #define PG8_SCHED __builtin_amdgcn_sched_barrier(0)
; template <class Epi, class Sched, bool ALIGN_EPI = false, bool SP2 = false, bool F8 = false>
; __device__ __forceinline__ void gemm_phase(PG8_LAS unsigned char* lds, const Gemm g, const Sched& S, const Epi& E) {
;     ...
;             PG8_LDA(At, 1, 1); PG8_STAGE(PG8_SB(1, 0), b3, voffB); PG8_STAGE(PG8_SB(1, 1), b3 + hstep, voffB); PG8_STAGE(PG8_SA(1, 0), a3, voffA);
;             PG8_WAIT_V(8); PG8_WAIT_L(0); PG8_BAR; PG8_MMA(1, 0, At, B0); PG8_MMA(1, 1, At, B1); PG8_BAR; PG8_SCHED;
;     ...
;         if constexpr (ALIGN_EPI) { if (wr == 0) PG8_BAR; }
	s_add_i32 s0, s0, s75
	v_lshl_add_u64 v[238:239], v[238:239], 0, s[42:43]
	s_mov_b32 m0, s0
	ds_read_b128 v[206:209], v160 offset:49152
	ds_read_b128 v[210:213], v160 offset:50176
	ds_read_b128 v[214:217], v160 offset:51200
	ds_read_b128 v[218:221], v160 offset:52224
	ds_read_b128 v[222:225], v160 offset:53248
	ds_read_b128 v[226:229], v160 offset:54272
	ds_read_b128 v[230:233], v160 offset:55296
	ds_read_b128 v[234:237], v160 offset:56320
	global_load_lds_dwordx4 v[238:239], off
	s_add_i32 m0, s0, 0x2000
	s_add_u32 s4, s52, 0xe0080
	v_lshl_add_u64 v[238:239], v[240:241], 0, s[42:43]
	s_addc_u32 s5, s53, 0
	s_add_i32 s0, s1, s75
	global_load_lds_dwordx4 v[238:239], off
	v_lshl_add_u64 v[238:239], s[4:5], 0, v[132:133]
	s_mov_b32 m0, s0
	s_nop 0
	global_load_lds_dwordx4 v[238:239], off
	v_lshl_add_u64 v[238:239], s[4:5], 0, v[136:137]
	s_add_i32 m0, s0, 0x2000
	s_nop 0
	global_load_lds_dwordx4 v[238:239], off
	v_lshl_add_u64 v[238:239], v[242:243], 0, s[42:43]
	s_mov_b32 m0, s87
	s_nop 0
	global_load_lds_dwordx4 v[238:239], off
	v_lshl_add_u64 v[238:239], v[244:245], 0, s[42:43]
	s_mov_b32 m0, s88
	s_nop 0
	global_load_lds_dwordx4 v[238:239], off
	s_waitcnt vmcnt(8)
	s_waitcnt lgkmcnt(0)
	s_barrier
	s_setprio 3
	v_mfma_f32_16x16x32_bf16 v[66:69], v[174:177], v[206:209], v[66:69]
	v_mfma_f32_16x16x32_bf16 v[70:73], v[182:185], v[206:209], v[70:73]
	v_mfma_f32_16x16x32_bf16 v[90:93], v[174:177], v[214:217], v[90:93]
	v_mfma_f32_16x16x32_bf16 v[94:97], v[182:185], v[214:217], v[94:97]
	v_mfma_f32_16x16x32_bf16 v[106:109], v[174:177], v[222:225], v[106:109]
	v_mfma_f32_16x16x32_bf16 v[110:113], v[182:185], v[222:225], v[110:113]
	v_mfma_f32_16x16x32_bf16 v[114:117], v[174:177], v[230:233], v[114:117]
	v_mfma_f32_16x16x32_bf16 v[126:129], v[182:185], v[230:233], v[126:129]
	v_mfma_f32_16x16x32_bf16 v[66:69], v[178:181], v[210:213], v[66:69]
	v_mfma_f32_16x16x32_bf16 v[70:73], v[186:189], v[210:213], v[70:73]
	v_mfma_f32_16x16x32_bf16 v[90:93], v[178:181], v[218:221], v[90:93]
	v_mfma_f32_16x16x32_bf16 v[94:97], v[186:189], v[218:221], v[94:97]
	v_mfma_f32_16x16x32_bf16 v[106:109], v[178:181], v[226:229], v[106:109]
	v_mfma_f32_16x16x32_bf16 v[110:113], v[186:189], v[226:229], v[110:113]
	v_mfma_f32_16x16x32_bf16 v[114:117], v[178:181], v[234:237], v[114:117]
	v_mfma_f32_16x16x32_bf16 v[126:129], v[186:189], v[234:237], v[126:129]
	v_mfma_f32_16x16x32_bf16 v[18:21], v[190:193], v[206:209], v[18:21]
	v_mfma_f32_16x16x32_bf16 v[26:29], v[198:201], v[206:209], v[26:29]
	v_mfma_f32_16x16x32_bf16 v[42:45], v[190:193], v[214:217], v[42:45]
	v_mfma_f32_16x16x32_bf16 v[50:53], v[198:201], v[214:217], v[50:53]
	v_mfma_f32_16x16x32_bf16 v[74:77], v[190:193], v[222:225], v[74:77]
	v_mfma_f32_16x16x32_bf16 v[82:85], v[198:201], v[222:225], v[82:85]
	v_mfma_f32_16x16x32_bf16 v[122:125], v[190:193], v[230:233], v[122:125]
	v_mfma_f32_16x16x32_bf16 v[118:121], v[198:201], v[230:233], v[118:121]
	v_mfma_f32_16x16x32_bf16 v[18:21], v[194:197], v[210:213], v[18:21]
	v_mfma_f32_16x16x32_bf16 v[26:29], v[202:205], v[210:213], v[26:29]
	v_mfma_f32_16x16x32_bf16 v[42:45], v[194:197], v[218:221], v[42:45]
	v_mfma_f32_16x16x32_bf16 v[50:53], v[202:205], v[218:221], v[50:53]
	v_mfma_f32_16x16x32_bf16 v[74:77], v[194:197], v[226:229], v[74:77]
	v_mfma_f32_16x16x32_bf16 v[82:85], v[202:205], v[226:229], v[82:85]
	v_mfma_f32_16x16x32_bf16 v[122:125], v[194:197], v[234:237], v[122:125]
	v_mfma_f32_16x16x32_bf16 v[118:121], v[202:205], v[234:237], v[118:121]
	s_setprio 0
	s_barrier
	s_add_i32 s3, s3, 2
	s_add_u32 s50, s50, 0x100
	s_addc_u32 s51, s51, 0
	s_cmp_gt_u32 s3, 53
	s_cbranch_scc0 .LBB0_674
	s_and_b64 vcc, exec, s[44:45]
	s_cbranch_vccz .LBB0_677
	s_barrier

; template <class Epi, class Sched, bool ALIGN_EPI = false, bool SP2 = false, bool F8 = false>
; __device__ __forceinline__ void gemm_phase(PG8_LAS unsigned char* lds, const Gemm g, const Sched& S, const Epi& E) {
;     ...
;     for (;;) {
;         const bool has_next = S.next(ui + 1, nxt);
;         const char* nA = has_next ? (const char*)g.A + (size_t)nxt.pm * tstep + nxt.ko : cA; const char* nB = has_next ? (const char*)g.Bt + (size_t)nxt.pn * tstep + nxt.ko : cB;
;         for (int t = 0; t < nt; t += 2) {
;             const bool last = (t == nt - 2);
;             const char* a1 = cA + (size_t)(t + 1) * kstep;
;             const char* a2 = last ? nA : cA + (size_t)(t + 2) * kstep; const char* b2 = last ? nB : cB + (size_t)(t + 2) * kstep;
;             const char* a3 = a2 + kstep; const char* b3 = b2 + kstep;
;             if (last && has_next) S.a_ready(nxt);
;             if constexpr (SP2) {
;             PG8_LDB(B0, 0, 0); PG8_LDB(B1, 0, 1); PG8_SCHED; PG8_LDA(At, 0, 0); PG8_STAGE(PG8_SA(1, 1), a1 + hstep, voffA);
;             PG8_WAIT_V(8); PG8_WAIT_L(0); PG8_BAR; PG8_MMA(0, 0, At, B0); PG8_MMA(0, 1, At, B1); PG8_BAR; PG8_SCHED;
;             PG8_LDA(At, 0, 1); PG8_STAGE(PG8_SB(0, 0), b2, voffB); PG8_STAGE(PG8_SB(0, 1), b2 + hstep, voffB); PG8_STAGE(PG8_SA(0, 0), a2, voffA);
;             PG8_WAIT_V(8); PG8_WAIT_L(0); PG8_BAR; PG8_MMA(1, 0, At, B0); PG8_MMA(1, 1, At, B1); PG8_BAR; PG8_SCHED;
;             PG8_LDB(B0, 1, 0); PG8_LDB(B1, 1, 1); PG8_SCHED; PG8_LDA(At, 1, 0); PG8_STAGE(PG8_SA(0, 1), a2 + hstep, voffA);
;             PG8_WAIT_V(8); PG8_WAIT_L(0); PG8_BAR; PG8_MMA(0, 0, At, B0); PG8_MMA(0, 1, At, B1); PG8_BAR; PG8_SCHED;
;             PG8_LDA(At, 1, 1); PG8_STAGE(PG8_SB(1, 0), b3, voffB); PG8_STAGE(PG8_SB(1, 1), b3 + hstep, voffB); PG8_STAGE(PG8_SA(1, 0), a3, voffA);
;             PG8_WAIT_V(8); PG8_WAIT_L(0); PG8_BAR; PG8_MMA(1, 0, At, B0); PG8_MMA(1, 1, At, B1); PG8_BAR; PG8_SCHED;
;             } else {
;             PG8_LDB(B0, 0, 0); PG8_SCHED; PG8_LDA(At, 0, 0); PG8_STAGE(PG8_SA(1, 1), a1 + hstep, voffA);
;             PG8_WAIT_L(8); PG8_BAR; PG8_WAIT_L(0); PG8_MMA(0, 0, At, B0); PG8_BAR; PG8_SCHED;
;             PG8_LDB(B1, 0, 1); PG8_STAGE(PG8_SB(0, 0), b2, voffB);
;             PG8_BAR; PG8_WAIT_L(0); PG8_MMA(0, 1, At, B1); PG8_BAR;
;             PG8_LDA(At, 0, 1); PG8_STAGE(PG8_SA(0, 0), a2, voffA);
.Lprobe_tramp:
	s_branch .Lprobe_reentry

; #define PG8_STAGE(bufoff, gbase, voff) do { _Pragma("unroll") for (int _i = 0; _i < 2; ++_i) \
;         __builtin_amdgcn_global_load_lds((const unsigned*)((const char*)(gbase) + (voff)[_i]), (PG8_LAS unsigned*)(lds + (bufoff) + ldsw + _i * 8192), 16, 0, 0); } while (0)
; #define PG8_LDA(dst, b, h) do { _Pragma("unroll") for (int m = 0; m < 4; ++m) Frag<F8>::load(dst[m], lds + PG8_SA(b, h) + aoff + m * 2048); } while (0)
; #define PG8_LDB(dst, b, h) do { _Pragma("unroll") for (int n = 0; n < 2; ++n) Frag<F8>::load(dst[n], lds + PG8_SB(b, h) + boff + n * 2048); } while (0)
; #define PG8_WAIT_V(n) asm volatile("s_waitcnt vmcnt(" #n ")" ::: "memory")
; #define PG8_WAIT_L(n) asm volatile("s_waitcnt lgkmcnt(" #n ")" ::: "memory")
; #define PG8_BAR __builtin_amdgcn_s_barrier()
; template <class Epi, class Sched, bool ALIGN_EPI = false, bool SP2 = false, bool F8 = false>
; __device__ __forceinline__ void gemm_phase(PG8_LAS unsigned char* lds, const Gemm g, const Sched& S, const Epi& E) {
;     ...
;         const char* nA = has_next ? (const char*)g.A + (size_t)nxt.pm * tstep + nxt.ko : cA; const char* nB = has_next ? (const char*)g.Bt + (size_t)nxt.pn * tstep + nxt.ko : cB;
;         for (int t = 0; t < nt; t += 2) {
;             const bool last = (t == nt - 2);
;             const char* a1 = cA + (size_t)(t + 1) * kstep;
;             const char* a2 = last ? nA : cA + (size_t)(t + 2) * kstep; const char* b2 = last ? nB : cB + (size_t)(t + 2) * kstep;
;             const char* a3 = a2 + kstep; const char* b3 = b2 + kstep;
;             if (last && has_next) S.a_ready(nxt);
;             if constexpr (SP2) {
;             PG8_LDB(B0, 0, 0); PG8_LDB(B1, 0, 1); PG8_SCHED; PG8_LDA(At, 0, 0); PG8_STAGE(PG8_SA(1, 1), a1 + hstep, voffA);
;             PG8_WAIT_V(8); PG8_WAIT_L(0); PG8_BAR; PG8_MMA(0, 0, At, B0); PG8_MMA(0, 1, At, B1); PG8_BAR; PG8_SCHED;
;             PG8_LDA(At, 0, 1); PG8_STAGE(PG8_SB(0, 0), b2, voffB); PG8_STAGE(PG8_SB(0, 1), b2 + hstep, voffB); PG8_STAGE(PG8_SA(0, 0), a2, voffA);
;             PG8_WAIT_V(8); PG8_WAIT_L(0); PG8_BAR; PG8_MMA(1, 0, At, B0); PG8_MMA(1, 1, At, B1); PG8_BAR; PG8_SCHED;
;             PG8_LDB(B0, 1, 0); PG8_LDB(B1, 1, 1); PG8_SCHED; PG8_LDA(At, 1, 0); PG8_STAGE(PG8_SA(0, 1), a2 + hstep, voffA);
;             PG8_WAIT_V(8); PG8_WAIT_L(0); PG8_BAR; PG8_MMA(0, 0, At, B0); PG8_MMA(0, 1, At, B1); PG8_BAR; PG8_SCHED;
.LBB0_801:
	s_ashr_i32 s25, s24, 31
	s_lshl_b64 s[4:5], s[24:25], 18
	s_add_u32 s36, s49, s4
	s_addc_u32 s37, s50, s5
	s_and_b64 s[4:5], s[8:9], exec
	s_cselect_b32 s25, s37, s43
	s_cselect_b32 s83, s36, s42
	s_ashr_i32 s31, s30, 31
	s_lshl_b64 s[4:5], s[30:31], 18
	s_add_u32 s38, s51, s4
	s_addc_u32 s39, s52, s5
	s_and_b64 s[4:5], s[8:9], exec
	s_cselect_b32 s31, s39, s45
	s_cselect_b32 s84, s38, s44
	s_add_u32 s42, s42, 0x20080
	s_addc_u32 s43, s43, 0
	s_add_u32 s85, s44, 0x100
	s_addc_u32 s86, s45, 0
	s_mov_b32 s87, -2
	ds_read_b128 v[18:21], v194
	ds_read_b128 v[22:25], v194 offset:1024
	ds_read_b128 v[26:29], v194 offset:2048
	ds_read_b128 v[30:33], v194 offset:3072
	ds_read_b128 v[2:5], v195
	ds_read_b128 v[6:9], v195 offset:1024
	ds_read_b128 v[10:13], v195 offset:2048
	ds_read_b128 v[14:17], v195 offset:3072
	s_add_u32 s0, s42, 0xfffe0080
	s_addc_u32 s1, s43, -1
	s_cmp_eq_u32 s87, 4
	s_cselect_b32 s47, s25, s1
	s_cselect_b32 s46, s83, s0
	s_cselect_b32 s45, s31, s86
	s_cselect_b32 s44, s84, s85
	v_lshl_add_u64 v[224:225], s[42:43], 0, v[174:175]
	s_add_i32 m0, s41, 0xc000
	ds_read_b128 v[182:185], v196
	ds_read_b128 v[186:189], v196 offset:1024
	ds_read_b128 v[200:203], v196 offset:2048
	ds_read_b128 v[204:207], v196 offset:3072
	ds_read_b128 v[208:211], v196 offset:4096
	ds_read_b128 v[212:215], v196 offset:5120
	ds_read_b128 v[216:219], v196 offset:6144
	ds_read_b128 v[220:223], v196 offset:7168
	global_load_lds_dwordx4 v[224:225], off
	v_lshl_add_u64 v[224:225], s[42:43], 0, v[176:177]
	s_add_i32 m0, s41, 0xe000
	s_nop 0
	global_load_lds_dwordx4 v[224:225], off
	s_waitcnt vmcnt(8)
	s_waitcnt lgkmcnt(0)
	s_barrier
	s_setprio 3
	v_mfma_f32_16x16x128_f8f6f4 v[158:161], v[18:25], v[182:189], 0
	v_mfma_f32_16x16x128_f8f6f4 v[154:157], v[26:33], v[182:189], 0
	v_mfma_f32_16x16x128_f8f6f4 v[150:153], v[18:25], v[200:207], 0
	v_mfma_f32_16x16x128_f8f6f4 v[142:145], v[26:33], v[200:207], 0
	v_mfma_f32_16x16x128_f8f6f4 v[130:133], v[18:25], v[208:215], 0
	v_mfma_f32_16x16x128_f8f6f4 v[122:125], v[26:33], v[208:215], 0
	v_mfma_f32_16x16x128_f8f6f4 v[118:121], v[18:25], v[216:223], 0
	v_mfma_f32_16x16x128_f8f6f4 v[110:113], v[26:33], v[216:223], 0
	v_mfma_f32_16x16x128_f8f6f4 v[146:149], v[2:9], v[182:189], 0
	v_mfma_f32_16x16x128_f8f6f4 v[138:141], v[10:17], v[182:189], 0
	v_mfma_f32_16x16x128_f8f6f4 v[134:137], v[2:9], v[200:207], 0
	v_mfma_f32_16x16x128_f8f6f4 v[126:129], v[10:17], v[200:207], 0
	v_mfma_f32_16x16x128_f8f6f4 v[114:117], v[2:9], v[208:215], 0
	v_mfma_f32_16x16x128_f8f6f4 v[106:109], v[10:17], v[208:215], 0
	v_mfma_f32_16x16x128_f8f6f4 v[102:105], v[2:9], v[216:223], 0
	v_mfma_f32_16x16x128_f8f6f4 v[98:101], v[10:17], v[216:223], 0
	s_setprio 0
	s_barrier
	s_add_i32 s0, s79, s48
	v_lshl_add_u64 v[182:183], s[44:45], 0, v[170:171]
	s_mov_b32 m0, s0
	ds_read_b128 v[200:203], v196 offset:16384
	ds_read_b128 v[204:207], v196 offset:17408
	ds_read_b128 v[208:211], v196 offset:18432
	ds_read_b128 v[212:215], v196 offset:19456
	ds_read_b128 v[216:219], v196 offset:20480
	ds_read_b128 v[220:223], v196 offset:21504
	ds_read_b128 v[224:227], v196 offset:22528
	ds_read_b128 v[228:231], v196 offset:23552
	global_load_lds_dwordx4 v[182:183], off
	s_add_i32 m0, s0, 0x2000
	s_add_u32 s4, s44, 0x20000
	v_lshl_add_u64 v[184:185], s[44:45], 0, v[166:167]
	s_addc_u32 s5, s45, 0
	s_add_i32 s0, s80, s48
	global_load_lds_dwordx4 v[184:185], off
	v_lshl_add_u64 v[186:187], s[4:5], 0, v[170:171]
	s_mov_b32 m0, s0
	v_lshl_add_u64 v[188:189], s[46:47], 0, v[168:169]
	global_load_lds_dwordx4 v[186:187], off
	v_lshl_add_u64 v[186:187], s[4:5], 0, v[166:167]
	s_add_i32 m0, s0, 0x2000
	s_nop 0
	global_load_lds_dwordx4 v[186:187], off
	v_lshl_add_u64 v[186:187], s[46:47], 0, v[172:173]
	s_mov_b32 m0, s41
	s_nop 0
	global_load_lds_dwordx4 v[186:187], off
	s_mov_b32 m0, s71
	s_nop 0
	global_load_lds_dwordx4 v[188:189], off
	s_waitcnt vmcnt(8)
	s_waitcnt lgkmcnt(0)
	s_barrier
	s_setprio 3
	v_mfma_f32_16x16x128_f8f6f4 v[94:97], v[18:25], v[200:207], 0
	v_mfma_f32_16x16x128_f8f6f4 v[90:93], v[26:33], v[200:207], 0
	v_mfma_f32_16x16x128_f8f6f4 v[86:89], v[18:25], v[208:215], 0
	v_mfma_f32_16x16x128_f8f6f4 v[82:85], v[26:33], v[208:215], 0
	v_mfma_f32_16x16x128_f8f6f4 v[70:73], v[18:25], v[216:223], 0
	v_mfma_f32_16x16x128_f8f6f4 v[66:69], v[26:33], v[216:223], 0
	v_mfma_f32_16x16x128_f8f6f4 v[54:57], v[18:25], v[224:231], 0
	v_mfma_f32_16x16x128_f8f6f4 v[50:53], v[26:33], v[224:231], 0
	v_mfma_f32_16x16x128_f8f6f4 v[78:81], v[2:9], v[200:207], 0
	v_mfma_f32_16x16x128_f8f6f4 v[74:77], v[10:17], v[200:207], 0
	v_mfma_f32_16x16x128_f8f6f4 v[62:65], v[2:9], v[208:215], 0
	v_mfma_f32_16x16x128_f8f6f4 v[58:61], v[10:17], v[208:215], 0
	v_mfma_f32_16x16x128_f8f6f4 v[46:49], v[2:9], v[216:223], 0
	v_mfma_f32_16x16x128_f8f6f4 v[42:45], v[10:17], v[216:223], 0
	v_mfma_f32_16x16x128_f8f6f4 v[38:41], v[2:9], v[224:231], 0
	v_mfma_f32_16x16x128_f8f6f4 v[34:37], v[10:17], v[224:231], 0
	s_setprio 0
	s_barrier
	s_add_i32 s0, 0, 0x18000
	s_add_i32 s1, 0, 0x1c000
	v_add_u32_e32 v14, s0, v190
	v_add_u32_e32 v30, s1, v190
	ds_read_b128 v[2:5], v14
	ds_read_b128 v[6:9], v14 offset:1024
	ds_read_b128 v[10:13], v14 offset:2048
	ds_read_b128 v[14:17], v14 offset:3072
	ds_read_b128 v[18:21], v30
	ds_read_b128 v[22:25], v30 offset:1024
	ds_read_b128 v[26:29], v30 offset:2048
	ds_read_b128 v[30:33], v30 offset:3072
	s_add_u32 s4, s46, 0x20000
	s_addc_u32 s5, s47, 0
	s_mov_b32 m0, s72
	v_lshl_add_u64 v[232:233], s[4:5], 0, v[172:173]
	ds_read_b128 v[200:203], v196 offset:32768
	ds_read_b128 v[204:207], v196 offset:33792
	ds_read_b128 v[208:211], v196 offset:34816
	ds_read_b128 v[212:215], v196 offset:35840
	ds_read_b128 v[216:219], v196 offset:36864
	ds_read_b128 v[220:223], v196 offset:37888
	ds_read_b128 v[224:227], v196 offset:38912
	ds_read_b128 v[228:231], v196 offset:39936
	global_load_lds_dwordx4 v[232:233], off
	v_lshl_add_u64 v[232:233], s[4:5], 0, v[168:169]
	s_mov_b32 m0, s73
	s_nop 0
	global_load_lds_dwordx4 v[232:233], off
	s_waitcnt vmcnt(8)
	s_waitcnt lgkmcnt(0)
	s_barrier
; #define PG8_STAGE(bufoff, gbase, voff) do { _Pragma("unroll") for (int _i = 0; _i < 2; ++_i) \
;         __builtin_amdgcn_global_load_lds((const unsigned*)((const char*)(gbase) + (voff)[_i]), (PG8_LAS unsigned*)(lds + (bufoff) + ldsw + _i * 8192), 16, 0, 0); } while (0)
; #define PG8_LDA(dst, b, h) do { _Pragma("unroll") for (int m = 0; m < 4; ++m) Frag<F8>::load(dst[m], lds + PG8_SA(b, h) + aoff + m * 2048); } while (0)
; #define PG8_LDB(dst, b, h) do { _Pragma("unroll") for (int n = 0; n < 2; ++n) Frag<F8>::load(dst[n], lds + PG8_SB(b, h) + boff + n * 2048); } while (0)
; #define PG8_MMA(ai, bj, At, Bt) do { __builtin_amdgcn_s_setprio(3); _Pragma("unroll") for (int m = 0; m < 4; ++m) _Pragma("unroll") for (int n = 0; n < 2; ++n) Frag<F8>::mma(acc[ai][bj][m][n], Bt[n], At[m]); \
;         __builtin_amdgcn_s_setprio(0); } while (0)
; #define PG8_WAIT_V(n) asm volatile("s_waitcnt vmcnt(" #n ")" ::: "memory")
; #define PG8_WAIT_L(n) asm volatile("s_waitcnt lgkmcnt(" #n ")" ::: "memory")
; #define PG8_BAR __builtin_amdgcn_s_barrier()
; #define PG8_SCHED __builtin_amdgcn_sched_barrier(0)
; template <class Epi, class Sched, bool ALIGN_EPI = false, bool SP2 = false, bool F8 = false>
; __device__ __forceinline__ void gemm_phase(PG8_LAS unsigned char* lds, const Gemm g, const Sched& S, const Epi& E) {
;     ...
;             PG8_LDB(B0, 0, 0); PG8_LDB(B1, 0, 1); PG8_SCHED; PG8_LDA(At, 0, 0); PG8_STAGE(PG8_SA(1, 1), a1 + hstep, voffA);
;             PG8_WAIT_V(8); PG8_WAIT_L(0); PG8_BAR; PG8_MMA(0, 0, At, B0); PG8_MMA(0, 1, At, B1); PG8_BAR; PG8_SCHED;
;     ...
;             PG8_LDA(At, 1, 1); PG8_STAGE(PG8_SB(1, 0), b3, voffB); PG8_STAGE(PG8_SB(1, 1), b3 + hstep, voffB); PG8_STAGE(PG8_SA(1, 0), a3, voffA);
;             PG8_WAIT_V(8); PG8_WAIT_L(0); PG8_BAR; PG8_MMA(1, 0, At, B0); PG8_MMA(1, 1, At, B1); PG8_BAR; PG8_SCHED;
	s_setprio 3
	v_mfma_f32_16x16x128_f8f6f4 v[158:161], v[2:9], v[200:207], v[158:161]
	v_mfma_f32_16x16x128_f8f6f4 v[154:157], v[10:17], v[200:207], v[154:157]
	v_mfma_f32_16x16x128_f8f6f4 v[150:153], v[2:9], v[208:215], v[150:153]
	v_mfma_f32_16x16x128_f8f6f4 v[142:145], v[10:17], v[208:215], v[142:145]
	v_mfma_f32_16x16x128_f8f6f4 v[130:133], v[2:9], v[216:223], v[130:133]
	v_mfma_f32_16x16x128_f8f6f4 v[122:125], v[10:17], v[216:223], v[122:125]
	v_mfma_f32_16x16x128_f8f6f4 v[118:121], v[2:9], v[224:231], v[118:121]
	v_mfma_f32_16x16x128_f8f6f4 v[110:113], v[10:17], v[224:231], v[110:113]
	v_mfma_f32_16x16x128_f8f6f4 v[146:149], v[18:25], v[200:207], v[146:149]
	v_mfma_f32_16x16x128_f8f6f4 v[138:141], v[26:33], v[200:207], v[138:141]
	v_mfma_f32_16x16x128_f8f6f4 v[134:137], v[18:25], v[208:215], v[134:137]
	v_mfma_f32_16x16x128_f8f6f4 v[126:129], v[26:33], v[208:215], v[126:129]
	v_mfma_f32_16x16x128_f8f6f4 v[114:117], v[18:25], v[216:223], v[114:117]
	v_mfma_f32_16x16x128_f8f6f4 v[106:109], v[26:33], v[216:223], v[106:109]
	v_mfma_f32_16x16x128_f8f6f4 v[102:105], v[18:25], v[224:231], v[102:105]
	v_mfma_f32_16x16x128_f8f6f4 v[98:101], v[26:33], v[224:231], v[98:101]
	s_setprio 0
	s_barrier
	s_add_i32 s0, s0, s48
	v_lshl_add_u64 v[182:183], v[182:183], 0, s[18:19]
	s_mov_b32 m0, s0
	ds_read_b128 v[200:203], v196 offset:49152
	ds_read_b128 v[204:207], v196 offset:50176
	ds_read_b128 v[208:211], v196 offset:51200
	ds_read_b128 v[212:215], v196 offset:52224
	ds_read_b128 v[216:219], v196 offset:53248
	ds_read_b128 v[220:223], v196 offset:54272
	ds_read_b128 v[224:227], v196 offset:55296
	ds_read_b128 v[228:231], v196 offset:56320
	global_load_lds_dwordx4 v[182:183], off
	s_add_i32 m0, s0, 0x2000
	s_add_u32 s4, s44, 0x20080
	v_lshl_add_u64 v[182:183], v[184:185], 0, s[18:19]
	s_addc_u32 s5, s45, 0
	s_add_i32 s0, s1, s48
	global_load_lds_dwordx4 v[182:183], off
	v_lshl_add_u64 v[182:183], s[4:5], 0, v[170:171]
	s_mov_b32 m0, s0
	s_nop 0
	global_load_lds_dwordx4 v[182:183], off
	v_lshl_add_u64 v[182:183], s[4:5], 0, v[166:167]
	s_add_i32 m0, s0, 0x2000
	s_nop 0
	global_load_lds_dwordx4 v[182:183], off
	v_lshl_add_u64 v[182:183], v[186:187], 0, s[18:19]
	s_mov_b32 m0, s74
	s_nop 0
	global_load_lds_dwordx4 v[182:183], off
	v_lshl_add_u64 v[182:183], v[188:189], 0, s[18:19]
	s_mov_b32 m0, s75
	s_nop 0
	global_load_lds_dwordx4 v[182:183], off
	s_waitcnt vmcnt(8)
	s_waitcnt lgkmcnt(0)
	s_barrier
	s_setprio 3
	v_mfma_f32_16x16x128_f8f6f4 v[94:97], v[2:9], v[200:207], v[94:97]
	v_mfma_f32_16x16x128_f8f6f4 v[90:93], v[10:17], v[200:207], v[90:93]
	v_mfma_f32_16x16x128_f8f6f4 v[86:89], v[2:9], v[208:215], v[86:89]
	v_mfma_f32_16x16x128_f8f6f4 v[82:85], v[10:17], v[208:215], v[82:85]
	v_mfma_f32_16x16x128_f8f6f4 v[70:73], v[2:9], v[216:223], v[70:73]
	v_mfma_f32_16x16x128_f8f6f4 v[66:69], v[10:17], v[216:223], v[66:69]
	v_mfma_f32_16x16x128_f8f6f4 v[54:57], v[2:9], v[224:231], v[54:57]
	v_mfma_f32_16x16x128_f8f6f4 v[50:53], v[10:17], v[224:231], v[50:53]
	v_mfma_f32_16x16x128_f8f6f4 v[78:81], v[18:25], v[200:207], v[78:81]
	v_mfma_f32_16x16x128_f8f6f4 v[74:77], v[26:33], v[200:207], v[74:77]
	v_mfma_f32_16x16x128_f8f6f4 v[62:65], v[18:25], v[208:215], v[62:65]
	v_mfma_f32_16x16x128_f8f6f4 v[58:61], v[26:33], v[208:215], v[58:61]
	v_mfma_f32_16x16x128_f8f6f4 v[46:49], v[18:25], v[216:223], v[46:49]
	v_mfma_f32_16x16x128_f8f6f4 v[42:45], v[26:33], v[216:223], v[42:45]
	v_mfma_f32_16x16x128_f8f6f4 v[38:41], v[18:25], v[224:231], v[38:41]
	v_mfma_f32_16x16x128_f8f6f4 v[34:37], v[26:33], v[224:231], v[34:37]
	s_setprio 0
	s_barrier
	s_add_i32 s87, s87, 2
	s_add_u32 s42, s42, 0x100
	s_addc_u32 s43, s43, 0
	s_add_u32 s85, s85, 0x100
	s_addc_u32 s86, s86, 0
	s_cmp_gt_u32 s87, 5
	s_cbranch_scc1 .Lpeel_exit_2
.LBB0_802:
	ds_read_b128 v[18:21], v194
	ds_read_b128 v[22:25], v194 offset:1024
	ds_read_b128 v[26:29], v194 offset:2048
	ds_read_b128 v[30:33], v194 offset:3072
	ds_read_b128 v[2:5], v195
	ds_read_b128 v[6:9], v195 offset:1024
	ds_read_b128 v[10:13], v195 offset:2048
	ds_read_b128 v[14:17], v195 offset:3072
	s_add_u32 s0, s42, 0xfffe0080
	s_addc_u32 s1, s43, -1
	s_cmp_eq_u32 s87, 4
	s_cselect_b32 s47, s25, s1
	s_cselect_b32 s46, s83, s0
	s_cselect_b32 s45, s31, s86
	s_cselect_b32 s44, s84, s85
	v_lshl_add_u64 v[224:225], s[42:43], 0, v[174:175]
	s_add_i32 m0, s41, 0xc000
	ds_read_b128 v[182:185], v196
	ds_read_b128 v[186:189], v196 offset:1024
	ds_read_b128 v[200:203], v196 offset:2048
	ds_read_b128 v[204:207], v196 offset:3072
	ds_read_b128 v[208:211], v196 offset:4096
	ds_read_b128 v[212:215], v196 offset:5120
	ds_read_b128 v[216:219], v196 offset:6144
	ds_read_b128 v[220:223], v196 offset:7168
	global_load_lds_dwordx4 v[224:225], off
	v_lshl_add_u64 v[224:225], s[42:43], 0, v[176:177]
	s_add_i32 m0, s41, 0xe000
	s_nop 0
	global_load_lds_dwordx4 v[224:225], off
	s_waitcnt vmcnt(8)
	s_waitcnt lgkmcnt(0)
	s_barrier
	s_setprio 3
	v_mfma_f32_16x16x128_f8f6f4 v[158:161], v[18:25], v[182:189], v[158:161]
	v_mfma_f32_16x16x128_f8f6f4 v[154:157], v[26:33], v[182:189], v[154:157]
	v_mfma_f32_16x16x128_f8f6f4 v[150:153], v[18:25], v[200:207], v[150:153]
	v_mfma_f32_16x16x128_f8f6f4 v[142:145], v[26:33], v[200:207], v[142:145]
	v_mfma_f32_16x16x128_f8f6f4 v[130:133], v[18:25], v[208:215], v[130:133]
	v_mfma_f32_16x16x128_f8f6f4 v[122:125], v[26:33], v[208:215], v[122:125]
	v_mfma_f32_16x16x128_f8f6f4 v[118:121], v[18:25], v[216:223], v[118:121]
	v_mfma_f32_16x16x128_f8f6f4 v[110:113], v[26:33], v[216:223], v[110:113]
	v_mfma_f32_16x16x128_f8f6f4 v[146:149], v[2:9], v[182:189], v[146:149]
	v_mfma_f32_16x16x128_f8f6f4 v[138:141], v[10:17], v[182:189], v[138:141]
	v_mfma_f32_16x16x128_f8f6f4 v[134:137], v[2:9], v[200:207], v[134:137]
	v_mfma_f32_16x16x128_f8f6f4 v[126:129], v[10:17], v[200:207], v[126:129]
	v_mfma_f32_16x16x128_f8f6f4 v[114:117], v[2:9], v[208:215], v[114:117]
	v_mfma_f32_16x16x128_f8f6f4 v[106:109], v[10:17], v[208:215], v[106:109]
	v_mfma_f32_16x16x128_f8f6f4 v[102:105], v[2:9], v[216:223], v[102:105]
	v_mfma_f32_16x16x128_f8f6f4 v[98:101], v[10:17], v[216:223], v[98:101]
	s_setprio 0
	s_barrier
; #define PG8_STAGE(bufoff, gbase, voff) do { _Pragma("unroll") for (int _i = 0; _i < 2; ++_i) \
;         __builtin_amdgcn_global_load_lds((const unsigned*)((const char*)(gbase) + (voff)[_i]), (PG8_LAS unsigned*)(lds + (bufoff) + ldsw + _i * 8192), 16, 0, 0); } while (0)
; #define PG8_LDA(dst, b, h) do { _Pragma("unroll") for (int m = 0; m < 4; ++m) Frag<F8>::load(dst[m], lds + PG8_SA(b, h) + aoff + m * 2048); } while (0)
; #define PG8_LDB(dst, b, h) do { _Pragma("unroll") for (int n = 0; n < 2; ++n) Frag<F8>::load(dst[n], lds + PG8_SB(b, h) + boff + n * 2048); } while (0)
; #define PG8_MMA(ai, bj, At, Bt) do { __builtin_amdgcn_s_setprio(3); _Pragma("unroll") for (int m = 0; m < 4; ++m) _Pragma("unroll") for (int n = 0; n < 2; ++n) Frag<F8>::mma(acc[ai][bj][m][n], Bt[n], At[m]); \
;         __builtin_amdgcn_s_setprio(0); } while (0)
; #define PG8_WAIT_V(n) asm volatile("s_waitcnt vmcnt(" #n ")" ::: "memory")
; #define PG8_WAIT_L(n) asm volatile("s_waitcnt lgkmcnt(" #n ")" ::: "memory")
; #define PG8_BAR __builtin_amdgcn_s_barrier()
; #define PG8_SCHED __builtin_amdgcn_sched_barrier(0)
; template <class Epi, class Sched, bool ALIGN_EPI = false, bool SP2 = false, bool F8 = false>
; __device__ __forceinline__ void gemm_phase(PG8_LAS unsigned char* lds, const Gemm g, const Sched& S, const Epi& E) {
;     ...
;             PG8_LDA(At, 0, 1); PG8_STAGE(PG8_SB(0, 0), b2, voffB); PG8_STAGE(PG8_SB(0, 1), b2 + hstep, voffB); PG8_STAGE(PG8_SA(0, 0), a2, voffA);
;             PG8_WAIT_V(8); PG8_WAIT_L(0); PG8_BAR; PG8_MMA(1, 0, At, B0); PG8_MMA(1, 1, At, B1); PG8_BAR; PG8_SCHED;
;             PG8_LDB(B0, 1, 0); PG8_LDB(B1, 1, 1); PG8_SCHED; PG8_LDA(At, 1, 0); PG8_STAGE(PG8_SA(0, 1), a2 + hstep, voffA);
;             PG8_WAIT_V(8); PG8_WAIT_L(0); PG8_BAR; PG8_MMA(0, 0, At, B0); PG8_MMA(0, 1, At, B1); PG8_BAR; PG8_SCHED;
	s_add_i32 s0, s79, s48
	v_lshl_add_u64 v[182:183], s[44:45], 0, v[170:171]
	s_mov_b32 m0, s0
	ds_read_b128 v[200:203], v196 offset:16384
	ds_read_b128 v[204:207], v196 offset:17408
	ds_read_b128 v[208:211], v196 offset:18432
	ds_read_b128 v[212:215], v196 offset:19456
	ds_read_b128 v[216:219], v196 offset:20480
	ds_read_b128 v[220:223], v196 offset:21504
	ds_read_b128 v[224:227], v196 offset:22528
	ds_read_b128 v[228:231], v196 offset:23552
	global_load_lds_dwordx4 v[182:183], off
	s_add_i32 m0, s0, 0x2000
	s_add_u32 s4, s44, 0x20000
	v_lshl_add_u64 v[184:185], s[44:45], 0, v[166:167]
	s_addc_u32 s5, s45, 0
	s_add_i32 s0, s80, s48
	global_load_lds_dwordx4 v[184:185], off
	v_lshl_add_u64 v[186:187], s[4:5], 0, v[170:171]
	s_mov_b32 m0, s0
	v_lshl_add_u64 v[188:189], s[46:47], 0, v[168:169]
	global_load_lds_dwordx4 v[186:187], off
	v_lshl_add_u64 v[186:187], s[4:5], 0, v[166:167]
	s_add_i32 m0, s0, 0x2000
	s_nop 0
	global_load_lds_dwordx4 v[186:187], off
	v_lshl_add_u64 v[186:187], s[46:47], 0, v[172:173]
	s_mov_b32 m0, s41
	s_nop 0
	global_load_lds_dwordx4 v[186:187], off
	s_mov_b32 m0, s71
	s_nop 0
	global_load_lds_dwordx4 v[188:189], off
	s_waitcnt vmcnt(8)
	s_waitcnt lgkmcnt(0)
	s_barrier
	s_setprio 3
	v_mfma_f32_16x16x128_f8f6f4 v[94:97], v[18:25], v[200:207], v[94:97]
	v_mfma_f32_16x16x128_f8f6f4 v[90:93], v[26:33], v[200:207], v[90:93]
	v_mfma_f32_16x16x128_f8f6f4 v[86:89], v[18:25], v[208:215], v[86:89]
	v_mfma_f32_16x16x128_f8f6f4 v[82:85], v[26:33], v[208:215], v[82:85]
	v_mfma_f32_16x16x128_f8f6f4 v[70:73], v[18:25], v[216:223], v[70:73]
	v_mfma_f32_16x16x128_f8f6f4 v[66:69], v[26:33], v[216:223], v[66:69]
	v_mfma_f32_16x16x128_f8f6f4 v[54:57], v[18:25], v[224:231], v[54:57]
	v_mfma_f32_16x16x128_f8f6f4 v[50:53], v[26:33], v[224:231], v[50:53]
	v_mfma_f32_16x16x128_f8f6f4 v[78:81], v[2:9], v[200:207], v[78:81]
	v_mfma_f32_16x16x128_f8f6f4 v[74:77], v[10:17], v[200:207], v[74:77]
	v_mfma_f32_16x16x128_f8f6f4 v[62:65], v[2:9], v[208:215], v[62:65]
	v_mfma_f32_16x16x128_f8f6f4 v[58:61], v[10:17], v[208:215], v[58:61]
	v_mfma_f32_16x16x128_f8f6f4 v[46:49], v[2:9], v[216:223], v[46:49]
	v_mfma_f32_16x16x128_f8f6f4 v[42:45], v[10:17], v[216:223], v[42:45]
	v_mfma_f32_16x16x128_f8f6f4 v[38:41], v[2:9], v[224:231], v[38:41]
	v_mfma_f32_16x16x128_f8f6f4 v[34:37], v[10:17], v[224:231], v[34:37]
	s_setprio 0
	s_barrier
	s_add_i32 s0, 0, 0x18000
	s_add_i32 s1, 0, 0x1c000
	v_add_u32_e32 v14, s0, v190
	v_add_u32_e32 v30, s1, v190
	ds_read_b128 v[2:5], v14
	ds_read_b128 v[6:9], v14 offset:1024
	ds_read_b128 v[10:13], v14 offset:2048
	ds_read_b128 v[14:17], v14 offset:3072
	ds_read_b128 v[18:21], v30
	ds_read_b128 v[22:25], v30 offset:1024
	ds_read_b128 v[26:29], v30 offset:2048
	ds_read_b128 v[30:33], v30 offset:3072
	s_add_u32 s4, s46, 0x20000
	s_addc_u32 s5, s47, 0
	s_mov_b32 m0, s72
	v_lshl_add_u64 v[232:233], s[4:5], 0, v[172:173]
	ds_read_b128 v[200:203], v196 offset:32768
	ds_read_b128 v[204:207], v196 offset:33792
	ds_read_b128 v[208:211], v196 offset:34816
	ds_read_b128 v[212:215], v196 offset:35840
	ds_read_b128 v[216:219], v196 offset:36864
	ds_read_b128 v[220:223], v196 offset:37888
	ds_read_b128 v[224:227], v196 offset:38912
	ds_read_b128 v[228:231], v196 offset:39936
	global_load_lds_dwordx4 v[232:233], off
	v_lshl_add_u64 v[232:233], s[4:5], 0, v[168:169]
	s_mov_b32 m0, s73
	s_nop 0
	global_load_lds_dwordx4 v[232:233], off
	s_waitcnt vmcnt(8)
	s_waitcnt lgkmcnt(0)
	s_barrier
; #define PG8_STAGE(bufoff, gbase, voff) do { _Pragma("unroll") for (int _i = 0; _i < 2; ++_i) \
;         __builtin_amdgcn_global_load_lds((const unsigned*)((const char*)(gbase) + (voff)[_i]), (PG8_LAS unsigned*)(lds + (bufoff) + ldsw + _i * 8192), 16, 0, 0); } while (0)
; #define PG8_LDA(dst, b, h) do { _Pragma("unroll") for (int m = 0; m < 4; ++m) Frag<F8>::load(dst[m], lds + PG8_SA(b, h) + aoff + m * 2048); } while (0)
; #define PG8_MMA(ai, bj, At, Bt) do { __builtin_amdgcn_s_setprio(3); _Pragma("unroll") for (int m = 0; m < 4; ++m) _Pragma("unroll") for (int n = 0; n < 2; ++n) Frag<F8>::mma(acc[ai][bj][m][n], Bt[n], At[m]); \
;         __builtin_amdgcn_s_setprio(0); } while (0)
; #define PG8_WAIT_V(n) asm volatile("s_waitcnt vmcnt(" #n ")" ::: "memory")
; #define PG8_WAIT_L(n) asm volatile("s_waitcnt lgkmcnt(" #n ")" ::: "memory")
; #define PG8_BAR __builtin_amdgcn_s_barrier()
; #define PG8_SCHED __builtin_amdgcn_sched_barrier(0)
; template <class Epi, class Sched, bool ALIGN_EPI = false, bool SP2 = false, bool F8 = false>
; __device__ __forceinline__ void gemm_phase(PG8_LAS unsigned char* lds, const Gemm g, const Sched& S, const Epi& E) {
;     ...
;             PG8_LDA(At, 1, 1); PG8_STAGE(PG8_SB(1, 0), b3, voffB); PG8_STAGE(PG8_SB(1, 1), b3 + hstep, voffB); PG8_STAGE(PG8_SA(1, 0), a3, voffA);
;             PG8_WAIT_V(8); PG8_WAIT_L(0); PG8_BAR; PG8_MMA(1, 0, At, B0); PG8_MMA(1, 1, At, B1); PG8_BAR; PG8_SCHED;
	s_setprio 3
	v_mfma_f32_16x16x128_f8f6f4 v[158:161], v[2:9], v[200:207], v[158:161]
	v_mfma_f32_16x16x128_f8f6f4 v[154:157], v[10:17], v[200:207], v[154:157]
	v_mfma_f32_16x16x128_f8f6f4 v[150:153], v[2:9], v[208:215], v[150:153]
	v_mfma_f32_16x16x128_f8f6f4 v[142:145], v[10:17], v[208:215], v[142:145]
	v_mfma_f32_16x16x128_f8f6f4 v[130:133], v[2:9], v[216:223], v[130:133]
	v_mfma_f32_16x16x128_f8f6f4 v[122:125], v[10:17], v[216:223], v[122:125]
	v_mfma_f32_16x16x128_f8f6f4 v[118:121], v[2:9], v[224:231], v[118:121]
	v_mfma_f32_16x16x128_f8f6f4 v[110:113], v[10:17], v[224:231], v[110:113]
	v_mfma_f32_16x16x128_f8f6f4 v[146:149], v[18:25], v[200:207], v[146:149]
	v_mfma_f32_16x16x128_f8f6f4 v[138:141], v[26:33], v[200:207], v[138:141]
	v_mfma_f32_16x16x128_f8f6f4 v[134:137], v[18:25], v[208:215], v[134:137]
	v_mfma_f32_16x16x128_f8f6f4 v[126:129], v[26:33], v[208:215], v[126:129]
	v_mfma_f32_16x16x128_f8f6f4 v[114:117], v[18:25], v[216:223], v[114:117]
	v_mfma_f32_16x16x128_f8f6f4 v[106:109], v[26:33], v[216:223], v[106:109]
	v_mfma_f32_16x16x128_f8f6f4 v[102:105], v[18:25], v[224:231], v[102:105]
	v_mfma_f32_16x16x128_f8f6f4 v[98:101], v[26:33], v[224:231], v[98:101]
	s_setprio 0
	s_barrier
	s_add_i32 s0, s0, s48
	v_lshl_add_u64 v[182:183], v[182:183], 0, s[18:19]
	s_mov_b32 m0, s0
	ds_read_b128 v[200:203], v196 offset:49152
	ds_read_b128 v[204:207], v196 offset:50176
	ds_read_b128 v[208:211], v196 offset:51200
	ds_read_b128 v[212:215], v196 offset:52224
	ds_read_b128 v[216:219], v196 offset:53248
	ds_read_b128 v[220:223], v196 offset:54272
	ds_read_b128 v[224:227], v196 offset:55296
	ds_read_b128 v[228:231], v196 offset:56320
	global_load_lds_dwordx4 v[182:183], off
	s_add_i32 m0, s0, 0x2000
	s_add_u32 s4, s44, 0x20080
	v_lshl_add_u64 v[182:183], v[184:185], 0, s[18:19]
	s_addc_u32 s5, s45, 0
	s_add_i32 s0, s1, s48
	global_load_lds_dwordx4 v[182:183], off
	v_lshl_add_u64 v[182:183], s[4:5], 0, v[170:171]
	s_mov_b32 m0, s0
	s_nop 0
	global_load_lds_dwordx4 v[182:183], off
	v_lshl_add_u64 v[182:183], s[4:5], 0, v[166:167]
	s_add_i32 m0, s0, 0x2000
	s_nop 0
	global_load_lds_dwordx4 v[182:183], off
	v_lshl_add_u64 v[182:183], v[186:187], 0, s[18:19]
	s_mov_b32 m0, s74
	s_nop 0
	global_load_lds_dwordx4 v[182:183], off
	v_lshl_add_u64 v[182:183], v[188:189], 0, s[18:19]
	s_mov_b32 m0, s75
	s_nop 0
	global_load_lds_dwordx4 v[182:183], off
	s_waitcnt vmcnt(8)
	s_waitcnt lgkmcnt(0)
	s_barrier
	s_setprio 3
	v_mfma_f32_16x16x128_f8f6f4 v[94:97], v[2:9], v[200:207], v[94:97]
	v_mfma_f32_16x16x128_f8f6f4 v[90:93], v[10:17], v[200:207], v[90:93]
	v_mfma_f32_16x16x128_f8f6f4 v[86:89], v[2:9], v[208:215], v[86:89]
	v_mfma_f32_16x16x128_f8f6f4 v[82:85], v[10:17], v[208:215], v[82:85]
	v_mfma_f32_16x16x128_f8f6f4 v[70:73], v[2:9], v[216:223], v[70:73]
	v_mfma_f32_16x16x128_f8f6f4 v[66:69], v[10:17], v[216:223], v[66:69]
	v_mfma_f32_16x16x128_f8f6f4 v[54:57], v[2:9], v[224:231], v[54:57]
	v_mfma_f32_16x16x128_f8f6f4 v[50:53], v[10:17], v[224:231], v[50:53]
	v_mfma_f32_16x16x128_f8f6f4 v[78:81], v[18:25], v[200:207], v[78:81]
	v_mfma_f32_16x16x128_f8f6f4 v[74:77], v[26:33], v[200:207], v[74:77]
	v_mfma_f32_16x16x128_f8f6f4 v[62:65], v[18:25], v[208:215], v[62:65]
	v_mfma_f32_16x16x128_f8f6f4 v[58:61], v[26:33], v[208:215], v[58:61]
	v_mfma_f32_16x16x128_f8f6f4 v[46:49], v[18:25], v[216:223], v[46:49]
	v_mfma_f32_16x16x128_f8f6f4 v[42:45], v[26:33], v[216:223], v[42:45]
	v_mfma_f32_16x16x128_f8f6f4 v[38:41], v[18:25], v[224:231], v[38:41]
	v_mfma_f32_16x16x128_f8f6f4 v[34:37], v[26:33], v[224:231], v[34:37]
	s_setprio 0
	s_barrier
	s_add_i32 s87, s87, 2
	s_add_u32 s42, s42, 0x100
	s_addc_u32 s43, s43, 0
	s_add_u32 s85, s85, 0x100
	s_addc_u32 s86, s86, 0
	s_cmp_gt_u32 s87, 5
	s_cbranch_scc0 .LBB0_802

; #define PG8_STAGE(bufoff, gbase, voff) do { _Pragma("unroll") for (int _i = 0; _i < 2; ++_i) \
;         __builtin_amdgcn_global_load_lds((const unsigned*)((const char*)(gbase) + (voff)[_i]), (PG8_LAS unsigned*)(lds + (bufoff) + ldsw + _i * 8192), 16, 0, 0); } while (0)
; #define PG8_LDA(dst, b, h) do { _Pragma("unroll") for (int m = 0; m < 4; ++m) Frag<F8>::load(dst[m], lds + PG8_SA(b, h) + aoff + m * 2048); } while (0)
; #define PG8_LDB(dst, b, h) do { _Pragma("unroll") for (int n = 0; n < 2; ++n) Frag<F8>::load(dst[n], lds + PG8_SB(b, h) + boff + n * 2048); } while (0)
; #define PG8_MMA(ai, bj, At, Bt) do { __builtin_amdgcn_s_setprio(3); _Pragma("unroll") for (int m = 0; m < 4; ++m) _Pragma("unroll") for (int n = 0; n < 2; ++n) Frag<F8>::mma(acc[ai][bj][m][n], Bt[n], At[m]); \
;         __builtin_amdgcn_s_setprio(0); } while (0)
; #define PG8_WAIT_V(n) asm volatile("s_waitcnt vmcnt(" #n ")" ::: "memory")
; #define PG8_WAIT_L(n) asm volatile("s_waitcnt lgkmcnt(" #n ")" ::: "memory")
; #define PG8_BAR __builtin_amdgcn_s_barrier()
; #define PG8_SCHED __builtin_amdgcn_sched_barrier(0)
; template <class Epi, class Sched, bool ALIGN_EPI = false, bool SP2 = false, bool F8 = false>
; __device__ __forceinline__ void gemm_phase(PG8_LAS unsigned char* lds, const Gemm g, const Sched& S, const Epi& E) {
;     ...
;         for (int t = 0; t < nt; t += 2) {
;             const bool last = (t == nt - 2);
;             const char* a1 = cA + (size_t)(t + 1) * kstep;
;             const char* a2 = last ? nA : cA + (size_t)(t + 2) * kstep; const char* b2 = last ? nB : cB + (size_t)(t + 2) * kstep;
;             const char* a3 = a2 + kstep; const char* b3 = b2 + kstep;
;             if (last && has_next) S.a_ready(nxt);
;             if constexpr (SP2) {
;             PG8_LDB(B0, 0, 0); PG8_LDB(B1, 0, 1); PG8_SCHED; PG8_LDA(At, 0, 0); PG8_STAGE(PG8_SA(1, 1), a1 + hstep, voffA);
;             PG8_WAIT_V(8); PG8_WAIT_L(0); PG8_BAR; PG8_MMA(0, 0, At, B0); PG8_MMA(0, 1, At, B1); PG8_BAR; PG8_SCHED;
;             PG8_LDA(At, 0, 1); PG8_STAGE(PG8_SB(0, 0), b2, voffB); PG8_STAGE(PG8_SB(0, 1), b2 + hstep, voffB); PG8_STAGE(PG8_SA(0, 0), a2, voffA);
;             PG8_WAIT_V(8); PG8_WAIT_L(0); PG8_BAR; PG8_MMA(1, 0, At, B0); PG8_MMA(1, 1, At, B1); PG8_BAR; PG8_SCHED;
.LBB0_1066:
	v_add_u32_e32 v160, s72, v157
	ds_read_b128 v[164:167], v160
	ds_read_b128 v[168:171], v160 offset:1024
	ds_read_b128 v[172:175], v160 offset:2048
	ds_read_b128 v[176:179], v160 offset:3072
	v_add_u32_e32 v160, s73, v157
	s_add_u32 s0, s20, s44
	ds_read_b128 v[180:183], v160
	ds_read_b128 v[184:187], v160 offset:1024
	ds_read_b128 v[188:191], v160 offset:2048
	ds_read_b128 v[192:195], v160 offset:3072
	s_addc_u32 s1, s21, s45
	s_add_u32 s0, s0, 0x100
	s_addc_u32 s1, s1, 0
	s_add_u32 s37, s3, s44
	s_addc_u32 s39, s4, s45
	s_cmpk_eq_i32 s44, 0x300
	s_cselect_b32 s49, s5, s1
	s_cselect_b32 s48, s6, s0
	s_cselect_b32 s47, s7, s39
	s_cselect_b32 s46, s31, s37
	v_lshl_add_u64 v[160:161], v[146:147], 0, s[44:45]
	s_add_i32 m0, s17, 0xc000
	ds_read_b128 v[196:199], v159
	ds_read_b128 v[200:203], v159 offset:1024
	ds_read_b128 v[204:207], v159 offset:2048
	ds_read_b128 v[208:211], v159 offset:3072
	ds_read_b128 v[212:215], v159 offset:4096
	ds_read_b128 v[216:219], v159 offset:5120
	ds_read_b128 v[220:223], v159 offset:6144
	ds_read_b128 v[224:227], v159 offset:7168
	global_load_lds_dwordx4 v[160:161], off
	v_lshl_add_u64 v[160:161], v[148:149], 0, s[44:45]
	s_add_i32 m0, s17, 0xe000
	s_nop 0
	global_load_lds_dwordx4 v[160:161], off
	s_waitcnt vmcnt(8)
	s_waitcnt lgkmcnt(0)
	s_barrier
	s_setprio 3
	v_mfma_f32_16x16x32_bf16 v[54:57], v[164:167], v[196:199], v[54:57]
	v_mfma_f32_16x16x32_bf16 v[50:53], v[172:175], v[196:199], v[50:53]
	v_mfma_f32_16x16x32_bf16 v[70:73], v[164:167], v[204:207], v[70:73]
	v_mfma_f32_16x16x32_bf16 v[66:69], v[172:175], v[204:207], v[66:69]
	v_mfma_f32_16x16x32_bf16 v[78:81], v[164:167], v[212:215], v[78:81]
	v_mfma_f32_16x16x32_bf16 v[74:77], v[172:175], v[212:215], v[74:77]
	v_mfma_f32_16x16x32_bf16 v[86:89], v[164:167], v[220:223], v[86:89]
	v_mfma_f32_16x16x32_bf16 v[82:85], v[172:175], v[220:223], v[82:85]
	v_mfma_f32_16x16x32_bf16 v[54:57], v[168:171], v[200:203], v[54:57]
	v_mfma_f32_16x16x32_bf16 v[50:53], v[176:179], v[200:203], v[50:53]
	v_mfma_f32_16x16x32_bf16 v[70:73], v[168:171], v[208:211], v[70:73]
	v_mfma_f32_16x16x32_bf16 v[66:69], v[176:179], v[208:211], v[66:69]
	v_mfma_f32_16x16x32_bf16 v[78:81], v[168:171], v[216:219], v[78:81]
	v_mfma_f32_16x16x32_bf16 v[74:77], v[176:179], v[216:219], v[74:77]
	v_mfma_f32_16x16x32_bf16 v[86:89], v[168:171], v[224:227], v[86:89]
	v_mfma_f32_16x16x32_bf16 v[82:85], v[176:179], v[224:227], v[82:85]
	v_mfma_f32_16x16x32_bf16 v[14:17], v[180:183], v[196:199], v[14:17]
	v_mfma_f32_16x16x32_bf16 v[10:13], v[188:191], v[196:199], v[10:13]
	v_mfma_f32_16x16x32_bf16 v[22:25], v[180:183], v[204:207], v[22:25]
	v_mfma_f32_16x16x32_bf16 v[18:21], v[188:191], v[204:207], v[18:21]
	v_mfma_f32_16x16x32_bf16 v[30:33], v[180:183], v[212:215], v[30:33]
	v_mfma_f32_16x16x32_bf16 v[26:29], v[188:191], v[212:215], v[26:29]
	v_mfma_f32_16x16x32_bf16 v[46:49], v[180:183], v[220:223], v[46:49]
	v_mfma_f32_16x16x32_bf16 v[42:45], v[188:191], v[220:223], v[42:45]
	v_mfma_f32_16x16x32_bf16 v[14:17], v[184:187], v[200:203], v[14:17]
	v_mfma_f32_16x16x32_bf16 v[10:13], v[192:195], v[200:203], v[10:13]
	v_mfma_f32_16x16x32_bf16 v[22:25], v[184:187], v[208:211], v[22:25]
	v_mfma_f32_16x16x32_bf16 v[18:21], v[192:195], v[208:211], v[18:21]
	v_mfma_f32_16x16x32_bf16 v[30:33], v[184:187], v[216:219], v[30:33]
	v_mfma_f32_16x16x32_bf16 v[26:29], v[192:195], v[216:219], v[26:29]
	v_mfma_f32_16x16x32_bf16 v[46:49], v[184:187], v[224:227], v[46:49]
	v_mfma_f32_16x16x32_bf16 v[42:45], v[192:195], v[224:227], v[42:45]
	s_setprio 0
	s_barrier
	s_add_i32 s0, s72, s57
	v_lshl_add_u64 v[160:161], s[46:47], 0, v[132:133]
	s_mov_b32 m0, s0
	ds_read_b128 v[196:199], v159 offset:16384
	ds_read_b128 v[200:203], v159 offset:17408
	ds_read_b128 v[204:207], v159 offset:18432
	ds_read_b128 v[208:211], v159 offset:19456
	ds_read_b128 v[212:215], v159 offset:20480
	ds_read_b128 v[216:219], v159 offset:21504
	ds_read_b128 v[220:223], v159 offset:22528
	ds_read_b128 v[224:227], v159 offset:23552
	global_load_lds_dwordx4 v[160:161], off
	s_add_i32 m0, s0, 0x2000
	s_add_u32 s68, s46, 0x20000
	v_lshl_add_u64 v[228:229], s[46:47], 0, v[136:137]
	s_addc_u32 s69, s47, 0
	s_add_i32 s0, s73, s57
	global_load_lds_dwordx4 v[228:229], off
	v_lshl_add_u64 v[230:231], s[68:69], 0, v[132:133]
	s_mov_b32 m0, s0
	v_lshl_add_u64 v[232:233], s[48:49], 0, v[134:135]
	global_load_lds_dwordx4 v[230:231], off
	v_lshl_add_u64 v[230:231], s[68:69], 0, v[136:137]
	s_add_i32 m0, s0, 0x2000
	s_nop 0
	global_load_lds_dwordx4 v[230:231], off
	v_lshl_add_u64 v[230:231], s[48:49], 0, v[130:131]
	s_mov_b32 m0, s17
	s_nop 0
	global_load_lds_dwordx4 v[230:231], off
	s_mov_b32 m0, s59
	s_nop 0
	global_load_lds_dwordx4 v[232:233], off
	s_waitcnt vmcnt(8)
	s_waitcnt lgkmcnt(0)
	s_barrier
; #define PG8_STAGE(bufoff, gbase, voff) do { _Pragma("unroll") for (int _i = 0; _i < 2; ++_i) \
;         __builtin_amdgcn_global_load_lds((const unsigned*)((const char*)(gbase) + (voff)[_i]), (PG8_LAS unsigned*)(lds + (bufoff) + ldsw + _i * 8192), 16, 0, 0); } while (0)
; #define PG8_LDA(dst, b, h) do { _Pragma("unroll") for (int m = 0; m < 4; ++m) Frag<F8>::load(dst[m], lds + PG8_SA(b, h) + aoff + m * 2048); } while (0)
; #define PG8_LDB(dst, b, h) do { _Pragma("unroll") for (int n = 0; n < 2; ++n) Frag<F8>::load(dst[n], lds + PG8_SB(b, h) + boff + n * 2048); } while (0)
; #define PG8_MMA(ai, bj, At, Bt) do { __builtin_amdgcn_s_setprio(3); _Pragma("unroll") for (int m = 0; m < 4; ++m) _Pragma("unroll") for (int n = 0; n < 2; ++n) Frag<F8>::mma(acc[ai][bj][m][n], Bt[n], At[m]); \
;         __builtin_amdgcn_s_setprio(0); } while (0)
; #define PG8_WAIT_V(n) asm volatile("s_waitcnt vmcnt(" #n ")" ::: "memory")
; #define PG8_WAIT_L(n) asm volatile("s_waitcnt lgkmcnt(" #n ")" ::: "memory")
; #define PG8_BAR __builtin_amdgcn_s_barrier()
; #define PG8_SCHED __builtin_amdgcn_sched_barrier(0)
; template <class Epi, class Sched, bool ALIGN_EPI = false, bool SP2 = false, bool F8 = false>
; __device__ __forceinline__ void gemm_phase(PG8_LAS unsigned char* lds, const Gemm g, const Sched& S, const Epi& E) {
;     ...
;             PG8_WAIT_V(8); PG8_WAIT_L(0); PG8_BAR; PG8_MMA(1, 0, At, B0); PG8_MMA(1, 1, At, B1); PG8_BAR; PG8_SCHED;
;             PG8_LDB(B0, 1, 0); PG8_LDB(B1, 1, 1); PG8_SCHED; PG8_LDA(At, 1, 0); PG8_STAGE(PG8_SA(0, 1), a2 + hstep, voffA);
;             PG8_WAIT_V(8); PG8_WAIT_L(0); PG8_BAR; PG8_MMA(0, 0, At, B0); PG8_MMA(0, 1, At, B1); PG8_BAR; PG8_SCHED;
	s_setprio 3
	v_mfma_f32_16x16x32_bf16 v[38:41], v[164:167], v[196:199], v[38:41]
	v_mfma_f32_16x16x32_bf16 v[34:37], v[172:175], v[196:199], v[34:37]
	v_mfma_f32_16x16x32_bf16 v[62:65], v[164:167], v[204:207], v[62:65]
	v_mfma_f32_16x16x32_bf16 v[58:61], v[172:175], v[204:207], v[58:61]
	v_mfma_f32_16x16x32_bf16 v[118:121], v[164:167], v[212:215], v[118:121]
	v_mfma_f32_16x16x32_bf16 v[114:117], v[172:175], v[212:215], v[114:117]
	v_mfma_f32_16x16x32_bf16 v[126:129], v[164:167], v[220:223], v[126:129]
	v_mfma_f32_16x16x32_bf16 v[122:125], v[172:175], v[220:223], v[122:125]
	v_mfma_f32_16x16x32_bf16 v[38:41], v[168:171], v[200:203], v[38:41]
	v_mfma_f32_16x16x32_bf16 v[34:37], v[176:179], v[200:203], v[34:37]
	v_mfma_f32_16x16x32_bf16 v[62:65], v[168:171], v[208:211], v[62:65]
	v_mfma_f32_16x16x32_bf16 v[58:61], v[176:179], v[208:211], v[58:61]
	v_mfma_f32_16x16x32_bf16 v[118:121], v[168:171], v[216:219], v[118:121]
	v_mfma_f32_16x16x32_bf16 v[114:117], v[176:179], v[216:219], v[114:117]
	v_mfma_f32_16x16x32_bf16 v[126:129], v[168:171], v[224:227], v[126:129]
	v_mfma_f32_16x16x32_bf16 v[122:125], v[176:179], v[224:227], v[122:125]
	v_mfma_f32_16x16x32_bf16 v[6:9], v[180:183], v[196:199], v[6:9]
	v_mfma_f32_16x16x32_bf16 v[2:5], v[188:191], v[196:199], v[2:5]
	v_mfma_f32_16x16x32_bf16 v[94:97], v[180:183], v[204:207], v[94:97]
	v_mfma_f32_16x16x32_bf16 v[90:93], v[188:191], v[204:207], v[90:93]
	v_mfma_f32_16x16x32_bf16 v[102:105], v[180:183], v[212:215], v[102:105]
	v_mfma_f32_16x16x32_bf16 v[98:101], v[188:191], v[212:215], v[98:101]
	v_mfma_f32_16x16x32_bf16 v[110:113], v[180:183], v[220:223], v[110:113]
	v_mfma_f32_16x16x32_bf16 v[106:109], v[188:191], v[220:223], v[106:109]
	v_mfma_f32_16x16x32_bf16 v[6:9], v[184:187], v[200:203], v[6:9]
	v_mfma_f32_16x16x32_bf16 v[2:5], v[192:195], v[200:203], v[2:5]
	v_mfma_f32_16x16x32_bf16 v[94:97], v[184:187], v[208:211], v[94:97]
	v_mfma_f32_16x16x32_bf16 v[90:93], v[192:195], v[208:211], v[90:93]
	v_mfma_f32_16x16x32_bf16 v[102:105], v[184:187], v[216:219], v[102:105]
	v_mfma_f32_16x16x32_bf16 v[98:101], v[192:195], v[216:219], v[98:101]
	v_mfma_f32_16x16x32_bf16 v[110:113], v[184:187], v[224:227], v[110:113]
	v_mfma_f32_16x16x32_bf16 v[106:109], v[192:195], v[224:227], v[106:109]
	s_setprio 0
	s_barrier
	s_add_i32 s0, 0, 0x18000
	s_add_i32 s1, 0, 0x1c000
	v_add_u32_e32 v176, s0, v157
	v_add_u32_e32 v192, s1, v157
	ds_read_b128 v[164:167], v176
	ds_read_b128 v[168:171], v176 offset:1024
	ds_read_b128 v[172:175], v176 offset:2048
	ds_read_b128 v[176:179], v176 offset:3072
	ds_read_b128 v[180:183], v192
	ds_read_b128 v[184:187], v192 offset:1024
	ds_read_b128 v[188:191], v192 offset:2048
	ds_read_b128 v[192:195], v192 offset:3072
	s_add_u32 s48, s48, 0x20000
	s_addc_u32 s49, s49, 0
	s_mov_b32 m0, s60
	v_lshl_add_u64 v[234:235], s[48:49], 0, v[130:131]
	ds_read_b128 v[196:199], v159 offset:32768
	ds_read_b128 v[200:203], v159 offset:33792
	ds_read_b128 v[204:207], v159 offset:34816
	ds_read_b128 v[208:211], v159 offset:35840
	ds_read_b128 v[212:215], v159 offset:36864
	ds_read_b128 v[216:219], v159 offset:37888
	ds_read_b128 v[220:223], v159 offset:38912
	ds_read_b128 v[224:227], v159 offset:39936
	global_load_lds_dwordx4 v[234:235], off
	v_lshl_add_u64 v[234:235], s[48:49], 0, v[134:135]
	s_mov_b32 m0, s61
	s_nop 0
	global_load_lds_dwordx4 v[234:235], off
	s_waitcnt vmcnt(8)
	s_waitcnt lgkmcnt(0)
	s_barrier
	s_setprio 3
	v_mfma_f32_16x16x32_bf16 v[54:57], v[164:167], v[196:199], v[54:57]
	v_mfma_f32_16x16x32_bf16 v[50:53], v[172:175], v[196:199], v[50:53]
	v_mfma_f32_16x16x32_bf16 v[70:73], v[164:167], v[204:207], v[70:73]
	v_mfma_f32_16x16x32_bf16 v[66:69], v[172:175], v[204:207], v[66:69]
	v_mfma_f32_16x16x32_bf16 v[78:81], v[164:167], v[212:215], v[78:81]
	v_mfma_f32_16x16x32_bf16 v[74:77], v[172:175], v[212:215], v[74:77]
	v_mfma_f32_16x16x32_bf16 v[86:89], v[164:167], v[220:223], v[86:89]
	v_mfma_f32_16x16x32_bf16 v[82:85], v[172:175], v[220:223], v[82:85]
	v_mfma_f32_16x16x32_bf16 v[54:57], v[168:171], v[200:203], v[54:57]
	v_mfma_f32_16x16x32_bf16 v[50:53], v[176:179], v[200:203], v[50:53]
	v_mfma_f32_16x16x32_bf16 v[70:73], v[168:171], v[208:211], v[70:73]
	v_mfma_f32_16x16x32_bf16 v[66:69], v[176:179], v[208:211], v[66:69]
	v_mfma_f32_16x16x32_bf16 v[78:81], v[168:171], v[216:219], v[78:81]
	v_mfma_f32_16x16x32_bf16 v[74:77], v[176:179], v[216:219], v[74:77]
	v_mfma_f32_16x16x32_bf16 v[86:89], v[168:171], v[224:227], v[86:89]
	v_mfma_f32_16x16x32_bf16 v[82:85], v[176:179], v[224:227], v[82:85]
	v_mfma_f32_16x16x32_bf16 v[14:17], v[180:183], v[196:199], v[14:17]
	v_mfma_f32_16x16x32_bf16 v[10:13], v[188:191], v[196:199], v[10:13]
	v_mfma_f32_16x16x32_bf16 v[22:25], v[180:183], v[204:207], v[22:25]
	v_mfma_f32_16x16x32_bf16 v[18:21], v[188:191], v[204:207], v[18:21]
	v_mfma_f32_16x16x32_bf16 v[30:33], v[180:183], v[212:215], v[30:33]
	v_mfma_f32_16x16x32_bf16 v[26:29], v[188:191], v[212:215], v[26:29]
	v_mfma_f32_16x16x32_bf16 v[46:49], v[180:183], v[220:223], v[46:49]
	v_mfma_f32_16x16x32_bf16 v[42:45], v[188:191], v[220:223], v[42:45]
	v_mfma_f32_16x16x32_bf16 v[14:17], v[184:187], v[200:203], v[14:17]
	v_mfma_f32_16x16x32_bf16 v[10:13], v[192:195], v[200:203], v[10:13]
	v_mfma_f32_16x16x32_bf16 v[22:25], v[184:187], v[208:211], v[22:25]
	v_mfma_f32_16x16x32_bf16 v[18:21], v[192:195], v[208:211], v[18:21]
	v_mfma_f32_16x16x32_bf16 v[30:33], v[184:187], v[216:219], v[30:33]
	v_mfma_f32_16x16x32_bf16 v[26:29], v[192:195], v[216:219], v[26:29]
	v_mfma_f32_16x16x32_bf16 v[46:49], v[184:187], v[224:227], v[46:49]
	v_mfma_f32_16x16x32_bf16 v[42:45], v[192:195], v[224:227], v[42:45]
	s_setprio 0
	s_barrier
; #define PG8_STAGE(bufoff, gbase, voff) do { _Pragma("unroll") for (int _i = 0; _i < 2; ++_i) \
;         __builtin_amdgcn_global_load_lds((const unsigned*)((const char*)(gbase) + (voff)[_i]), (PG8_LAS unsigned*)(lds + (bufoff) + ldsw + _i * 8192), 16, 0, 0); } while (0)
; #define PG8_LDA(dst, b, h) do { _Pragma("unroll") for (int m = 0; m < 4; ++m) Frag<F8>::load(dst[m], lds + PG8_SA(b, h) + aoff + m * 2048); } while (0)
; #define PG8_MMA(ai, bj, At, Bt) do { __builtin_amdgcn_s_setprio(3); _Pragma("unroll") for (int m = 0; m < 4; ++m) _Pragma("unroll") for (int n = 0; n < 2; ++n) Frag<F8>::mma(acc[ai][bj][m][n], Bt[n], At[m]); \
;         __builtin_amdgcn_s_setprio(0); } while (0)
; #define PG8_WAIT_V(n) asm volatile("s_waitcnt vmcnt(" #n ")" ::: "memory")
; #define PG8_WAIT_L(n) asm volatile("s_waitcnt lgkmcnt(" #n ")" ::: "memory")
; #define PG8_BAR __builtin_amdgcn_s_barrier()
; #define PG8_SCHED __builtin_amdgcn_sched_barrier(0)
; template <class Epi, class Sched, bool ALIGN_EPI = false, bool SP2 = false, bool F8 = false>
; __device__ __forceinline__ void gemm_phase(PG8_LAS unsigned char* lds, const Gemm g, const Sched& S, const Epi& E) {
;     ...
;             PG8_LDA(At, 1, 1); PG8_STAGE(PG8_SB(1, 0), b3, voffB); PG8_STAGE(PG8_SB(1, 1), b3 + hstep, voffB); PG8_STAGE(PG8_SA(1, 0), a3, voffA);
;             PG8_WAIT_V(8); PG8_WAIT_L(0); PG8_BAR; PG8_MMA(1, 0, At, B0); PG8_MMA(1, 1, At, B1); PG8_BAR; PG8_SCHED;
;     ...
;         if constexpr (ALIGN_EPI) { if (wr == 0) PG8_BAR; }
	s_add_i32 s0, s0, s57
	v_lshl_add_u64 v[160:161], v[160:161], 0, s[22:23]
	s_mov_b32 m0, s0
	ds_read_b128 v[196:199], v159 offset:49152
	ds_read_b128 v[200:203], v159 offset:50176
	ds_read_b128 v[204:207], v159 offset:51200
	ds_read_b128 v[208:211], v159 offset:52224
	ds_read_b128 v[212:215], v159 offset:53248
	ds_read_b128 v[216:219], v159 offset:54272
	ds_read_b128 v[220:223], v159 offset:55296
	ds_read_b128 v[224:227], v159 offset:56320
	global_load_lds_dwordx4 v[160:161], off
	s_add_i32 m0, s0, 0x2000
	s_add_u32 s46, s46, 0x20080
	v_lshl_add_u64 v[160:161], v[228:229], 0, s[22:23]
	s_addc_u32 s47, s47, 0
	s_add_i32 s0, s1, s57
	global_load_lds_dwordx4 v[160:161], off
	v_lshl_add_u64 v[160:161], s[46:47], 0, v[132:133]
	s_mov_b32 m0, s0
	s_nop 0
	global_load_lds_dwordx4 v[160:161], off
	v_lshl_add_u64 v[160:161], s[46:47], 0, v[136:137]
	s_add_i32 m0, s0, 0x2000
	s_nop 0
	global_load_lds_dwordx4 v[160:161], off
	v_lshl_add_u64 v[160:161], v[230:231], 0, s[22:23]
	s_mov_b32 m0, s70
	s_nop 0
	global_load_lds_dwordx4 v[160:161], off
	v_lshl_add_u64 v[160:161], v[232:233], 0, s[22:23]
	s_mov_b32 m0, s71
	s_nop 0
	global_load_lds_dwordx4 v[160:161], off
	s_waitcnt vmcnt(8)
	s_waitcnt lgkmcnt(0)
	s_barrier
	s_setprio 3
	v_mfma_f32_16x16x32_bf16 v[38:41], v[164:167], v[196:199], v[38:41]
	v_mfma_f32_16x16x32_bf16 v[34:37], v[172:175], v[196:199], v[34:37]
	v_mfma_f32_16x16x32_bf16 v[62:65], v[164:167], v[204:207], v[62:65]
	v_mfma_f32_16x16x32_bf16 v[58:61], v[172:175], v[204:207], v[58:61]
	v_mfma_f32_16x16x32_bf16 v[118:121], v[164:167], v[212:215], v[118:121]
	v_mfma_f32_16x16x32_bf16 v[114:117], v[172:175], v[212:215], v[114:117]
	v_mfma_f32_16x16x32_bf16 v[126:129], v[164:167], v[220:223], v[126:129]
	v_mfma_f32_16x16x32_bf16 v[122:125], v[172:175], v[220:223], v[122:125]
	v_mfma_f32_16x16x32_bf16 v[38:41], v[168:171], v[200:203], v[38:41]
	v_mfma_f32_16x16x32_bf16 v[34:37], v[176:179], v[200:203], v[34:37]
	v_mfma_f32_16x16x32_bf16 v[62:65], v[168:171], v[208:211], v[62:65]
	v_mfma_f32_16x16x32_bf16 v[58:61], v[176:179], v[208:211], v[58:61]
	v_mfma_f32_16x16x32_bf16 v[118:121], v[168:171], v[216:219], v[118:121]
	v_mfma_f32_16x16x32_bf16 v[114:117], v[176:179], v[216:219], v[114:117]
	v_mfma_f32_16x16x32_bf16 v[126:129], v[168:171], v[224:227], v[126:129]
	v_mfma_f32_16x16x32_bf16 v[122:125], v[176:179], v[224:227], v[122:125]
	v_mfma_f32_16x16x32_bf16 v[6:9], v[180:183], v[196:199], v[6:9]
	v_mfma_f32_16x16x32_bf16 v[2:5], v[188:191], v[196:199], v[2:5]
	v_mfma_f32_16x16x32_bf16 v[94:97], v[180:183], v[204:207], v[94:97]
	v_mfma_f32_16x16x32_bf16 v[90:93], v[188:191], v[204:207], v[90:93]
	v_mfma_f32_16x16x32_bf16 v[102:105], v[180:183], v[212:215], v[102:105]
	v_mfma_f32_16x16x32_bf16 v[98:101], v[188:191], v[212:215], v[98:101]
	v_mfma_f32_16x16x32_bf16 v[110:113], v[180:183], v[220:223], v[110:113]
	v_mfma_f32_16x16x32_bf16 v[106:109], v[188:191], v[220:223], v[106:109]
	v_mfma_f32_16x16x32_bf16 v[6:9], v[184:187], v[200:203], v[6:9]
	v_mfma_f32_16x16x32_bf16 v[2:5], v[192:195], v[200:203], v[2:5]
	v_mfma_f32_16x16x32_bf16 v[94:97], v[184:187], v[208:211], v[94:97]
	v_mfma_f32_16x16x32_bf16 v[90:93], v[192:195], v[208:211], v[90:93]
	v_mfma_f32_16x16x32_bf16 v[102:105], v[184:187], v[216:219], v[102:105]
	v_mfma_f32_16x16x32_bf16 v[98:101], v[192:195], v[216:219], v[98:101]
	v_mfma_f32_16x16x32_bf16 v[110:113], v[184:187], v[224:227], v[110:113]
	v_mfma_f32_16x16x32_bf16 v[106:109], v[192:195], v[224:227], v[106:109]
	s_setprio 0
	s_barrier
	s_add_i32 s33, s33, 2
	s_add_u32 s44, s44, 0x100
	s_addc_u32 s45, s45, 0
	s_cmp_gt_u32 s33, 5
	s_cbranch_scc0 .LBB0_1066
	s_and_b64 vcc, exec, s[24:25]
	s_cbranch_vccz .LBB0_1069
	s_barrier

; #define PG8_STAGE(bufoff, gbase, voff) do { _Pragma("unroll") for (int _i = 0; _i < 2; ++_i) \
;         __builtin_amdgcn_global_load_lds((const unsigned*)((const char*)(gbase) + (voff)[_i]), (PG8_LAS unsigned*)(lds + (bufoff) + ldsw + _i * 8192), 16, 0, 0); } while (0)
; #define PG8_LDA(dst, b, h) do { _Pragma("unroll") for (int m = 0; m < 4; ++m) Frag<F8>::load(dst[m], lds + PG8_SA(b, h) + aoff + m * 2048); } while (0)
; #define PG8_LDB(dst, b, h) do { _Pragma("unroll") for (int n = 0; n < 2; ++n) Frag<F8>::load(dst[n], lds + PG8_SB(b, h) + boff + n * 2048); } while (0)
; #define PG8_WAIT_V(n) asm volatile("s_waitcnt vmcnt(" #n ")" ::: "memory")
; #define PG8_WAIT_L(n) asm volatile("s_waitcnt lgkmcnt(" #n ")" ::: "memory")
; #define PG8_BAR __builtin_amdgcn_s_barrier()
; template <class Epi, class Sched, bool ALIGN_EPI = false, bool SP2 = false, bool F8 = false>
; __device__ __forceinline__ void gemm_phase(PG8_LAS unsigned char* lds, const Gemm g, const Sched& S, const Epi& E) {
;     ...
;         const char* nA = has_next ? (const char*)g.A + (size_t)nxt.pm * tstep + nxt.ko : cA; const char* nB = has_next ? (const char*)g.Bt + (size_t)nxt.pn * tstep + nxt.ko : cB;
;         for (int t = 0; t < nt; t += 2) {
;             const bool last = (t == nt - 2);
;             const char* a1 = cA + (size_t)(t + 1) * kstep;
;             const char* a2 = last ? nA : cA + (size_t)(t + 2) * kstep; const char* b2 = last ? nB : cB + (size_t)(t + 2) * kstep;
;             const char* a3 = a2 + kstep; const char* b3 = b2 + kstep;
;             if (last && has_next) S.a_ready(nxt);
;             if constexpr (SP2) {
;             PG8_LDB(B0, 0, 0); PG8_LDB(B1, 0, 1); PG8_SCHED; PG8_LDA(At, 0, 0); PG8_STAGE(PG8_SA(1, 1), a1 + hstep, voffA);
;             PG8_WAIT_V(8); PG8_WAIT_L(0); PG8_BAR; PG8_MMA(0, 0, At, B0); PG8_MMA(0, 1, At, B1); PG8_BAR; PG8_SCHED;
;             PG8_LDA(At, 0, 1); PG8_STAGE(PG8_SB(0, 0), b2, voffB); PG8_STAGE(PG8_SB(0, 1), b2 + hstep, voffB); PG8_STAGE(PG8_SA(0, 0), a2, voffA);
;             PG8_WAIT_V(8); PG8_WAIT_L(0); PG8_BAR; PG8_MMA(1, 0, At, B0); PG8_MMA(1, 1, At, B1); PG8_BAR; PG8_SCHED;
;             PG8_LDB(B0, 1, 0); PG8_LDB(B1, 1, 1); PG8_SCHED; PG8_LDA(At, 1, 0); PG8_STAGE(PG8_SA(0, 1), a2 + hstep, voffA);
;             PG8_WAIT_V(8); PG8_WAIT_L(0); PG8_BAR; PG8_MMA(0, 0, At, B0); PG8_MMA(0, 1, At, B1); PG8_BAR; PG8_SCHED;
.LBB0_1309:
	s_ashr_i32 s25, s24, 31
	s_lshl_b64 s[4:5], s[24:25], 18
	s_add_u32 s30, s48, s4
	s_addc_u32 s31, s49, s5
	s_and_b64 s[4:5], s[22:23], exec
	s_cselect_b32 s25, s31, s43
	s_cselect_b32 s77, s30, s42
	s_ashr_i32 s27, s26, 31
	s_lshl_b64 s[4:5], s[26:27], 18
	s_add_u32 s36, s50, s4
	s_addc_u32 s37, s51, s5
	s_and_b64 s[4:5], s[22:23], exec
	s_cselect_b32 s27, s37, s45
	s_cselect_b32 s78, s36, s44
	s_add_u32 s42, s42, 0x20080
	s_addc_u32 s43, s43, 0
	s_add_u32 s79, s44, 0x100
	s_addc_u32 s80, s45, 0
	s_mov_b32 s81, -2
	ds_read_b128 v[18:21], v186
	ds_read_b128 v[22:25], v186 offset:1024
	ds_read_b128 v[26:29], v186 offset:2048
	ds_read_b128 v[30:33], v186 offset:3072
	ds_read_b128 v[2:5], v187
	ds_read_b128 v[6:9], v187 offset:1024
	ds_read_b128 v[10:13], v187 offset:2048
	ds_read_b128 v[14:17], v187 offset:3072
	s_add_u32 s0, s42, 0xfffe0080
	s_addc_u32 s1, s43, -1
	s_cmp_eq_u32 s81, 4
	s_cselect_b32 s47, s25, s1
	s_cselect_b32 s46, s77, s0
	s_cselect_b32 s45, s27, s80
	s_cselect_b32 s44, s78, s79
	v_lshl_add_u64 v[214:215], s[42:43], 0, v[172:173]
	s_add_i32 m0, s39, 0xc000
	ds_read_b128 v[176:179], v188
	ds_read_b128 v[180:183], v188 offset:1024
	ds_read_b128 v[190:193], v188 offset:2048
	ds_read_b128 v[194:197], v188 offset:3072
	ds_read_b128 v[198:201], v188 offset:4096
	ds_read_b128 v[202:205], v188 offset:5120
	ds_read_b128 v[206:209], v188 offset:6144
	ds_read_b128 v[210:213], v188 offset:7168
	global_load_lds_dwordx4 v[214:215], off
	v_lshl_add_u64 v[214:215], s[42:43], 0, v[174:175]
	s_add_i32 m0, s39, 0xe000
	s_nop 0
	global_load_lds_dwordx4 v[214:215], off
	s_waitcnt vmcnt(8)
	s_waitcnt lgkmcnt(0)
	s_barrier
	s_setprio 3
	v_mfma_f32_16x16x128_f8f6f4 v[158:161], v[18:25], v[176:183], 0
	v_mfma_f32_16x16x128_f8f6f4 v[150:153], v[26:33], v[176:183], 0
	v_mfma_f32_16x16x128_f8f6f4 v[142:145], v[18:25], v[190:197], 0
	v_mfma_f32_16x16x128_f8f6f4 v[134:137], v[26:33], v[190:197], 0
	v_mfma_f32_16x16x128_f8f6f4 v[126:129], v[18:25], v[198:205], 0
	v_mfma_f32_16x16x128_f8f6f4 v[118:121], v[26:33], v[198:205], 0
	v_mfma_f32_16x16x128_f8f6f4 v[110:113], v[18:25], v[206:213], 0
	v_mfma_f32_16x16x128_f8f6f4 v[102:105], v[26:33], v[206:213], 0
	v_mfma_f32_16x16x128_f8f6f4 v[154:157], v[2:9], v[176:183], 0
	v_mfma_f32_16x16x128_f8f6f4 v[146:149], v[10:17], v[176:183], 0
	v_mfma_f32_16x16x128_f8f6f4 v[138:141], v[2:9], v[190:197], 0
	v_mfma_f32_16x16x128_f8f6f4 v[130:133], v[10:17], v[190:197], 0
	v_mfma_f32_16x16x128_f8f6f4 v[122:125], v[2:9], v[198:205], 0
	v_mfma_f32_16x16x128_f8f6f4 v[114:117], v[10:17], v[198:205], 0
	v_mfma_f32_16x16x128_f8f6f4 v[106:109], v[2:9], v[206:213], 0
	v_mfma_f32_16x16x128_f8f6f4 v[98:101], v[10:17], v[206:213], 0
	s_setprio 0
	s_barrier
	s_add_i32 s0, s74, s52
	v_lshl_add_u64 v[176:177], s[44:45], 0, v[168:169]
	s_mov_b32 m0, s0
	ds_read_b128 v[190:193], v188 offset:16384
	ds_read_b128 v[194:197], v188 offset:17408
	ds_read_b128 v[198:201], v188 offset:18432
	ds_read_b128 v[202:205], v188 offset:19456
	ds_read_b128 v[206:209], v188 offset:20480
	ds_read_b128 v[210:213], v188 offset:21504
	ds_read_b128 v[214:217], v188 offset:22528
	ds_read_b128 v[218:221], v188 offset:23552
	global_load_lds_dwordx4 v[176:177], off
	s_add_i32 m0, s0, 0x2000
	s_add_u32 s4, s44, 0x20000
	v_lshl_add_u64 v[178:179], s[44:45], 0, v[164:165]
	s_addc_u32 s5, s45, 0
	s_add_i32 s0, s75, s52
	global_load_lds_dwordx4 v[178:179], off
	v_lshl_add_u64 v[180:181], s[4:5], 0, v[168:169]
	s_mov_b32 m0, s0
	v_lshl_add_u64 v[182:183], s[46:47], 0, v[166:167]
	global_load_lds_dwordx4 v[180:181], off
	v_lshl_add_u64 v[180:181], s[4:5], 0, v[164:165]
	s_add_i32 m0, s0, 0x2000
	s_nop 0
	global_load_lds_dwordx4 v[180:181], off
	v_lshl_add_u64 v[180:181], s[46:47], 0, v[170:171]
	s_mov_b32 m0, s39
	s_nop 0
	global_load_lds_dwordx4 v[180:181], off
	s_mov_b32 m0, s41
	s_nop 0
	global_load_lds_dwordx4 v[182:183], off
	s_waitcnt vmcnt(8)
	s_waitcnt lgkmcnt(0)
	s_barrier
	s_setprio 3
	v_mfma_f32_16x16x128_f8f6f4 v[94:97], v[18:25], v[190:197], 0
	v_mfma_f32_16x16x128_f8f6f4 v[86:89], v[26:33], v[190:197], 0
	v_mfma_f32_16x16x128_f8f6f4 v[78:81], v[18:25], v[198:205], 0
	v_mfma_f32_16x16x128_f8f6f4 v[70:73], v[26:33], v[198:205], 0
	v_mfma_f32_16x16x128_f8f6f4 v[62:65], v[18:25], v[206:213], 0
	v_mfma_f32_16x16x128_f8f6f4 v[54:57], v[26:33], v[206:213], 0
	v_mfma_f32_16x16x128_f8f6f4 v[46:49], v[18:25], v[214:221], 0
	v_mfma_f32_16x16x128_f8f6f4 v[38:41], v[26:33], v[214:221], 0
	v_mfma_f32_16x16x128_f8f6f4 v[90:93], v[2:9], v[190:197], 0
	v_mfma_f32_16x16x128_f8f6f4 v[82:85], v[10:17], v[190:197], 0
	v_mfma_f32_16x16x128_f8f6f4 v[74:77], v[2:9], v[198:205], 0
	v_mfma_f32_16x16x128_f8f6f4 v[66:69], v[10:17], v[198:205], 0
	v_mfma_f32_16x16x128_f8f6f4 v[58:61], v[2:9], v[206:213], 0
	v_mfma_f32_16x16x128_f8f6f4 v[50:53], v[10:17], v[206:213], 0
	v_mfma_f32_16x16x128_f8f6f4 v[42:45], v[2:9], v[214:221], 0
	v_mfma_f32_16x16x128_f8f6f4 v[34:37], v[10:17], v[214:221], 0
	s_setprio 0
	s_barrier
	s_add_i32 s0, 0, 0x18000
	s_add_i32 s1, 0, 0x1c000
	v_add_u32_e32 v14, s0, v184
	v_add_u32_e32 v30, s1, v184
	ds_read_b128 v[2:5], v14
	ds_read_b128 v[6:9], v14 offset:1024
	ds_read_b128 v[10:13], v14 offset:2048
	ds_read_b128 v[14:17], v14 offset:3072
	ds_read_b128 v[18:21], v30
	ds_read_b128 v[22:25], v30 offset:1024
	ds_read_b128 v[26:29], v30 offset:2048
	ds_read_b128 v[30:33], v30 offset:3072
	s_add_u32 s4, s46, 0x20000
	s_addc_u32 s5, s47, 0
	s_mov_b32 m0, s58
	v_lshl_add_u64 v[222:223], s[4:5], 0, v[170:171]
	ds_read_b128 v[190:193], v188 offset:32768
	ds_read_b128 v[194:197], v188 offset:33792
	ds_read_b128 v[198:201], v188 offset:34816
	ds_read_b128 v[202:205], v188 offset:35840
	ds_read_b128 v[206:209], v188 offset:36864
	ds_read_b128 v[210:213], v188 offset:37888
	ds_read_b128 v[214:217], v188 offset:38912
	ds_read_b128 v[218:221], v188 offset:39936
	global_load_lds_dwordx4 v[222:223], off
	v_lshl_add_u64 v[222:223], s[4:5], 0, v[166:167]
	s_mov_b32 m0, s59
	s_nop 0
	global_load_lds_dwordx4 v[222:223], off
	s_waitcnt vmcnt(8)
	s_waitcnt lgkmcnt(0)
	s_barrier
; #define PG8_STAGE(bufoff, gbase, voff) do { _Pragma("unroll") for (int _i = 0; _i < 2; ++_i) \
;         __builtin_amdgcn_global_load_lds((const unsigned*)((const char*)(gbase) + (voff)[_i]), (PG8_LAS unsigned*)(lds + (bufoff) + ldsw + _i * 8192), 16, 0, 0); } while (0)
; #define PG8_LDA(dst, b, h) do { _Pragma("unroll") for (int m = 0; m < 4; ++m) Frag<F8>::load(dst[m], lds + PG8_SA(b, h) + aoff + m * 2048); } while (0)
; #define PG8_LDB(dst, b, h) do { _Pragma("unroll") for (int n = 0; n < 2; ++n) Frag<F8>::load(dst[n], lds + PG8_SB(b, h) + boff + n * 2048); } while (0)
; #define PG8_MMA(ai, bj, At, Bt) do { __builtin_amdgcn_s_setprio(3); _Pragma("unroll") for (int m = 0; m < 4; ++m) _Pragma("unroll") for (int n = 0; n < 2; ++n) Frag<F8>::mma(acc[ai][bj][m][n], Bt[n], At[m]); \
;         __builtin_amdgcn_s_setprio(0); } while (0)
; #define PG8_WAIT_V(n) asm volatile("s_waitcnt vmcnt(" #n ")" ::: "memory")
; #define PG8_WAIT_L(n) asm volatile("s_waitcnt lgkmcnt(" #n ")" ::: "memory")
; #define PG8_BAR __builtin_amdgcn_s_barrier()
; #define PG8_SCHED __builtin_amdgcn_sched_barrier(0)
; template <class Epi, class Sched, bool ALIGN_EPI = false, bool SP2 = false, bool F8 = false>
; __device__ __forceinline__ void gemm_phase(PG8_LAS unsigned char* lds, const Gemm g, const Sched& S, const Epi& E) {
;     ...
;             PG8_LDB(B0, 0, 0); PG8_LDB(B1, 0, 1); PG8_SCHED; PG8_LDA(At, 0, 0); PG8_STAGE(PG8_SA(1, 1), a1 + hstep, voffA);
;             PG8_WAIT_V(8); PG8_WAIT_L(0); PG8_BAR; PG8_MMA(0, 0, At, B0); PG8_MMA(0, 1, At, B1); PG8_BAR; PG8_SCHED;
;     ...
;             PG8_LDA(At, 1, 1); PG8_STAGE(PG8_SB(1, 0), b3, voffB); PG8_STAGE(PG8_SB(1, 1), b3 + hstep, voffB); PG8_STAGE(PG8_SA(1, 0), a3, voffA);
;             PG8_WAIT_V(8); PG8_WAIT_L(0); PG8_BAR; PG8_MMA(1, 0, At, B0); PG8_MMA(1, 1, At, B1); PG8_BAR; PG8_SCHED;
	s_setprio 3
	v_mfma_f32_16x16x128_f8f6f4 v[158:161], v[2:9], v[190:197], v[158:161]
	v_mfma_f32_16x16x128_f8f6f4 v[150:153], v[10:17], v[190:197], v[150:153]
	v_mfma_f32_16x16x128_f8f6f4 v[142:145], v[2:9], v[198:205], v[142:145]
	v_mfma_f32_16x16x128_f8f6f4 v[134:137], v[10:17], v[198:205], v[134:137]
	v_mfma_f32_16x16x128_f8f6f4 v[126:129], v[2:9], v[206:213], v[126:129]
	v_mfma_f32_16x16x128_f8f6f4 v[118:121], v[10:17], v[206:213], v[118:121]
	v_mfma_f32_16x16x128_f8f6f4 v[110:113], v[2:9], v[214:221], v[110:113]
	v_mfma_f32_16x16x128_f8f6f4 v[102:105], v[10:17], v[214:221], v[102:105]
	v_mfma_f32_16x16x128_f8f6f4 v[154:157], v[18:25], v[190:197], v[154:157]
	v_mfma_f32_16x16x128_f8f6f4 v[146:149], v[26:33], v[190:197], v[146:149]
	v_mfma_f32_16x16x128_f8f6f4 v[138:141], v[18:25], v[198:205], v[138:141]
	v_mfma_f32_16x16x128_f8f6f4 v[130:133], v[26:33], v[198:205], v[130:133]
	v_mfma_f32_16x16x128_f8f6f4 v[122:125], v[18:25], v[206:213], v[122:125]
	v_mfma_f32_16x16x128_f8f6f4 v[114:117], v[26:33], v[206:213], v[114:117]
	v_mfma_f32_16x16x128_f8f6f4 v[106:109], v[18:25], v[214:221], v[106:109]
	v_mfma_f32_16x16x128_f8f6f4 v[98:101], v[26:33], v[214:221], v[98:101]
	s_setprio 0
	s_barrier
	s_add_i32 s0, s0, s52
	v_lshl_add_u64 v[176:177], v[176:177], 0, s[14:15]
	s_mov_b32 m0, s0
	ds_read_b128 v[190:193], v188 offset:49152
	ds_read_b128 v[194:197], v188 offset:50176
	ds_read_b128 v[198:201], v188 offset:51200
	ds_read_b128 v[202:205], v188 offset:52224
	ds_read_b128 v[206:209], v188 offset:53248
	ds_read_b128 v[210:213], v188 offset:54272
	ds_read_b128 v[214:217], v188 offset:55296
	ds_read_b128 v[218:221], v188 offset:56320
	global_load_lds_dwordx4 v[176:177], off
	s_add_i32 m0, s0, 0x2000
	s_add_u32 s4, s44, 0x20080
	v_lshl_add_u64 v[176:177], v[178:179], 0, s[14:15]
	s_addc_u32 s5, s45, 0
	s_add_i32 s0, s1, s52
	global_load_lds_dwordx4 v[176:177], off
	v_lshl_add_u64 v[176:177], s[4:5], 0, v[168:169]
	s_mov_b32 m0, s0
	s_nop 0
	global_load_lds_dwordx4 v[176:177], off
	v_lshl_add_u64 v[176:177], s[4:5], 0, v[164:165]
	s_add_i32 m0, s0, 0x2000
	s_nop 0
	global_load_lds_dwordx4 v[176:177], off
	v_lshl_add_u64 v[176:177], v[180:181], 0, s[14:15]
	s_mov_b32 m0, s60
	s_nop 0
	global_load_lds_dwordx4 v[176:177], off
	v_lshl_add_u64 v[176:177], v[182:183], 0, s[14:15]
	s_mov_b32 m0, s61
	s_nop 0
	global_load_lds_dwordx4 v[176:177], off
	s_waitcnt vmcnt(8)
	s_waitcnt lgkmcnt(0)
	s_barrier
	s_setprio 3
	v_mfma_f32_16x16x128_f8f6f4 v[94:97], v[2:9], v[190:197], v[94:97]
	v_mfma_f32_16x16x128_f8f6f4 v[86:89], v[10:17], v[190:197], v[86:89]
	v_mfma_f32_16x16x128_f8f6f4 v[78:81], v[2:9], v[198:205], v[78:81]
	v_mfma_f32_16x16x128_f8f6f4 v[70:73], v[10:17], v[198:205], v[70:73]
	v_mfma_f32_16x16x128_f8f6f4 v[62:65], v[2:9], v[206:213], v[62:65]
	v_mfma_f32_16x16x128_f8f6f4 v[54:57], v[10:17], v[206:213], v[54:57]
	v_mfma_f32_16x16x128_f8f6f4 v[46:49], v[2:9], v[214:221], v[46:49]
	v_mfma_f32_16x16x128_f8f6f4 v[38:41], v[10:17], v[214:221], v[38:41]
	v_mfma_f32_16x16x128_f8f6f4 v[90:93], v[18:25], v[190:197], v[90:93]
	v_mfma_f32_16x16x128_f8f6f4 v[82:85], v[26:33], v[190:197], v[82:85]
	v_mfma_f32_16x16x128_f8f6f4 v[74:77], v[18:25], v[198:205], v[74:77]
	v_mfma_f32_16x16x128_f8f6f4 v[66:69], v[26:33], v[198:205], v[66:69]
	v_mfma_f32_16x16x128_f8f6f4 v[58:61], v[18:25], v[206:213], v[58:61]
	v_mfma_f32_16x16x128_f8f6f4 v[50:53], v[26:33], v[206:213], v[50:53]
	v_mfma_f32_16x16x128_f8f6f4 v[42:45], v[18:25], v[214:221], v[42:45]
	v_mfma_f32_16x16x128_f8f6f4 v[34:37], v[26:33], v[214:221], v[34:37]
	s_setprio 0
	s_barrier
	s_add_i32 s81, s81, 2
	s_add_u32 s42, s42, 0x100
	s_addc_u32 s43, s43, 0
	s_add_u32 s79, s79, 0x100
	s_addc_u32 s80, s80, 0
	s_cmp_gt_u32 s81, 5
	s_cbranch_scc1 .Lpeel_exit_3
.LBB0_1310:
	ds_read_b128 v[18:21], v186
	ds_read_b128 v[22:25], v186 offset:1024
	ds_read_b128 v[26:29], v186 offset:2048
	ds_read_b128 v[30:33], v186 offset:3072
	ds_read_b128 v[2:5], v187
	ds_read_b128 v[6:9], v187 offset:1024
	ds_read_b128 v[10:13], v187 offset:2048
	ds_read_b128 v[14:17], v187 offset:3072
	s_add_u32 s0, s42, 0xfffe0080
	s_addc_u32 s1, s43, -1
	s_cmp_eq_u32 s81, 4
	s_cselect_b32 s47, s25, s1
	s_cselect_b32 s46, s77, s0
	s_cselect_b32 s45, s27, s80
	s_cselect_b32 s44, s78, s79
	v_lshl_add_u64 v[214:215], s[42:43], 0, v[172:173]
	s_add_i32 m0, s39, 0xc000
	ds_read_b128 v[176:179], v188
	ds_read_b128 v[180:183], v188 offset:1024
	ds_read_b128 v[190:193], v188 offset:2048
	ds_read_b128 v[194:197], v188 offset:3072
	ds_read_b128 v[198:201], v188 offset:4096
	ds_read_b128 v[202:205], v188 offset:5120
	ds_read_b128 v[206:209], v188 offset:6144
	ds_read_b128 v[210:213], v188 offset:7168
	global_load_lds_dwordx4 v[214:215], off
	v_lshl_add_u64 v[214:215], s[42:43], 0, v[174:175]
	s_add_i32 m0, s39, 0xe000
	s_nop 0
	global_load_lds_dwordx4 v[214:215], off
	s_waitcnt vmcnt(8)
	s_waitcnt lgkmcnt(0)
	s_barrier
	s_setprio 3
	v_mfma_f32_16x16x128_f8f6f4 v[158:161], v[18:25], v[176:183], v[158:161]
	v_mfma_f32_16x16x128_f8f6f4 v[150:153], v[26:33], v[176:183], v[150:153]
	v_mfma_f32_16x16x128_f8f6f4 v[142:145], v[18:25], v[190:197], v[142:145]
	v_mfma_f32_16x16x128_f8f6f4 v[134:137], v[26:33], v[190:197], v[134:137]
	v_mfma_f32_16x16x128_f8f6f4 v[126:129], v[18:25], v[198:205], v[126:129]
	v_mfma_f32_16x16x128_f8f6f4 v[118:121], v[26:33], v[198:205], v[118:121]
	v_mfma_f32_16x16x128_f8f6f4 v[110:113], v[18:25], v[206:213], v[110:113]
	v_mfma_f32_16x16x128_f8f6f4 v[102:105], v[26:33], v[206:213], v[102:105]
	v_mfma_f32_16x16x128_f8f6f4 v[154:157], v[2:9], v[176:183], v[154:157]
	v_mfma_f32_16x16x128_f8f6f4 v[146:149], v[10:17], v[176:183], v[146:149]
	v_mfma_f32_16x16x128_f8f6f4 v[138:141], v[2:9], v[190:197], v[138:141]
	v_mfma_f32_16x16x128_f8f6f4 v[130:133], v[10:17], v[190:197], v[130:133]
	v_mfma_f32_16x16x128_f8f6f4 v[122:125], v[2:9], v[198:205], v[122:125]
	v_mfma_f32_16x16x128_f8f6f4 v[114:117], v[10:17], v[198:205], v[114:117]
	v_mfma_f32_16x16x128_f8f6f4 v[106:109], v[2:9], v[206:213], v[106:109]
	v_mfma_f32_16x16x128_f8f6f4 v[98:101], v[10:17], v[206:213], v[98:101]
	s_setprio 0
	s_barrier
; #define PG8_STAGE(bufoff, gbase, voff) do { _Pragma("unroll") for (int _i = 0; _i < 2; ++_i) \
;         __builtin_amdgcn_global_load_lds((const unsigned*)((const char*)(gbase) + (voff)[_i]), (PG8_LAS unsigned*)(lds + (bufoff) + ldsw + _i * 8192), 16, 0, 0); } while (0)
; #define PG8_LDA(dst, b, h) do { _Pragma("unroll") for (int m = 0; m < 4; ++m) Frag<F8>::load(dst[m], lds + PG8_SA(b, h) + aoff + m * 2048); } while (0)
; #define PG8_LDB(dst, b, h) do { _Pragma("unroll") for (int n = 0; n < 2; ++n) Frag<F8>::load(dst[n], lds + PG8_SB(b, h) + boff + n * 2048); } while (0)
; #define PG8_MMA(ai, bj, At, Bt) do { __builtin_amdgcn_s_setprio(3); _Pragma("unroll") for (int m = 0; m < 4; ++m) _Pragma("unroll") for (int n = 0; n < 2; ++n) Frag<F8>::mma(acc[ai][bj][m][n], Bt[n], At[m]); \
;         __builtin_amdgcn_s_setprio(0); } while (0)
; #define PG8_WAIT_V(n) asm volatile("s_waitcnt vmcnt(" #n ")" ::: "memory")
; #define PG8_WAIT_L(n) asm volatile("s_waitcnt lgkmcnt(" #n ")" ::: "memory")
; #define PG8_BAR __builtin_amdgcn_s_barrier()
; #define PG8_SCHED __builtin_amdgcn_sched_barrier(0)
; template <class Epi, class Sched, bool ALIGN_EPI = false, bool SP2 = false, bool F8 = false>
; __device__ __forceinline__ void gemm_phase(PG8_LAS unsigned char* lds, const Gemm g, const Sched& S, const Epi& E) {
;     ...
;             PG8_LDA(At, 0, 1); PG8_STAGE(PG8_SB(0, 0), b2, voffB); PG8_STAGE(PG8_SB(0, 1), b2 + hstep, voffB); PG8_STAGE(PG8_SA(0, 0), a2, voffA);
;             PG8_WAIT_V(8); PG8_WAIT_L(0); PG8_BAR; PG8_MMA(1, 0, At, B0); PG8_MMA(1, 1, At, B1); PG8_BAR; PG8_SCHED;
;             PG8_LDB(B0, 1, 0); PG8_LDB(B1, 1, 1); PG8_SCHED; PG8_LDA(At, 1, 0); PG8_STAGE(PG8_SA(0, 1), a2 + hstep, voffA);
;             PG8_WAIT_V(8); PG8_WAIT_L(0); PG8_BAR; PG8_MMA(0, 0, At, B0); PG8_MMA(0, 1, At, B1); PG8_BAR; PG8_SCHED;
	s_add_i32 s0, s74, s52
	v_lshl_add_u64 v[176:177], s[44:45], 0, v[168:169]
	s_mov_b32 m0, s0
	ds_read_b128 v[190:193], v188 offset:16384
	ds_read_b128 v[194:197], v188 offset:17408
	ds_read_b128 v[198:201], v188 offset:18432
	ds_read_b128 v[202:205], v188 offset:19456
	ds_read_b128 v[206:209], v188 offset:20480
	ds_read_b128 v[210:213], v188 offset:21504
	ds_read_b128 v[214:217], v188 offset:22528
	ds_read_b128 v[218:221], v188 offset:23552
	global_load_lds_dwordx4 v[176:177], off
	s_add_i32 m0, s0, 0x2000
	s_add_u32 s4, s44, 0x20000
	v_lshl_add_u64 v[178:179], s[44:45], 0, v[164:165]
	s_addc_u32 s5, s45, 0
	s_add_i32 s0, s75, s52
	global_load_lds_dwordx4 v[178:179], off
	v_lshl_add_u64 v[180:181], s[4:5], 0, v[168:169]
	s_mov_b32 m0, s0
	v_lshl_add_u64 v[182:183], s[46:47], 0, v[166:167]
	global_load_lds_dwordx4 v[180:181], off
	v_lshl_add_u64 v[180:181], s[4:5], 0, v[164:165]
	s_add_i32 m0, s0, 0x2000
	s_nop 0
	global_load_lds_dwordx4 v[180:181], off
	v_lshl_add_u64 v[180:181], s[46:47], 0, v[170:171]
	s_mov_b32 m0, s39
	s_nop 0
	global_load_lds_dwordx4 v[180:181], off
	s_mov_b32 m0, s41
	s_nop 0
	global_load_lds_dwordx4 v[182:183], off
	s_waitcnt vmcnt(8)
	s_waitcnt lgkmcnt(0)
	s_barrier
	s_setprio 3
	v_mfma_f32_16x16x128_f8f6f4 v[94:97], v[18:25], v[190:197], v[94:97]
	v_mfma_f32_16x16x128_f8f6f4 v[86:89], v[26:33], v[190:197], v[86:89]
	v_mfma_f32_16x16x128_f8f6f4 v[78:81], v[18:25], v[198:205], v[78:81]
	v_mfma_f32_16x16x128_f8f6f4 v[70:73], v[26:33], v[198:205], v[70:73]
	v_mfma_f32_16x16x128_f8f6f4 v[62:65], v[18:25], v[206:213], v[62:65]
	v_mfma_f32_16x16x128_f8f6f4 v[54:57], v[26:33], v[206:213], v[54:57]
	v_mfma_f32_16x16x128_f8f6f4 v[46:49], v[18:25], v[214:221], v[46:49]
	v_mfma_f32_16x16x128_f8f6f4 v[38:41], v[26:33], v[214:221], v[38:41]
	v_mfma_f32_16x16x128_f8f6f4 v[90:93], v[2:9], v[190:197], v[90:93]
	v_mfma_f32_16x16x128_f8f6f4 v[82:85], v[10:17], v[190:197], v[82:85]
	v_mfma_f32_16x16x128_f8f6f4 v[74:77], v[2:9], v[198:205], v[74:77]
	v_mfma_f32_16x16x128_f8f6f4 v[66:69], v[10:17], v[198:205], v[66:69]
	v_mfma_f32_16x16x128_f8f6f4 v[58:61], v[2:9], v[206:213], v[58:61]
	v_mfma_f32_16x16x128_f8f6f4 v[50:53], v[10:17], v[206:213], v[50:53]
	v_mfma_f32_16x16x128_f8f6f4 v[42:45], v[2:9], v[214:221], v[42:45]
	v_mfma_f32_16x16x128_f8f6f4 v[34:37], v[10:17], v[214:221], v[34:37]
	s_setprio 0
	s_barrier
	s_add_i32 s0, 0, 0x18000
	s_add_i32 s1, 0, 0x1c000
	v_add_u32_e32 v14, s0, v184
	v_add_u32_e32 v30, s1, v184
	ds_read_b128 v[2:5], v14
	ds_read_b128 v[6:9], v14 offset:1024
	ds_read_b128 v[10:13], v14 offset:2048
	ds_read_b128 v[14:17], v14 offset:3072
	ds_read_b128 v[18:21], v30
	ds_read_b128 v[22:25], v30 offset:1024
	ds_read_b128 v[26:29], v30 offset:2048
	ds_read_b128 v[30:33], v30 offset:3072
	s_add_u32 s4, s46, 0x20000
	s_addc_u32 s5, s47, 0
	s_mov_b32 m0, s58
	v_lshl_add_u64 v[222:223], s[4:5], 0, v[170:171]
	ds_read_b128 v[190:193], v188 offset:32768
	ds_read_b128 v[194:197], v188 offset:33792
	ds_read_b128 v[198:201], v188 offset:34816
	ds_read_b128 v[202:205], v188 offset:35840
	ds_read_b128 v[206:209], v188 offset:36864
	ds_read_b128 v[210:213], v188 offset:37888
	ds_read_b128 v[214:217], v188 offset:38912
	ds_read_b128 v[218:221], v188 offset:39936
	global_load_lds_dwordx4 v[222:223], off
	v_lshl_add_u64 v[222:223], s[4:5], 0, v[166:167]
	s_mov_b32 m0, s59
	s_nop 0
	global_load_lds_dwordx4 v[222:223], off
	s_waitcnt vmcnt(8)
	s_waitcnt lgkmcnt(0)
	s_barrier
; #define PG8_STAGE(bufoff, gbase, voff) do { _Pragma("unroll") for (int _i = 0; _i < 2; ++_i) \
;         __builtin_amdgcn_global_load_lds((const unsigned*)((const char*)(gbase) + (voff)[_i]), (PG8_LAS unsigned*)(lds + (bufoff) + ldsw + _i * 8192), 16, 0, 0); } while (0)
; #define PG8_LDA(dst, b, h) do { _Pragma("unroll") for (int m = 0; m < 4; ++m) Frag<F8>::load(dst[m], lds + PG8_SA(b, h) + aoff + m * 2048); } while (0)
; #define PG8_MMA(ai, bj, At, Bt) do { __builtin_amdgcn_s_setprio(3); _Pragma("unroll") for (int m = 0; m < 4; ++m) _Pragma("unroll") for (int n = 0; n < 2; ++n) Frag<F8>::mma(acc[ai][bj][m][n], Bt[n], At[m]); \
;         __builtin_amdgcn_s_setprio(0); } while (0)
; #define PG8_WAIT_V(n) asm volatile("s_waitcnt vmcnt(" #n ")" ::: "memory")
; #define PG8_WAIT_L(n) asm volatile("s_waitcnt lgkmcnt(" #n ")" ::: "memory")
; #define PG8_BAR __builtin_amdgcn_s_barrier()
; #define PG8_SCHED __builtin_amdgcn_sched_barrier(0)
; template <class Epi, class Sched, bool ALIGN_EPI = false, bool SP2 = false, bool F8 = false>
; __device__ __forceinline__ void gemm_phase(PG8_LAS unsigned char* lds, const Gemm g, const Sched& S, const Epi& E) {
;     ...
;             PG8_LDA(At, 1, 1); PG8_STAGE(PG8_SB(1, 0), b3, voffB); PG8_STAGE(PG8_SB(1, 1), b3 + hstep, voffB); PG8_STAGE(PG8_SA(1, 0), a3, voffA);
;             PG8_WAIT_V(8); PG8_WAIT_L(0); PG8_BAR; PG8_MMA(1, 0, At, B0); PG8_MMA(1, 1, At, B1); PG8_BAR; PG8_SCHED;
	s_setprio 3
	v_mfma_f32_16x16x128_f8f6f4 v[158:161], v[2:9], v[190:197], v[158:161]
	v_mfma_f32_16x16x128_f8f6f4 v[150:153], v[10:17], v[190:197], v[150:153]
	v_mfma_f32_16x16x128_f8f6f4 v[142:145], v[2:9], v[198:205], v[142:145]
	v_mfma_f32_16x16x128_f8f6f4 v[134:137], v[10:17], v[198:205], v[134:137]
	v_mfma_f32_16x16x128_f8f6f4 v[126:129], v[2:9], v[206:213], v[126:129]
	v_mfma_f32_16x16x128_f8f6f4 v[118:121], v[10:17], v[206:213], v[118:121]
	v_mfma_f32_16x16x128_f8f6f4 v[110:113], v[2:9], v[214:221], v[110:113]
	v_mfma_f32_16x16x128_f8f6f4 v[102:105], v[10:17], v[214:221], v[102:105]
	v_mfma_f32_16x16x128_f8f6f4 v[154:157], v[18:25], v[190:197], v[154:157]
	v_mfma_f32_16x16x128_f8f6f4 v[146:149], v[26:33], v[190:197], v[146:149]
	v_mfma_f32_16x16x128_f8f6f4 v[138:141], v[18:25], v[198:205], v[138:141]
	v_mfma_f32_16x16x128_f8f6f4 v[130:133], v[26:33], v[198:205], v[130:133]
	v_mfma_f32_16x16x128_f8f6f4 v[122:125], v[18:25], v[206:213], v[122:125]
	v_mfma_f32_16x16x128_f8f6f4 v[114:117], v[26:33], v[206:213], v[114:117]
	v_mfma_f32_16x16x128_f8f6f4 v[106:109], v[18:25], v[214:221], v[106:109]
	v_mfma_f32_16x16x128_f8f6f4 v[98:101], v[26:33], v[214:221], v[98:101]
	s_setprio 0
	s_barrier
	s_add_i32 s0, s0, s52
	v_lshl_add_u64 v[176:177], v[176:177], 0, s[14:15]
	s_mov_b32 m0, s0
	ds_read_b128 v[190:193], v188 offset:49152
	ds_read_b128 v[194:197], v188 offset:50176
	ds_read_b128 v[198:201], v188 offset:51200
	ds_read_b128 v[202:205], v188 offset:52224
	ds_read_b128 v[206:209], v188 offset:53248
	ds_read_b128 v[210:213], v188 offset:54272
	ds_read_b128 v[214:217], v188 offset:55296
	ds_read_b128 v[218:221], v188 offset:56320
	global_load_lds_dwordx4 v[176:177], off
	s_add_i32 m0, s0, 0x2000
	s_add_u32 s4, s44, 0x20080
	v_lshl_add_u64 v[176:177], v[178:179], 0, s[14:15]
	s_addc_u32 s5, s45, 0
	s_add_i32 s0, s1, s52
	global_load_lds_dwordx4 v[176:177], off
	v_lshl_add_u64 v[176:177], s[4:5], 0, v[168:169]
	s_mov_b32 m0, s0
	s_nop 0
	global_load_lds_dwordx4 v[176:177], off
	v_lshl_add_u64 v[176:177], s[4:5], 0, v[164:165]
	s_add_i32 m0, s0, 0x2000
	s_nop 0
	global_load_lds_dwordx4 v[176:177], off
	v_lshl_add_u64 v[176:177], v[180:181], 0, s[14:15]
	s_mov_b32 m0, s60
	s_nop 0
	global_load_lds_dwordx4 v[176:177], off
	v_lshl_add_u64 v[176:177], v[182:183], 0, s[14:15]
	s_mov_b32 m0, s61
	s_nop 0
	global_load_lds_dwordx4 v[176:177], off
	s_waitcnt vmcnt(8)
	s_waitcnt lgkmcnt(0)
	s_barrier
	s_setprio 3
	v_mfma_f32_16x16x128_f8f6f4 v[94:97], v[2:9], v[190:197], v[94:97]
	v_mfma_f32_16x16x128_f8f6f4 v[86:89], v[10:17], v[190:197], v[86:89]
	v_mfma_f32_16x16x128_f8f6f4 v[78:81], v[2:9], v[198:205], v[78:81]
	v_mfma_f32_16x16x128_f8f6f4 v[70:73], v[10:17], v[198:205], v[70:73]
	v_mfma_f32_16x16x128_f8f6f4 v[62:65], v[2:9], v[206:213], v[62:65]
	v_mfma_f32_16x16x128_f8f6f4 v[54:57], v[10:17], v[206:213], v[54:57]
	v_mfma_f32_16x16x128_f8f6f4 v[46:49], v[2:9], v[214:221], v[46:49]
	v_mfma_f32_16x16x128_f8f6f4 v[38:41], v[10:17], v[214:221], v[38:41]
	v_mfma_f32_16x16x128_f8f6f4 v[90:93], v[18:25], v[190:197], v[90:93]
	v_mfma_f32_16x16x128_f8f6f4 v[82:85], v[26:33], v[190:197], v[82:85]
	v_mfma_f32_16x16x128_f8f6f4 v[74:77], v[18:25], v[198:205], v[74:77]
	v_mfma_f32_16x16x128_f8f6f4 v[66:69], v[26:33], v[198:205], v[66:69]
	v_mfma_f32_16x16x128_f8f6f4 v[58:61], v[18:25], v[206:213], v[58:61]
	v_mfma_f32_16x16x128_f8f6f4 v[50:53], v[26:33], v[206:213], v[50:53]
	v_mfma_f32_16x16x128_f8f6f4 v[42:45], v[18:25], v[214:221], v[42:45]
	v_mfma_f32_16x16x128_f8f6f4 v[34:37], v[26:33], v[214:221], v[34:37]
	s_setprio 0
	s_barrier
	s_add_i32 s81, s81, 2
	s_add_u32 s42, s42, 0x100
	s_addc_u32 s43, s43, 0
	s_add_u32 s79, s79, 0x100
	s_addc_u32 s80, s80, 0
	s_cmp_gt_u32 s81, 5
	s_cbranch_scc0 .LBB0_1310

; #define PG8_STAGE(bufoff, gbase, voff) do { _Pragma("unroll") for (int _i = 0; _i < 2; ++_i) \
;         __builtin_amdgcn_global_load_lds((const unsigned*)((const char*)(gbase) + (voff)[_i]), (PG8_LAS unsigned*)(lds + (bufoff) + ldsw + _i * 8192), 16, 0, 0); } while (0)
; #define PG8_LDA(dst, b, h) do { _Pragma("unroll") for (int m = 0; m < 4; ++m) Frag<F8>::load(dst[m], lds + PG8_SA(b, h) + aoff + m * 2048); } while (0)
; #define PG8_LDB(dst, b, h) do { _Pragma("unroll") for (int n = 0; n < 2; ++n) Frag<F8>::load(dst[n], lds + PG8_SB(b, h) + boff + n * 2048); } while (0)
; #define PG8_WAIT_V(n) asm volatile("s_waitcnt vmcnt(" #n ")" ::: "memory")
; #define PG8_WAIT_L(n) asm volatile("s_waitcnt lgkmcnt(" #n ")" ::: "memory")
; #define PG8_BAR __builtin_amdgcn_s_barrier()
; template <class Epi, class Sched, bool ALIGN_EPI = false, bool SP2 = false, bool F8 = false>
; __device__ __forceinline__ void gemm_phase(PG8_LAS unsigned char* lds, const Gemm g, const Sched& S, const Epi& E) {
;     ...
;         const char* nA = has_next ? (const char*)g.A + (size_t)nxt.pm * tstep + nxt.ko : cA; const char* nB = has_next ? (const char*)g.Bt + (size_t)nxt.pn * tstep + nxt.ko : cB;
;         for (int t = 0; t < nt; t += 2) {
;             const bool last = (t == nt - 2);
;             const char* a1 = cA + (size_t)(t + 1) * kstep;
;             const char* a2 = last ? nA : cA + (size_t)(t + 2) * kstep; const char* b2 = last ? nB : cB + (size_t)(t + 2) * kstep;
;             const char* a3 = a2 + kstep; const char* b3 = b2 + kstep;
;             if (last && has_next) S.a_ready(nxt);
;             if constexpr (SP2) {
;             PG8_LDB(B0, 0, 0); PG8_LDB(B1, 0, 1); PG8_SCHED; PG8_LDA(At, 0, 0); PG8_STAGE(PG8_SA(1, 1), a1 + hstep, voffA);
;             PG8_WAIT_V(8); PG8_WAIT_L(0); PG8_BAR; PG8_MMA(0, 0, At, B0); PG8_MMA(0, 1, At, B1); PG8_BAR; PG8_SCHED;
;             PG8_LDA(At, 0, 1); PG8_STAGE(PG8_SB(0, 0), b2, voffB); PG8_STAGE(PG8_SB(0, 1), b2 + hstep, voffB); PG8_STAGE(PG8_SA(0, 0), a2, voffA);
;             PG8_WAIT_V(8); PG8_WAIT_L(0); PG8_BAR; PG8_MMA(1, 0, At, B0); PG8_MMA(1, 1, At, B1); PG8_BAR; PG8_SCHED;
;             PG8_LDB(B0, 1, 0); PG8_LDB(B1, 1, 1); PG8_SCHED; PG8_LDA(At, 1, 0); PG8_STAGE(PG8_SA(0, 1), a2 + hstep, voffA);
;             PG8_WAIT_V(8); PG8_WAIT_L(0); PG8_BAR; PG8_MMA(0, 0, At, B0); PG8_MMA(0, 1, At, B1); PG8_BAR; PG8_SCHED;
.LBB0_1391:
	v_lshl_add_u64 v[180:181], v[2:3], 0, s[24:25]
	s_mov_b32 s76, -2
	ds_read_b128 v[18:21], v192
	ds_read_b128 v[22:25], v192 offset:1024
	ds_read_b128 v[26:29], v192 offset:2048
	ds_read_b128 v[30:33], v192 offset:3072
	ds_read_b128 v[2:5], v193
	ds_read_b128 v[6:9], v193 offset:1024
	ds_read_b128 v[10:13], v193 offset:2048
	ds_read_b128 v[14:17], v193 offset:3072
	s_add_u32 s30, s36, 0x100
	s_addc_u32 s31, s37, 0
	s_cmp_eq_u32 s76, 24
	s_cselect_b64 vcc, -1, 0
	s_cselect_b32 s39, s27, s31
	s_cselect_b32 s38, s26, s30
	v_cndmask_b32_e32 v183, v181, v179, vcc
	v_cndmask_b32_e32 v182, v180, v178, vcc
	s_mov_b32 m0, s56
	v_lshl_add_u64 v[224:225], s[36:37], 0, v[174:175]
	ds_read_b128 v[184:187], v194
	ds_read_b128 v[188:191], v194 offset:1024
	ds_read_b128 v[200:203], v194 offset:2048
	ds_read_b128 v[204:207], v194 offset:3072
	ds_read_b128 v[208:211], v194 offset:4096
	ds_read_b128 v[212:215], v194 offset:5120
	ds_read_b128 v[216:219], v194 offset:6144
	ds_read_b128 v[220:223], v194 offset:7168
	global_load_lds_dwordx4 v[224:225], off
	v_lshl_add_u64 v[224:225], s[36:37], 0, v[176:177]
	s_mov_b32 m0, s57
	s_nop 0
	global_load_lds_dwordx4 v[224:225], off
	s_waitcnt vmcnt(8)
	s_waitcnt lgkmcnt(0)
	s_barrier
	s_setprio 3
	v_mfma_f32_16x16x128_f8f6f4 v[158:161], v[18:25], v[184:191], 0
	v_mfma_f32_16x16x128_f8f6f4 v[154:157], v[26:33], v[184:191], 0
	v_mfma_f32_16x16x128_f8f6f4 v[142:145], v[18:25], v[200:207], 0
	v_mfma_f32_16x16x128_f8f6f4 v[138:141], v[26:33], v[200:207], 0
	v_mfma_f32_16x16x128_f8f6f4 v[126:129], v[18:25], v[208:215], 0
	v_mfma_f32_16x16x128_f8f6f4 v[122:125], v[26:33], v[208:215], 0
	v_mfma_f32_16x16x128_f8f6f4 v[110:113], v[18:25], v[216:223], 0
	v_mfma_f32_16x16x128_f8f6f4 v[106:109], v[26:33], v[216:223], 0
	v_mfma_f32_16x16x128_f8f6f4 v[150:153], v[2:9], v[184:191], 0
	v_mfma_f32_16x16x128_f8f6f4 v[146:149], v[10:17], v[184:191], 0
	v_mfma_f32_16x16x128_f8f6f4 v[134:137], v[2:9], v[200:207], 0
	v_mfma_f32_16x16x128_f8f6f4 v[130:133], v[10:17], v[200:207], 0
	v_mfma_f32_16x16x128_f8f6f4 v[118:121], v[2:9], v[208:215], 0
	v_mfma_f32_16x16x128_f8f6f4 v[114:117], v[10:17], v[208:215], 0
	v_mfma_f32_16x16x128_f8f6f4 v[102:105], v[2:9], v[216:223], 0
	v_mfma_f32_16x16x128_f8f6f4 v[98:101], v[10:17], v[216:223], 0
	s_setprio 0
	s_barrier
	s_mov_b32 m0, s58
	v_lshl_add_u64 v[184:185], v[182:183], 0, v[166:167]
	ds_read_b128 v[200:203], v194 offset:16384
	ds_read_b128 v[204:207], v194 offset:17408
	ds_read_b128 v[208:211], v194 offset:18432
	ds_read_b128 v[212:215], v194 offset:19456
	ds_read_b128 v[216:219], v194 offset:20480
	ds_read_b128 v[220:223], v194 offset:21504
	ds_read_b128 v[224:227], v194 offset:22528
	ds_read_b128 v[228:231], v194 offset:23552
	global_load_lds_dwordx4 v[184:185], off
	v_lshl_add_u64 v[186:187], v[182:183], 0, v[170:171]
	s_mov_b32 m0, s59
	v_lshl_add_u64 v[188:189], v[182:183], 0, s[10:11]
	global_load_lds_dwordx4 v[186:187], off
	v_lshl_add_u64 v[190:191], v[188:189], 0, v[166:167]
	s_mov_b32 m0, s60
	v_lshl_add_u64 v[188:189], v[188:189], 0, v[170:171]
	global_load_lds_dwordx4 v[190:191], off
	s_mov_b32 m0, s61
	v_lshl_add_u64 v[190:191], s[38:39], 0, v[168:169]
	global_load_lds_dwordx4 v[188:189], off
	v_lshl_add_u64 v[188:189], s[38:39], 0, v[164:165]
	s_mov_b32 m0, s45
	s_nop 0
	global_load_lds_dwordx4 v[188:189], off
	s_mov_b32 m0, s46
	s_nop 0
	global_load_lds_dwordx4 v[190:191], off
	s_waitcnt vmcnt(8)
	s_waitcnt lgkmcnt(0)
	s_barrier
	s_setprio 3
	v_mfma_f32_16x16x128_f8f6f4 v[94:97], v[18:25], v[200:207], 0
	v_mfma_f32_16x16x128_f8f6f4 v[90:93], v[26:33], v[200:207], 0
	v_mfma_f32_16x16x128_f8f6f4 v[78:81], v[18:25], v[208:215], 0
	v_mfma_f32_16x16x128_f8f6f4 v[74:77], v[26:33], v[208:215], 0
	v_mfma_f32_16x16x128_f8f6f4 v[62:65], v[18:25], v[216:223], 0
	v_mfma_f32_16x16x128_f8f6f4 v[58:61], v[26:33], v[216:223], 0
	v_mfma_f32_16x16x128_f8f6f4 v[46:49], v[18:25], v[224:231], 0
	v_mfma_f32_16x16x128_f8f6f4 v[42:45], v[26:33], v[224:231], 0
	v_mfma_f32_16x16x128_f8f6f4 v[86:89], v[2:9], v[200:207], 0
	v_mfma_f32_16x16x128_f8f6f4 v[82:85], v[10:17], v[200:207], 0
	v_mfma_f32_16x16x128_f8f6f4 v[70:73], v[2:9], v[208:215], 0
	v_mfma_f32_16x16x128_f8f6f4 v[66:69], v[10:17], v[208:215], 0
	v_mfma_f32_16x16x128_f8f6f4 v[54:57], v[2:9], v[216:223], 0
	v_mfma_f32_16x16x128_f8f6f4 v[50:53], v[10:17], v[216:223], 0
	v_mfma_f32_16x16x128_f8f6f4 v[38:41], v[2:9], v[224:231], 0
	v_mfma_f32_16x16x128_f8f6f4 v[34:37], v[10:17], v[224:231], 0
	s_setprio 0
	s_barrier
	ds_read_b128 v[2:5], v196
	ds_read_b128 v[6:9], v196 offset:1024
	ds_read_b128 v[10:13], v196 offset:2048
	ds_read_b128 v[14:17], v196 offset:3072
	ds_read_b128 v[18:21], v197
	ds_read_b128 v[22:25], v197 offset:1024
	ds_read_b128 v[26:29], v197 offset:2048
	ds_read_b128 v[30:33], v197 offset:3072
	s_add_u32 s4, s38, 0x70000
	s_addc_u32 s5, s39, 0
	s_mov_b32 m0, s47
	v_lshl_add_u64 v[232:233], s[4:5], 0, v[164:165]
	ds_read_b128 v[200:203], v194 offset:32768
	ds_read_b128 v[204:207], v194 offset:33792
	ds_read_b128 v[208:211], v194 offset:34816
	ds_read_b128 v[212:215], v194 offset:35840
	ds_read_b128 v[216:219], v194 offset:36864
	ds_read_b128 v[220:223], v194 offset:37888
	ds_read_b128 v[224:227], v194 offset:38912
	ds_read_b128 v[228:231], v194 offset:39936
	global_load_lds_dwordx4 v[232:233], off
	v_lshl_add_u64 v[232:233], s[4:5], 0, v[168:169]
	s_mov_b32 m0, s48
	s_nop 0
	global_load_lds_dwordx4 v[232:233], off
	s_waitcnt vmcnt(8)
	s_waitcnt lgkmcnt(0)
	s_barrier
; #define PG8_STAGE(bufoff, gbase, voff) do { _Pragma("unroll") for (int _i = 0; _i < 2; ++_i) \
;         __builtin_amdgcn_global_load_lds((const unsigned*)((const char*)(gbase) + (voff)[_i]), (PG8_LAS unsigned*)(lds + (bufoff) + ldsw + _i * 8192), 16, 0, 0); } while (0)
; #define PG8_LDA(dst, b, h) do { _Pragma("unroll") for (int m = 0; m < 4; ++m) Frag<F8>::load(dst[m], lds + PG8_SA(b, h) + aoff + m * 2048); } while (0)
; #define PG8_LDB(dst, b, h) do { _Pragma("unroll") for (int n = 0; n < 2; ++n) Frag<F8>::load(dst[n], lds + PG8_SB(b, h) + boff + n * 2048); } while (0)
; #define PG8_MMA(ai, bj, At, Bt) do { __builtin_amdgcn_s_setprio(3); _Pragma("unroll") for (int m = 0; m < 4; ++m) _Pragma("unroll") for (int n = 0; n < 2; ++n) Frag<F8>::mma(acc[ai][bj][m][n], Bt[n], At[m]); \
;         __builtin_amdgcn_s_setprio(0); } while (0)
; #define PG8_WAIT_V(n) asm volatile("s_waitcnt vmcnt(" #n ")" ::: "memory")
; #define PG8_WAIT_L(n) asm volatile("s_waitcnt lgkmcnt(" #n ")" ::: "memory")
; #define PG8_BAR __builtin_amdgcn_s_barrier()
; #define PG8_SCHED __builtin_amdgcn_sched_barrier(0)
; template <class Epi, class Sched, bool ALIGN_EPI = false, bool SP2 = false, bool F8 = false>
; __device__ __forceinline__ void gemm_phase(PG8_LAS unsigned char* lds, const Gemm g, const Sched& S, const Epi& E) {
;     ...
;             PG8_LDB(B0, 0, 0); PG8_LDB(B1, 0, 1); PG8_SCHED; PG8_LDA(At, 0, 0); PG8_STAGE(PG8_SA(1, 1), a1 + hstep, voffA);
;             PG8_WAIT_V(8); PG8_WAIT_L(0); PG8_BAR; PG8_MMA(0, 0, At, B0); PG8_MMA(0, 1, At, B1); PG8_BAR; PG8_SCHED;
;     ...
;             PG8_LDA(At, 1, 1); PG8_STAGE(PG8_SB(1, 0), b3, voffB); PG8_STAGE(PG8_SB(1, 1), b3 + hstep, voffB); PG8_STAGE(PG8_SA(1, 0), a3, voffA);
;             PG8_WAIT_V(8); PG8_WAIT_L(0); PG8_BAR; PG8_MMA(1, 0, At, B0); PG8_MMA(1, 1, At, B1); PG8_BAR; PG8_SCHED;
	s_setprio 3
	v_mfma_f32_16x16x128_f8f6f4 v[158:161], v[2:9], v[200:207], v[158:161]
	v_mfma_f32_16x16x128_f8f6f4 v[154:157], v[10:17], v[200:207], v[154:157]
	v_mfma_f32_16x16x128_f8f6f4 v[142:145], v[2:9], v[208:215], v[142:145]
	v_mfma_f32_16x16x128_f8f6f4 v[138:141], v[10:17], v[208:215], v[138:141]
	v_mfma_f32_16x16x128_f8f6f4 v[126:129], v[2:9], v[216:223], v[126:129]
	v_mfma_f32_16x16x128_f8f6f4 v[122:125], v[10:17], v[216:223], v[122:125]
	v_mfma_f32_16x16x128_f8f6f4 v[110:113], v[2:9], v[224:231], v[110:113]
	v_mfma_f32_16x16x128_f8f6f4 v[106:109], v[10:17], v[224:231], v[106:109]
	v_mfma_f32_16x16x128_f8f6f4 v[150:153], v[18:25], v[200:207], v[150:153]
	v_mfma_f32_16x16x128_f8f6f4 v[146:149], v[26:33], v[200:207], v[146:149]
	v_mfma_f32_16x16x128_f8f6f4 v[134:137], v[18:25], v[208:215], v[134:137]
	v_mfma_f32_16x16x128_f8f6f4 v[130:133], v[26:33], v[208:215], v[130:133]
	v_mfma_f32_16x16x128_f8f6f4 v[118:121], v[18:25], v[216:223], v[118:121]
	v_mfma_f32_16x16x128_f8f6f4 v[114:117], v[26:33], v[216:223], v[114:117]
	v_mfma_f32_16x16x128_f8f6f4 v[102:105], v[18:25], v[224:231], v[102:105]
	v_mfma_f32_16x16x128_f8f6f4 v[98:101], v[26:33], v[224:231], v[98:101]
	s_setprio 0
	s_barrier
	s_mov_b32 m0, s67
	v_lshl_add_u64 v[184:185], v[184:185], 0, s[18:19]
	ds_read_b128 v[200:203], v194 offset:49152
	ds_read_b128 v[204:207], v194 offset:50176
	ds_read_b128 v[208:211], v194 offset:51200
	ds_read_b128 v[212:215], v194 offset:52224
	ds_read_b128 v[216:219], v194 offset:53248
	ds_read_b128 v[220:223], v194 offset:54272
	ds_read_b128 v[224:227], v194 offset:55296
	ds_read_b128 v[228:231], v194 offset:56320
	global_load_lds_dwordx4 v[184:185], off
	v_lshl_add_u64 v[184:185], v[186:187], 0, s[18:19]
	s_mov_b32 m0, s70
	v_lshl_add_u64 v[182:183], v[182:183], 0, s[20:21]
	global_load_lds_dwordx4 v[184:185], off
	v_lshl_add_u64 v[184:185], v[182:183], 0, v[166:167]
	s_mov_b32 m0, s71
	v_lshl_add_u64 v[182:183], v[182:183], 0, v[170:171]
	global_load_lds_dwordx4 v[184:185], off
	s_mov_b32 m0, s72
	s_nop 0
	global_load_lds_dwordx4 v[182:183], off
	v_lshl_add_u64 v[182:183], v[188:189], 0, s[18:19]
	s_mov_b32 m0, s49
	s_nop 0
	global_load_lds_dwordx4 v[182:183], off
	v_lshl_add_u64 v[182:183], v[190:191], 0, s[18:19]
	s_mov_b32 m0, s50
	s_nop 0
	global_load_lds_dwordx4 v[182:183], off
	s_waitcnt vmcnt(8)
	s_waitcnt lgkmcnt(0)
	s_barrier
	s_setprio 3
	v_mfma_f32_16x16x128_f8f6f4 v[94:97], v[2:9], v[200:207], v[94:97]
	v_mfma_f32_16x16x128_f8f6f4 v[90:93], v[10:17], v[200:207], v[90:93]
	v_mfma_f32_16x16x128_f8f6f4 v[78:81], v[2:9], v[208:215], v[78:81]
	v_mfma_f32_16x16x128_f8f6f4 v[74:77], v[10:17], v[208:215], v[74:77]
	v_mfma_f32_16x16x128_f8f6f4 v[62:65], v[2:9], v[216:223], v[62:65]
	v_mfma_f32_16x16x128_f8f6f4 v[58:61], v[10:17], v[216:223], v[58:61]
	v_mfma_f32_16x16x128_f8f6f4 v[46:49], v[2:9], v[224:231], v[46:49]
	v_mfma_f32_16x16x128_f8f6f4 v[42:45], v[10:17], v[224:231], v[42:45]
	v_mfma_f32_16x16x128_f8f6f4 v[86:89], v[18:25], v[200:207], v[86:89]
	v_mfma_f32_16x16x128_f8f6f4 v[82:85], v[26:33], v[200:207], v[82:85]
	v_mfma_f32_16x16x128_f8f6f4 v[70:73], v[18:25], v[208:215], v[70:73]
	v_mfma_f32_16x16x128_f8f6f4 v[66:69], v[26:33], v[208:215], v[66:69]
	v_mfma_f32_16x16x128_f8f6f4 v[54:57], v[18:25], v[216:223], v[54:57]
	v_mfma_f32_16x16x128_f8f6f4 v[50:53], v[26:33], v[216:223], v[50:53]
	v_mfma_f32_16x16x128_f8f6f4 v[38:41], v[18:25], v[224:231], v[38:41]
	v_mfma_f32_16x16x128_f8f6f4 v[34:37], v[26:33], v[224:231], v[34:37]
	s_setprio 0
	s_barrier
	s_add_i32 s76, s76, 2
	v_lshl_add_u64 v[180:181], v[180:181], 0, s[24:25]
	s_cmp_gt_u32 s76, 25
	s_mov_b64 s[36:37], s[30:31]
	s_cbranch_scc1 .Lpeel_exit_4
.LBB0_1392:
	ds_read_b128 v[18:21], v192
	ds_read_b128 v[22:25], v192 offset:1024
	ds_read_b128 v[26:29], v192 offset:2048
	ds_read_b128 v[30:33], v192 offset:3072
	ds_read_b128 v[2:5], v193
	ds_read_b128 v[6:9], v193 offset:1024
	ds_read_b128 v[10:13], v193 offset:2048
	ds_read_b128 v[14:17], v193 offset:3072
	s_add_u32 s30, s36, 0x100
	s_addc_u32 s31, s37, 0
	s_cmp_eq_u32 s76, 24
	s_cselect_b64 vcc, -1, 0
	s_cselect_b32 s39, s27, s31
	s_cselect_b32 s38, s26, s30
	v_cndmask_b32_e32 v183, v181, v179, vcc
	v_cndmask_b32_e32 v182, v180, v178, vcc
	s_mov_b32 m0, s56
	v_lshl_add_u64 v[224:225], s[36:37], 0, v[174:175]
	ds_read_b128 v[184:187], v194
	ds_read_b128 v[188:191], v194 offset:1024
	ds_read_b128 v[200:203], v194 offset:2048
	ds_read_b128 v[204:207], v194 offset:3072
	ds_read_b128 v[208:211], v194 offset:4096
	ds_read_b128 v[212:215], v194 offset:5120
	ds_read_b128 v[216:219], v194 offset:6144
	ds_read_b128 v[220:223], v194 offset:7168
	global_load_lds_dwordx4 v[224:225], off
	v_lshl_add_u64 v[224:225], s[36:37], 0, v[176:177]
	s_mov_b32 m0, s57
	s_nop 0
	global_load_lds_dwordx4 v[224:225], off
	s_waitcnt vmcnt(8)
	s_waitcnt lgkmcnt(0)
	s_barrier
	s_setprio 3
	v_mfma_f32_16x16x128_f8f6f4 v[158:161], v[18:25], v[184:191], v[158:161]
	v_mfma_f32_16x16x128_f8f6f4 v[154:157], v[26:33], v[184:191], v[154:157]
	v_mfma_f32_16x16x128_f8f6f4 v[142:145], v[18:25], v[200:207], v[142:145]
	v_mfma_f32_16x16x128_f8f6f4 v[138:141], v[26:33], v[200:207], v[138:141]
	v_mfma_f32_16x16x128_f8f6f4 v[126:129], v[18:25], v[208:215], v[126:129]
	v_mfma_f32_16x16x128_f8f6f4 v[122:125], v[26:33], v[208:215], v[122:125]
	v_mfma_f32_16x16x128_f8f6f4 v[110:113], v[18:25], v[216:223], v[110:113]
	v_mfma_f32_16x16x128_f8f6f4 v[106:109], v[26:33], v[216:223], v[106:109]
	v_mfma_f32_16x16x128_f8f6f4 v[150:153], v[2:9], v[184:191], v[150:153]
	v_mfma_f32_16x16x128_f8f6f4 v[146:149], v[10:17], v[184:191], v[146:149]
	v_mfma_f32_16x16x128_f8f6f4 v[134:137], v[2:9], v[200:207], v[134:137]
	v_mfma_f32_16x16x128_f8f6f4 v[130:133], v[10:17], v[200:207], v[130:133]
	v_mfma_f32_16x16x128_f8f6f4 v[118:121], v[2:9], v[208:215], v[118:121]
	v_mfma_f32_16x16x128_f8f6f4 v[114:117], v[10:17], v[208:215], v[114:117]
	v_mfma_f32_16x16x128_f8f6f4 v[102:105], v[2:9], v[216:223], v[102:105]
	v_mfma_f32_16x16x128_f8f6f4 v[98:101], v[10:17], v[216:223], v[98:101]
	s_setprio 0
	s_barrier
; #define PG8_STAGE(bufoff, gbase, voff) do { _Pragma("unroll") for (int _i = 0; _i < 2; ++_i) \
;         __builtin_amdgcn_global_load_lds((const unsigned*)((const char*)(gbase) + (voff)[_i]), (PG8_LAS unsigned*)(lds + (bufoff) + ldsw + _i * 8192), 16, 0, 0); } while (0)
; #define PG8_LDA(dst, b, h) do { _Pragma("unroll") for (int m = 0; m < 4; ++m) Frag<F8>::load(dst[m], lds + PG8_SA(b, h) + aoff + m * 2048); } while (0)
; #define PG8_LDB(dst, b, h) do { _Pragma("unroll") for (int n = 0; n < 2; ++n) Frag<F8>::load(dst[n], lds + PG8_SB(b, h) + boff + n * 2048); } while (0)
; #define PG8_WAIT_V(n) asm volatile("s_waitcnt vmcnt(" #n ")" ::: "memory")
; #define PG8_BAR __builtin_amdgcn_s_barrier()
; template <class Epi, class Sched, bool ALIGN_EPI = false, bool SP2 = false, bool F8 = false>
; __device__ __forceinline__ void gemm_phase(PG8_LAS unsigned char* lds, const Gemm g, const Sched& S, const Epi& E) {
;     ...
;         for (int t = 0; t < nt; t += 2) {
;             const bool last = (t == nt - 2);
;             const char* a1 = cA + (size_t)(t + 1) * kstep;
;             const char* a2 = last ? nA : cA + (size_t)(t + 2) * kstep; const char* b2 = last ? nB : cB + (size_t)(t + 2) * kstep;
;             const char* a3 = a2 + kstep; const char* b3 = b2 + kstep;
;             if (last && has_next) S.a_ready(nxt);
;             if constexpr (SP2) {
;             PG8_LDB(B0, 0, 0); PG8_LDB(B1, 0, 1); PG8_SCHED; PG8_LDA(At, 0, 0); PG8_STAGE(PG8_SA(1, 1), a1 + hstep, voffA);
;             PG8_WAIT_V(8); PG8_WAIT_L(0); PG8_BAR; PG8_MMA(0, 0, At, B0); PG8_MMA(0, 1, At, B1); PG8_BAR; PG8_SCHED;
;             PG8_LDA(At, 0, 1); PG8_STAGE(PG8_SB(0, 0), b2, voffB); PG8_STAGE(PG8_SB(0, 1), b2 + hstep, voffB); PG8_STAGE(PG8_SA(0, 0), a2, voffA);
;             PG8_WAIT_V(8); PG8_WAIT_L(0); PG8_BAR; PG8_MMA(1, 0, At, B0); PG8_MMA(1, 1, At, B1); PG8_BAR; PG8_SCHED;
;             PG8_LDB(B0, 1, 0); PG8_LDB(B1, 1, 1); PG8_SCHED; PG8_LDA(At, 1, 0); PG8_STAGE(PG8_SA(0, 1), a2 + hstep, voffA);
;             PG8_WAIT_V(8); PG8_WAIT_L(0); PG8_BAR; PG8_MMA(0, 0, At, B0); PG8_MMA(0, 1, At, B1); PG8_BAR; PG8_SCHED;
;             PG8_LDA(At, 1, 1); PG8_STAGE(PG8_SB(1, 0), b3, voffB); PG8_STAGE(PG8_SB(1, 1), b3 + hstep, voffB); PG8_STAGE(PG8_SA(1, 0), a3, voffA);
;             PG8_WAIT_V(8); PG8_WAIT_L(0); PG8_BAR; PG8_MMA(1, 0, At, B0); PG8_MMA(1, 1, At, B1); PG8_BAR; PG8_SCHED;
	s_mov_b32 m0, s58
	v_lshl_add_u64 v[184:185], v[182:183], 0, v[166:167]
	ds_read_b128 v[200:203], v194 offset:16384
	ds_read_b128 v[204:207], v194 offset:17408
	ds_read_b128 v[208:211], v194 offset:18432
	ds_read_b128 v[212:215], v194 offset:19456
	ds_read_b128 v[216:219], v194 offset:20480
	ds_read_b128 v[220:223], v194 offset:21504
	ds_read_b128 v[224:227], v194 offset:22528
	ds_read_b128 v[228:231], v194 offset:23552
	global_load_lds_dwordx4 v[184:185], off
	v_lshl_add_u64 v[186:187], v[182:183], 0, v[170:171]
	s_mov_b32 m0, s59
	v_lshl_add_u64 v[188:189], v[182:183], 0, s[10:11]
	global_load_lds_dwordx4 v[186:187], off
	v_lshl_add_u64 v[190:191], v[188:189], 0, v[166:167]
	s_mov_b32 m0, s60
	v_lshl_add_u64 v[188:189], v[188:189], 0, v[170:171]
	global_load_lds_dwordx4 v[190:191], off
	s_mov_b32 m0, s61
	v_lshl_add_u64 v[190:191], s[38:39], 0, v[168:169]
	global_load_lds_dwordx4 v[188:189], off
	v_lshl_add_u64 v[188:189], s[38:39], 0, v[164:165]
	s_mov_b32 m0, s45
	s_nop 0
	global_load_lds_dwordx4 v[188:189], off
	s_mov_b32 m0, s46
	s_nop 0
	global_load_lds_dwordx4 v[190:191], off
	s_waitcnt vmcnt(8)
	s_waitcnt lgkmcnt(0)
	s_barrier
	s_setprio 3
	v_mfma_f32_16x16x128_f8f6f4 v[94:97], v[18:25], v[200:207], v[94:97]
	v_mfma_f32_16x16x128_f8f6f4 v[90:93], v[26:33], v[200:207], v[90:93]
	v_mfma_f32_16x16x128_f8f6f4 v[78:81], v[18:25], v[208:215], v[78:81]
	v_mfma_f32_16x16x128_f8f6f4 v[74:77], v[26:33], v[208:215], v[74:77]
	v_mfma_f32_16x16x128_f8f6f4 v[62:65], v[18:25], v[216:223], v[62:65]
	v_mfma_f32_16x16x128_f8f6f4 v[58:61], v[26:33], v[216:223], v[58:61]
	v_mfma_f32_16x16x128_f8f6f4 v[46:49], v[18:25], v[224:231], v[46:49]
	v_mfma_f32_16x16x128_f8f6f4 v[42:45], v[26:33], v[224:231], v[42:45]
	v_mfma_f32_16x16x128_f8f6f4 v[86:89], v[2:9], v[200:207], v[86:89]
	v_mfma_f32_16x16x128_f8f6f4 v[82:85], v[10:17], v[200:207], v[82:85]
	v_mfma_f32_16x16x128_f8f6f4 v[70:73], v[2:9], v[208:215], v[70:73]
	v_mfma_f32_16x16x128_f8f6f4 v[66:69], v[10:17], v[208:215], v[66:69]
	v_mfma_f32_16x16x128_f8f6f4 v[54:57], v[2:9], v[216:223], v[54:57]
	v_mfma_f32_16x16x128_f8f6f4 v[50:53], v[10:17], v[216:223], v[50:53]
	v_mfma_f32_16x16x128_f8f6f4 v[38:41], v[2:9], v[224:231], v[38:41]
	v_mfma_f32_16x16x128_f8f6f4 v[34:37], v[10:17], v[224:231], v[34:37]
	s_setprio 0
	s_barrier
	ds_read_b128 v[2:5], v196
	ds_read_b128 v[6:9], v196 offset:1024
	ds_read_b128 v[10:13], v196 offset:2048
	ds_read_b128 v[14:17], v196 offset:3072
	ds_read_b128 v[18:21], v197
	ds_read_b128 v[22:25], v197 offset:1024
	ds_read_b128 v[26:29], v197 offset:2048
	ds_read_b128 v[30:33], v197 offset:3072
	s_add_u32 s4, s38, 0x70000
	s_addc_u32 s5, s39, 0
	s_mov_b32 m0, s47
	v_lshl_add_u64 v[232:233], s[4:5], 0, v[164:165]
	ds_read_b128 v[200:203], v194 offset:32768
	ds_read_b128 v[204:207], v194 offset:33792
	ds_read_b128 v[208:211], v194 offset:34816
	ds_read_b128 v[212:215], v194 offset:35840
	ds_read_b128 v[216:219], v194 offset:36864
	ds_read_b128 v[220:223], v194 offset:37888
	ds_read_b128 v[224:227], v194 offset:38912
	ds_read_b128 v[228:231], v194 offset:39936
	global_load_lds_dwordx4 v[232:233], off
	v_lshl_add_u64 v[232:233], s[4:5], 0, v[168:169]
	s_mov_b32 m0, s48
	s_nop 0
	global_load_lds_dwordx4 v[232:233], off
	s_waitcnt vmcnt(8)
	s_waitcnt lgkmcnt(0)
	s_barrier
	s_setprio 3
	v_mfma_f32_16x16x128_f8f6f4 v[158:161], v[2:9], v[200:207], v[158:161]
	v_mfma_f32_16x16x128_f8f6f4 v[154:157], v[10:17], v[200:207], v[154:157]
	v_mfma_f32_16x16x128_f8f6f4 v[142:145], v[2:9], v[208:215], v[142:145]
	v_mfma_f32_16x16x128_f8f6f4 v[138:141], v[10:17], v[208:215], v[138:141]
	v_mfma_f32_16x16x128_f8f6f4 v[126:129], v[2:9], v[216:223], v[126:129]
	v_mfma_f32_16x16x128_f8f6f4 v[122:125], v[10:17], v[216:223], v[122:125]
	v_mfma_f32_16x16x128_f8f6f4 v[110:113], v[2:9], v[224:231], v[110:113]
	v_mfma_f32_16x16x128_f8f6f4 v[106:109], v[10:17], v[224:231], v[106:109]
	v_mfma_f32_16x16x128_f8f6f4 v[150:153], v[18:25], v[200:207], v[150:153]
	v_mfma_f32_16x16x128_f8f6f4 v[146:149], v[26:33], v[200:207], v[146:149]
	v_mfma_f32_16x16x128_f8f6f4 v[134:137], v[18:25], v[208:215], v[134:137]
	v_mfma_f32_16x16x128_f8f6f4 v[130:133], v[26:33], v[208:215], v[130:133]
	v_mfma_f32_16x16x128_f8f6f4 v[118:121], v[18:25], v[216:223], v[118:121]
	v_mfma_f32_16x16x128_f8f6f4 v[114:117], v[26:33], v[216:223], v[114:117]
	v_mfma_f32_16x16x128_f8f6f4 v[102:105], v[18:25], v[224:231], v[102:105]
	v_mfma_f32_16x16x128_f8f6f4 v[98:101], v[26:33], v[224:231], v[98:101]
	s_setprio 0
	s_barrier
	s_mov_b32 m0, s67
	v_lshl_add_u64 v[184:185], v[184:185], 0, s[18:19]
	ds_read_b128 v[200:203], v194 offset:49152
	ds_read_b128 v[204:207], v194 offset:50176
	ds_read_b128 v[208:211], v194 offset:51200
	ds_read_b128 v[212:215], v194 offset:52224
	ds_read_b128 v[216:219], v194 offset:53248
	ds_read_b128 v[220:223], v194 offset:54272
	ds_read_b128 v[224:227], v194 offset:55296
	ds_read_b128 v[228:231], v194 offset:56320
	global_load_lds_dwordx4 v[184:185], off
	v_lshl_add_u64 v[184:185], v[186:187], 0, s[18:19]
	s_mov_b32 m0, s70
	v_lshl_add_u64 v[182:183], v[182:183], 0, s[20:21]
	global_load_lds_dwordx4 v[184:185], off
	v_lshl_add_u64 v[184:185], v[182:183], 0, v[166:167]
	s_mov_b32 m0, s71
	v_lshl_add_u64 v[182:183], v[182:183], 0, v[170:171]
	global_load_lds_dwordx4 v[184:185], off
	s_mov_b32 m0, s72
	s_nop 0
	global_load_lds_dwordx4 v[182:183], off
	v_lshl_add_u64 v[182:183], v[188:189], 0, s[18:19]
	s_mov_b32 m0, s49
	s_nop 0
	global_load_lds_dwordx4 v[182:183], off
	v_lshl_add_u64 v[182:183], v[190:191], 0, s[18:19]
	s_mov_b32 m0, s50
	s_nop 0
	global_load_lds_dwordx4 v[182:183], off
	s_waitcnt vmcnt(8)
	s_waitcnt lgkmcnt(0)
	s_barrier
	s_setprio 3
	v_mfma_f32_16x16x128_f8f6f4 v[94:97], v[2:9], v[200:207], v[94:97]
	v_mfma_f32_16x16x128_f8f6f4 v[90:93], v[10:17], v[200:207], v[90:93]
	v_mfma_f32_16x16x128_f8f6f4 v[78:81], v[2:9], v[208:215], v[78:81]
	v_mfma_f32_16x16x128_f8f6f4 v[74:77], v[10:17], v[208:215], v[74:77]
	v_mfma_f32_16x16x128_f8f6f4 v[62:65], v[2:9], v[216:223], v[62:65]
	v_mfma_f32_16x16x128_f8f6f4 v[58:61], v[10:17], v[216:223], v[58:61]
	v_mfma_f32_16x16x128_f8f6f4 v[46:49], v[2:9], v[224:231], v[46:49]
	v_mfma_f32_16x16x128_f8f6f4 v[42:45], v[10:17], v[224:231], v[42:45]
	v_mfma_f32_16x16x128_f8f6f4 v[86:89], v[18:25], v[200:207], v[86:89]
	v_mfma_f32_16x16x128_f8f6f4 v[82:85], v[26:33], v[200:207], v[82:85]
	v_mfma_f32_16x16x128_f8f6f4 v[70:73], v[18:25], v[208:215], v[70:73]
	v_mfma_f32_16x16x128_f8f6f4 v[66:69], v[26:33], v[208:215], v[66:69]
	v_mfma_f32_16x16x128_f8f6f4 v[54:57], v[18:25], v[216:223], v[54:57]
	v_mfma_f32_16x16x128_f8f6f4 v[50:53], v[26:33], v[216:223], v[50:53]
	v_mfma_f32_16x16x128_f8f6f4 v[38:41], v[18:25], v[224:231], v[38:41]
	v_mfma_f32_16x16x128_f8f6f4 v[34:37], v[26:33], v[224:231], v[34:37]
	s_setprio 0
	s_barrier
	s_add_i32 s76, s76, 2
	v_lshl_add_u64 v[180:181], v[180:181], 0, s[24:25]
	s_cmp_gt_u32 s76, 25
	s_mov_b64 s[36:37], s[30:31]
	s_cbranch_scc0 .LBB0_1392

; #define PG8_STAGE(bufoff, gbase, voff) do { _Pragma("unroll") for (int _i = 0; _i < 2; ++_i) \
;         __builtin_amdgcn_global_load_lds((const unsigned*)((const char*)(gbase) + (voff)[_i]), (PG8_LAS unsigned*)(lds + (bufoff) + ldsw + _i * 8192), 16, 0, 0); } while (0)
; #define PG8_LDA(dst, b, h) do { _Pragma("unroll") for (int m = 0; m < 4; ++m) Frag<F8>::load(dst[m], lds + PG8_SA(b, h) + aoff + m * 2048); } while (0)
; #define PG8_LDB(dst, b, h) do { _Pragma("unroll") for (int n = 0; n < 2; ++n) Frag<F8>::load(dst[n], lds + PG8_SB(b, h) + boff + n * 2048); } while (0)
; #define PG8_MMA(ai, bj, At, Bt) do { __builtin_amdgcn_s_setprio(3); _Pragma("unroll") for (int m = 0; m < 4; ++m) _Pragma("unroll") for (int n = 0; n < 2; ++n) Frag<F8>::mma(acc[ai][bj][m][n], Bt[n], At[m]); \
;         __builtin_amdgcn_s_setprio(0); } while (0)
; #define PG8_WAIT_V(n) asm volatile("s_waitcnt vmcnt(" #n ")" ::: "memory")
; #define PG8_WAIT_L(n) asm volatile("s_waitcnt lgkmcnt(" #n ")" ::: "memory")
; #define PG8_BAR __builtin_amdgcn_s_barrier()
; #define PG8_SCHED __builtin_amdgcn_sched_barrier(0)
; template <class Epi, class Sched, bool ALIGN_EPI = false, bool SP2 = false, bool F8 = false>
; __device__ __forceinline__ void gemm_phase(PG8_LAS unsigned char* lds, const Gemm g, const Sched& S, const Epi& E) {
;     ...
;         PG8_STAGE(PG8_SB(0, 0), cB, voffB); PG8_STAGE(PG8_SB(0, 1), cB + hstep, voffB); PG8_STAGE(PG8_SA(0, 0), cA, voffA); PG8_STAGE(PG8_SA(0, 1), cA + hstep, voffA);
;         if (wr == 1) PG8_BAR;
;         PG8_WAIT_V(2); PG8_BAR;
;         PG8_STAGE(PG8_SB(1, 0), cB + kstep, voffB); PG8_STAGE(PG8_SA(1, 0), cA + kstep, voffA); PG8_STAGE(PG8_SB(1, 1), cB + hstep + kstep, voffB);
;         PG8_WAIT_V(6); PG8_BAR;
;     ...
;             PG8_LDB(B0, 0, 0); PG8_LDB(B1, 0, 1); PG8_SCHED; PG8_LDA(At, 0, 0); PG8_STAGE(PG8_SA(1, 1), a1 + hstep, voffA);
;             PG8_WAIT_V(8); PG8_WAIT_L(0); PG8_BAR; PG8_MMA(0, 0, At, B0); PG8_MMA(0, 1, At, B1); PG8_BAR; PG8_SCHED;
.LBB0_1418:
	s_lshl_b32 s1, s15, 5
	s_add_i32 s15, 0, 0x18000
	s_and_b32 s27, s1, 0x60
	s_add_i32 s30, s15, s14
	s_mov_b64 s[8:9], 0x80
	s_lshl_b32 s0, s22, 13
	s_lshl_b32 s1, s27, 7
	v_lshl_add_u64 v[130:131], v[154:155], 0, s[8:9]
	s_mov_b32 m0, s30
	s_add_i32 s36, s30, 0x2000
	s_add_i32 s31, s4, 0x8000
	s_add_i32 s37, s4, 0xa000
	s_waitcnt vmcnt(2)
	s_barrier
	global_load_lds_dwordx4 v[130:131], off
	v_lshl_add_u64 v[132:133], v[156:157], 0, s[8:9]
	s_mov_b32 m0, s36
	v_lshl_add_u64 v[128:129], v[148:149], 0, s[8:9]
	v_lshl_add_u64 v[134:135], v[146:147], 0, s[8:9]
	s_add_u32 s8, s6, 0x70080
	global_load_lds_dwordx4 v[132:133], off
	s_mov_b32 m0, s31
	s_addc_u32 s9, s7, 0
	s_add_i32 s16, 0, 0x1c000
	global_load_lds_dwordx4 v[128:129], off
	s_mov_b32 m0, s37
	s_add_i32 s38, s16, s14
	global_load_lds_dwordx4 v[134:135], off
	v_lshl_add_u64 v[136:137], s[8:9], 0, v[158:159]
	s_mov_b32 m0, s38
	s_add_i32 s39, s38, 0x2000
	global_load_lds_dwordx4 v[136:137], off
	v_lshl_add_u64 v[138:139], s[8:9], 0, v[144:145]
	s_mov_b32 m0, s39
	v_and_b32_e32 v160, 15, v0
	global_load_lds_dwordx4 v[138:139], off
	v_bfe_u32 v161, v0, 4, 2
	v_lshlrev_b32_e32 v1, 6, v160
	v_lshlrev_b32_e32 v0, 2, v0
	v_lshl_or_b32 v1, v161, 4, v1
	v_and_b32_e32 v0, 32, v0
	v_bitop3_b32 v2, v1, s0, v0 bitop3:0xde
	v_bitop3_b32 v0, v1, s1, v0 bitop3:0xde
	s_add_i32 s42, 0, 0x10000
	s_add_i32 s44, 0, 0x14000
	v_add_u32_e32 v168, s42, v0
	s_add_u32 s20, s10, 0x70080
	s_waitcnt vmcnt(6)
	s_barrier
	v_add_u32_e32 v167, s44, v0
	s_addc_u32 s21, s11, 0
	s_add_i32 s42, s42, s14
	ds_read_b128 v[96:99], v168
	ds_read_b128 v[100:103], v168 offset:1024
	ds_read_b128 v[104:107], v168 offset:2048
	ds_read_b128 v[108:111], v168 offset:3072
	ds_read_b128 v[170:173], v167
	ds_read_b128 v[174:177], v167 offset:1024
	ds_read_b128 v[178:181], v167 offset:2048
	ds_read_b128 v[182:185], v167 offset:3072
	s_add_i32 s46, s4, 0xc000
	s_add_i32 s45, s4, 0xe000
	s_add_i32 s41, s42, 0x2000
	s_add_u32 s18, s6, 0x70100
	s_addc_u32 s19, s7, 0
	s_add_i32 s44, s44, s14
	s_add_i32 s43, s44, 0x2000
	v_add_u32_e32 v165, s16, v0
	s_add_u32 s16, s10, 0x70100
	s_addc_u32 s17, s11, 0
	s_add_u32 s14, s6, 0x70180
	v_add_u32_e32 v166, s15, v0
	s_addc_u32 s15, s7, 0
	s_add_u32 s6, s10, 0x70180
	s_mov_b32 s3, 0x8000
	s_mov_b32 s26, 0xc000
	s_addc_u32 s7, s11, 0
	s_mov_b32 s8, 0
	v_add_u32_e32 v163, 0, v2
	s_cmpk_gt_u32 s47, 0xff
	s_mov_b32 m0, s46
	v_lshl_add_u64 v[0:1], s[20:21], 0, v[158:159]
	ds_read_b128 v[36:39], v163
	ds_read_b128 v[40:43], v163 offset:1024
	ds_read_b128 v[44:47], v163 offset:2048
	ds_read_b128 v[48:51], v163 offset:3072
	ds_read_b128 v[68:71], v163 offset:4096
	ds_read_b128 v[72:75], v163 offset:5120
	ds_read_b128 v[76:79], v163 offset:6144
	ds_read_b128 v[80:83], v163 offset:7168
	global_load_lds_dwordx4 v[0:1], off
	v_lshl_add_u64 v[0:1], s[20:21], 0, v[144:145]
	s_mov_b32 m0, s45
	s_nop 0
	global_load_lds_dwordx4 v[0:1], off
	s_waitcnt vmcnt(8)
	s_waitcnt lgkmcnt(0)
	s_barrier
	s_setprio 3
	s_mov_b32 s9, s8
	s_mov_b32 s10, s8
	s_mov_b32 s11, s8
	v_mov_b64_e32 v[0:1], s[8:9]
	v_mov_b64_e32 v[30:31], s[10:11]
	v_mov_b64_e32 v[34:35], s[10:11]
	v_mov_b64_e32 v[22:23], s[10:11]
	v_mov_b64_e32 v[26:27], s[10:11]
	v_mov_b64_e32 v[14:15], s[10:11]
	v_mov_b64_e32 v[18:19], s[10:11]
	v_mov_b64_e32 v[4:5], s[8:9]
	v_mov_b64_e32 v[8:9], s[8:9]
	v_mov_b64_e32 v[2:3], s[10:11]
	v_mov_b64_e32 v[28:29], s[8:9]
	v_mov_b64_e32 v[32:33], s[8:9]
	v_mov_b64_e32 v[20:21], s[8:9]
	v_mov_b64_e32 v[24:25], s[8:9]
	v_mov_b64_e32 v[12:13], s[8:9]
	v_mov_b64_e32 v[16:17], s[8:9]
	v_mov_b64_e32 v[6:7], s[10:11]
	v_mov_b64_e32 v[10:11], s[10:11]
	v_mov_b32_e32 v164, 0x7f7f7f7f
	s_waitcnt lgkmcnt(0)
	v_mfma_f32_16x16x128_f8f6f4 v[28:31], v[96:103], v[36:43], v[28:31]
	v_mfma_f32_16x16x128_f8f6f4 v[32:35], v[104:111], v[36:43], v[32:35]
	v_mfma_f32_16x16x128_f8f6f4 v[20:23], v[96:103], v[44:51], v[20:23]
	v_mfma_f32_16x16x128_f8f6f4 v[24:27], v[104:111], v[44:51], v[24:27]
	v_mfma_f32_16x16x128_f8f6f4 v[12:15], v[96:103], v[68:75], v[12:15]
	v_mfma_f32_16x16x128_f8f6f4 v[16:19], v[104:111], v[68:75], v[16:19]
	v_mfma_f32_16x16x128_f8f6f4 v[4:7], v[96:103], v[76:83], v[4:7]
	v_mfma_f32_16x16x128_f8f6f4 v[8:11], v[104:111], v[76:83], v[8:11]
	v_mov_b64_e32 v[62:63], s[10:11]
	v_mov_b64_e32 v[66:67], s[10:11]
	v_mov_b64_e32 v[54:55], s[10:11]
	v_mov_b64_e32 v[58:59], s[10:11]
	v_mov_b64_e32 v[60:61], s[8:9]
	v_mov_b64_e32 v[64:65], s[8:9]
	v_mov_b64_e32 v[52:53], s[8:9]
	v_mov_b64_e32 v[56:57], s[8:9]
	v_mfma_f32_16x16x128_f8f6f4 v[60:63], v[170:177], v[36:43], v[60:63]
	v_mfma_f32_16x16x128_f8f6f4 v[64:67], v[178:185], v[36:43], v[64:67]
	v_mfma_f32_16x16x128_f8f6f4 v[52:55], v[170:177], v[44:51], v[52:55]
	v_mfma_f32_16x16x128_f8f6f4 v[56:59], v[178:185], v[44:51], v[56:59]
	v_mov_b64_e32 v[46:47], s[10:11]
	v_mov_b64_e32 v[50:51], s[10:11]
	v_mov_b64_e32 v[38:39], s[10:11]
	v_mov_b64_e32 v[42:43], s[10:11]
	v_mov_b64_e32 v[44:45], s[8:9]
	v_mov_b64_e32 v[48:49], s[8:9]
	v_mov_b64_e32 v[36:37], s[8:9]
	v_mov_b64_e32 v[40:41], s[8:9]
	v_mfma_f32_16x16x128_f8f6f4 v[44:47], v[170:177], v[68:75], v[44:47]
	v_mfma_f32_16x16x128_f8f6f4 v[48:51], v[178:185], v[68:75], v[48:51]
	v_mfma_f32_16x16x128_f8f6f4 v[36:39], v[170:177], v[76:83], v[36:39]
	v_mfma_f32_16x16x128_f8f6f4 v[40:43], v[178:185], v[76:83], v[40:43]
	s_setprio 0
	s_barrier
; #define PG8_STAGE(bufoff, gbase, voff) do { _Pragma("unroll") for (int _i = 0; _i < 2; ++_i) \
;         __builtin_amdgcn_global_load_lds((const unsigned*)((const char*)(gbase) + (voff)[_i]), (PG8_LAS unsigned*)(lds + (bufoff) + ldsw + _i * 8192), 16, 0, 0); } while (0)
; #define PG8_LDA(dst, b, h) do { _Pragma("unroll") for (int m = 0; m < 4; ++m) Frag<F8>::load(dst[m], lds + PG8_SA(b, h) + aoff + m * 2048); } while (0)
; #define PG8_LDB(dst, b, h) do { _Pragma("unroll") for (int n = 0; n < 2; ++n) Frag<F8>::load(dst[n], lds + PG8_SB(b, h) + boff + n * 2048); } while (0)
; #define PG8_MMA(ai, bj, At, Bt) do { __builtin_amdgcn_s_setprio(3); _Pragma("unroll") for (int m = 0; m < 4; ++m) _Pragma("unroll") for (int n = 0; n < 2; ++n) Frag<F8>::mma(acc[ai][bj][m][n], Bt[n], At[m]); \
;         __builtin_amdgcn_s_setprio(0); } while (0)
; #define PG8_WAIT_V(n) asm volatile("s_waitcnt vmcnt(" #n ")" ::: "memory")
; #define PG8_WAIT_L(n) asm volatile("s_waitcnt lgkmcnt(" #n ")" ::: "memory")
; #define PG8_BAR __builtin_amdgcn_s_barrier()
; #define PG8_SCHED __builtin_amdgcn_sched_barrier(0)
; template <class Epi, class Sched, bool ALIGN_EPI = false, bool SP2 = false, bool F8 = false>
; __device__ __forceinline__ void gemm_phase(PG8_LAS unsigned char* lds, const Gemm g, const Sched& S, const Epi& E) {
;     ...
;             PG8_WAIT_V(8); PG8_WAIT_L(0); PG8_BAR; PG8_MMA(0, 0, At, B0); PG8_MMA(0, 1, At, B1); PG8_BAR; PG8_SCHED;
;             PG8_LDA(At, 0, 1); PG8_STAGE(PG8_SB(0, 0), b2, voffB); PG8_STAGE(PG8_SB(0, 1), b2 + hstep, voffB); PG8_STAGE(PG8_SA(0, 0), a2, voffA);
;             PG8_WAIT_V(8); PG8_WAIT_L(0); PG8_BAR; PG8_MMA(1, 0, At, B0); PG8_MMA(1, 1, At, B1); PG8_BAR; PG8_SCHED;
;             PG8_LDB(B0, 1, 0); PG8_LDB(B1, 1, 1); PG8_SCHED; PG8_LDA(At, 1, 0); PG8_STAGE(PG8_SA(0, 1), a2 + hstep, voffA);
;             PG8_WAIT_V(8); PG8_WAIT_L(0); PG8_BAR; PG8_MMA(0, 0, At, B0); PG8_MMA(0, 1, At, B1); PG8_BAR; PG8_SCHED;
	s_mov_b64 s[8:9], 0x100
	s_mov_b32 m0, s42
	v_lshl_add_u64 v[68:69], v[154:155], 0, s[8:9]
	ds_read_b128 v[186:189], v163 offset:16384
	ds_read_b128 v[190:193], v163 offset:17408
	ds_read_b128 v[194:197], v163 offset:18432
	ds_read_b128 v[198:201], v163 offset:19456
	ds_read_b128 v[202:205], v163 offset:20480
	ds_read_b128 v[206:209], v163 offset:21504
	ds_read_b128 v[210:213], v163 offset:22528
	ds_read_b128 v[214:217], v163 offset:23552
	global_load_lds_dwordx4 v[68:69], off
	v_lshl_add_u64 v[68:69], v[156:157], 0, s[8:9]
	s_mov_b32 m0, s41
	s_nop 0
	global_load_lds_dwordx4 v[68:69], off
	v_lshl_add_u64 v[68:69], s[18:19], 0, v[158:159]
	s_mov_b32 m0, s44
	s_nop 0
	global_load_lds_dwordx4 v[68:69], off
	v_lshl_add_u64 v[68:69], s[18:19], 0, v[144:145]
	s_mov_b32 m0, s43
	s_nop 0
	global_load_lds_dwordx4 v[68:69], off
	v_lshl_add_u64 v[68:69], v[148:149], 0, s[8:9]
	s_mov_b32 m0, s4
	s_nop 0
	global_load_lds_dwordx4 v[68:69], off
	v_lshl_add_u64 v[68:69], v[146:147], 0, s[8:9]
	s_mov_b32 m0, s5
	s_nop 0
	global_load_lds_dwordx4 v[68:69], off
	s_waitcnt vmcnt(8)
	s_waitcnt lgkmcnt(0)
	s_barrier
	s_setprio 3
	v_mov_b64_e32 v[70:71], v[2:3]
	v_mov_b64_e32 v[86:87], v[2:3]
	v_mov_b64_e32 v[74:75], v[2:3]
	v_mov_b64_e32 v[90:91], v[2:3]
	v_mov_b64_e32 v[78:79], v[2:3]
	v_mov_b64_e32 v[94:95], v[2:3]
	v_mov_b64_e32 v[82:83], v[2:3]
	v_mov_b64_e32 v[68:69], v[0:1]
	v_mov_b64_e32 v[84:85], v[0:1]
	v_mov_b64_e32 v[72:73], v[0:1]
	v_mov_b64_e32 v[88:89], v[0:1]
	v_mov_b64_e32 v[76:77], v[0:1]
	v_mov_b64_e32 v[92:93], v[0:1]
	v_mov_b64_e32 v[80:81], v[0:1]
	s_waitcnt lgkmcnt(0)
	v_mfma_f32_16x16x128_f8f6f4 v[68:71], v[96:103], v[186:193], v[68:71]
	v_mfma_f32_16x16x128_f8f6f4 v[84:87], v[104:111], v[186:193], v[84:87]
	v_mfma_f32_16x16x128_f8f6f4 v[72:75], v[96:103], v[194:201], v[72:75]
	v_mfma_f32_16x16x128_f8f6f4 v[88:91], v[104:111], v[194:201], v[88:91]
	v_mfma_f32_16x16x128_f8f6f4 v[76:79], v[96:103], v[202:209], v[76:79]
	v_mfma_f32_16x16x128_f8f6f4 v[92:95], v[104:111], v[202:209], v[92:95]
	v_mfma_f32_16x16x128_f8f6f4 v[80:83], v[96:103], v[210:217], v[80:83]
	v_mov_b64_e32 v[98:99], v[2:3]
	v_mov_b64_e32 v[96:97], v[0:1]
	v_mfma_f32_16x16x128_f8f6f4 v[96:99], v[104:111], v[210:217], v[96:99]
	v_mov_b64_e32 v[118:119], v[2:3]
	v_mov_b64_e32 v[126:127], v[2:3]
	v_mov_b64_e32 v[110:111], v[2:3]
	v_mov_b64_e32 v[122:123], v[2:3]
	v_mov_b64_e32 v[106:107], v[2:3]
	v_mov_b64_e32 v[114:115], v[2:3]
	v_mov_b64_e32 v[102:103], v[2:3]
	v_mov_b64_e32 v[116:117], v[0:1]
	v_mov_b64_e32 v[124:125], v[0:1]
	v_mov_b64_e32 v[108:109], v[0:1]
	v_mov_b64_e32 v[120:121], v[0:1]
	v_mov_b64_e32 v[104:105], v[0:1]
	v_mov_b64_e32 v[112:113], v[0:1]
	v_mov_b64_e32 v[100:101], v[0:1]
	v_mfma_f32_16x16x128_f8f6f4 v[116:119], v[170:177], v[186:193], v[116:119]
	v_mfma_f32_16x16x128_f8f6f4 v[124:127], v[178:185], v[186:193], v[124:127]
	v_mfma_f32_16x16x128_f8f6f4 v[108:111], v[170:177], v[194:201], v[108:111]
	v_mfma_f32_16x16x128_f8f6f4 v[120:123], v[178:185], v[194:201], v[120:123]
	v_mfma_f32_16x16x128_f8f6f4 v[104:107], v[170:177], v[202:209], v[104:107]
	v_mfma_f32_16x16x128_f8f6f4 v[112:115], v[178:185], v[202:209], v[112:115]
	v_mfma_f32_16x16x128_f8f6f4 v[100:103], v[170:177], v[210:217], v[100:103]
	v_mfma_f32_16x16x128_f8f6f4 v[0:3], v[178:185], v[210:217], v[0:3]
	s_setprio 0
	s_barrier
	ds_read_b128 v[170:173], v166
	ds_read_b128 v[174:177], v166 offset:1024
	ds_read_b128 v[178:181], v166 offset:2048
	ds_read_b128 v[182:185], v166 offset:3072
	ds_read_b128 v[186:189], v165
	ds_read_b128 v[190:193], v165 offset:1024
	ds_read_b128 v[194:197], v165 offset:2048
	ds_read_b128 v[198:201], v165 offset:3072
	s_mov_b32 m0, s33
	v_lshl_add_u64 v[234:235], s[16:17], 0, v[158:159]
	ds_read_b128 v[202:205], v163 offset:32768
	ds_read_b128 v[206:209], v163 offset:33792
	ds_read_b128 v[210:213], v163 offset:34816
	ds_read_b128 v[214:217], v163 offset:35840
	ds_read_b128 v[218:221], v163 offset:36864
	ds_read_b128 v[222:225], v163 offset:37888
	ds_read_b128 v[226:229], v163 offset:38912
	ds_read_b128 v[230:233], v163 offset:39936
	global_load_lds_dwordx4 v[234:235], off
	v_lshl_add_u64 v[234:235], s[16:17], 0, v[144:145]
	s_mov_b32 m0, s40
	s_nop 0
	global_load_lds_dwordx4 v[234:235], off
	s_waitcnt vmcnt(8)
	s_waitcnt lgkmcnt(0)
	s_barrier
	s_setprio 3
	v_mfma_f32_16x16x128_f8f6f4 v[28:31], v[170:177], v[202:209], v[28:31]
	v_mfma_f32_16x16x128_f8f6f4 v[32:35], v[178:185], v[202:209], v[32:35]
	v_mfma_f32_16x16x128_f8f6f4 v[20:23], v[170:177], v[210:217], v[20:23]
	v_mfma_f32_16x16x128_f8f6f4 v[24:27], v[178:185], v[210:217], v[24:27]
	v_mfma_f32_16x16x128_f8f6f4 v[12:15], v[170:177], v[218:225], v[12:15]
	v_mfma_f32_16x16x128_f8f6f4 v[16:19], v[178:185], v[218:225], v[16:19]
	v_mfma_f32_16x16x128_f8f6f4 v[4:7], v[170:177], v[226:233], v[4:7]
	v_mfma_f32_16x16x128_f8f6f4 v[8:11], v[178:185], v[226:233], v[8:11]
	v_mfma_f32_16x16x128_f8f6f4 v[60:63], v[186:193], v[202:209], v[60:63]
	v_mfma_f32_16x16x128_f8f6f4 v[64:67], v[194:201], v[202:209], v[64:67]
	v_mfma_f32_16x16x128_f8f6f4 v[52:55], v[186:193], v[210:217], v[52:55]
	v_mfma_f32_16x16x128_f8f6f4 v[56:59], v[194:201], v[210:217], v[56:59]
	v_mfma_f32_16x16x128_f8f6f4 v[44:47], v[186:193], v[218:225], v[44:47]
	v_mfma_f32_16x16x128_f8f6f4 v[48:51], v[194:201], v[218:225], v[48:51]
	v_mfma_f32_16x16x128_f8f6f4 v[36:39], v[186:193], v[226:233], v[36:39]
	v_mfma_f32_16x16x128_f8f6f4 v[40:43], v[194:201], v[226:233], v[40:43]
	s_setprio 0
	s_barrier
; #define PG8_STAGE(bufoff, gbase, voff) do { _Pragma("unroll") for (int _i = 0; _i < 2; ++_i) \
;         __builtin_amdgcn_global_load_lds((const unsigned*)((const char*)(gbase) + (voff)[_i]), (PG8_LAS unsigned*)(lds + (bufoff) + ldsw + _i * 8192), 16, 0, 0); } while (0)
; #define PG8_LDA(dst, b, h) do { _Pragma("unroll") for (int m = 0; m < 4; ++m) Frag<F8>::load(dst[m], lds + PG8_SA(b, h) + aoff + m * 2048); } while (0)
; #define PG8_LDB(dst, b, h) do { _Pragma("unroll") for (int n = 0; n < 2; ++n) Frag<F8>::load(dst[n], lds + PG8_SB(b, h) + boff + n * 2048); } while (0)
; #define PG8_MMA(ai, bj, At, Bt) do { __builtin_amdgcn_s_setprio(3); _Pragma("unroll") for (int m = 0; m < 4; ++m) _Pragma("unroll") for (int n = 0; n < 2; ++n) Frag<F8>::mma(acc[ai][bj][m][n], Bt[n], At[m]); \
;         __builtin_amdgcn_s_setprio(0); } while (0)
; #define PG8_WAIT_V(n) asm volatile("s_waitcnt vmcnt(" #n ")" ::: "memory")
; #define PG8_WAIT_L(n) asm volatile("s_waitcnt lgkmcnt(" #n ")" ::: "memory")
; #define PG8_BAR __builtin_amdgcn_s_barrier()
; #define PG8_SCHED __builtin_amdgcn_sched_barrier(0)
; template <class Epi, class Sched, bool ALIGN_EPI = false, bool SP2 = false, bool F8 = false>
; __device__ __forceinline__ void gemm_phase(PG8_LAS unsigned char* lds, const Gemm g, const Sched& S, const Epi& E) {
;     ...
;             PG8_LDB(B0, 0, 0); PG8_LDB(B1, 0, 1); PG8_SCHED; PG8_LDA(At, 0, 0); PG8_STAGE(PG8_SA(1, 1), a1 + hstep, voffA);
;             PG8_WAIT_V(8); PG8_WAIT_L(0); PG8_BAR; PG8_MMA(0, 0, At, B0); PG8_MMA(0, 1, At, B1); PG8_BAR; PG8_SCHED;
;             PG8_LDA(At, 0, 1); PG8_STAGE(PG8_SB(0, 0), b2, voffB); PG8_STAGE(PG8_SB(0, 1), b2 + hstep, voffB); PG8_STAGE(PG8_SA(0, 0), a2, voffA);
;             PG8_WAIT_V(8); PG8_WAIT_L(0); PG8_BAR; PG8_MMA(1, 0, At, B0); PG8_MMA(1, 1, At, B1); PG8_BAR; PG8_SCHED;
;             PG8_LDB(B0, 1, 0); PG8_LDB(B1, 1, 1); PG8_SCHED; PG8_LDA(At, 1, 0); PG8_STAGE(PG8_SA(0, 1), a2 + hstep, voffA);
;             PG8_WAIT_V(8); PG8_WAIT_L(0); PG8_BAR; PG8_MMA(0, 0, At, B0); PG8_MMA(0, 1, At, B1); PG8_BAR; PG8_SCHED;
;             PG8_LDA(At, 1, 1); PG8_STAGE(PG8_SB(1, 0), b3, voffB); PG8_STAGE(PG8_SB(1, 1), b3 + hstep, voffB); PG8_STAGE(PG8_SA(1, 0), a3, voffA);
;             PG8_WAIT_V(8); PG8_WAIT_L(0); PG8_BAR; PG8_MMA(1, 0, At, B0); PG8_MMA(1, 1, At, B1); PG8_BAR; PG8_SCHED;
	s_mov_b64 s[8:9], 0x180
	s_mov_b32 m0, s30
	v_lshl_add_u64 v[234:235], v[154:155], 0, s[8:9]
	ds_read_b128 v[202:205], v163 offset:49152
	ds_read_b128 v[206:209], v163 offset:50176
	ds_read_b128 v[210:213], v163 offset:51200
	ds_read_b128 v[214:217], v163 offset:52224
	ds_read_b128 v[218:221], v163 offset:53248
	ds_read_b128 v[222:225], v163 offset:54272
	ds_read_b128 v[226:229], v163 offset:55296
	ds_read_b128 v[230:233], v163 offset:56320
	global_load_lds_dwordx4 v[234:235], off
	v_lshl_add_u64 v[234:235], v[156:157], 0, s[8:9]
	s_mov_b32 m0, s36
	s_nop 0
	global_load_lds_dwordx4 v[234:235], off
	v_lshl_add_u64 v[234:235], s[14:15], 0, v[158:159]
	s_mov_b32 m0, s38
	s_nop 0
	global_load_lds_dwordx4 v[234:235], off
	v_lshl_add_u64 v[234:235], s[14:15], 0, v[144:145]
	s_mov_b32 m0, s39
	s_nop 0
	global_load_lds_dwordx4 v[234:235], off
	v_lshl_add_u64 v[234:235], v[148:149], 0, s[8:9]
	s_mov_b32 m0, s31
	s_nop 0
	global_load_lds_dwordx4 v[234:235], off
	v_lshl_add_u64 v[234:235], v[146:147], 0, s[8:9]
	s_mov_b32 m0, s37
	s_nop 0
	global_load_lds_dwordx4 v[234:235], off
	s_waitcnt vmcnt(8)
	s_waitcnt lgkmcnt(0)
	s_barrier
	s_setprio 3
	v_mfma_f32_16x16x128_f8f6f4 v[68:71], v[170:177], v[202:209], v[68:71]
	v_mfma_f32_16x16x128_f8f6f4 v[84:87], v[178:185], v[202:209], v[84:87]
	v_mfma_f32_16x16x128_f8f6f4 v[72:75], v[170:177], v[210:217], v[72:75]
	v_mfma_f32_16x16x128_f8f6f4 v[88:91], v[178:185], v[210:217], v[88:91]
	v_mfma_f32_16x16x128_f8f6f4 v[76:79], v[170:177], v[218:225], v[76:79]
	v_mfma_f32_16x16x128_f8f6f4 v[92:95], v[178:185], v[218:225], v[92:95]
	v_mfma_f32_16x16x128_f8f6f4 v[80:83], v[170:177], v[226:233], v[80:83]
	v_mfma_f32_16x16x128_f8f6f4 v[96:99], v[178:185], v[226:233], v[96:99]
	v_mfma_f32_16x16x128_f8f6f4 v[116:119], v[186:193], v[202:209], v[116:119]
	v_mfma_f32_16x16x128_f8f6f4 v[124:127], v[194:201], v[202:209], v[124:127]
	v_mfma_f32_16x16x128_f8f6f4 v[108:111], v[186:193], v[210:217], v[108:111]
	v_mfma_f32_16x16x128_f8f6f4 v[120:123], v[194:201], v[210:217], v[120:123]
	v_mfma_f32_16x16x128_f8f6f4 v[104:107], v[186:193], v[218:225], v[104:107]
	v_mfma_f32_16x16x128_f8f6f4 v[112:115], v[194:201], v[218:225], v[112:115]
	v_mfma_f32_16x16x128_f8f6f4 v[100:103], v[186:193], v[226:233], v[100:103]
	v_mfma_f32_16x16x128_f8f6f4 v[0:3], v[194:201], v[226:233], v[0:3]
	s_setprio 0
	s_barrier
	ds_read_b128 v[170:173], v168
	ds_read_b128 v[174:177], v168 offset:1024
	ds_read_b128 v[178:181], v168 offset:2048
	ds_read_b128 v[182:185], v168 offset:3072
	ds_read_b128 v[186:189], v167
	ds_read_b128 v[190:193], v167 offset:1024
	ds_read_b128 v[194:197], v167 offset:2048
	ds_read_b128 v[198:201], v167 offset:3072
	s_mov_b32 m0, s46
	v_lshl_add_u64 v[158:159], s[6:7], 0, v[158:159]
	ds_read_b128 v[202:205], v163
	ds_read_b128 v[206:209], v163 offset:1024
	ds_read_b128 v[210:213], v163 offset:2048
	ds_read_b128 v[214:217], v163 offset:3072
	ds_read_b128 v[218:221], v163 offset:4096
	ds_read_b128 v[222:225], v163 offset:5120
	ds_read_b128 v[226:229], v163 offset:6144
	ds_read_b128 v[230:233], v163 offset:7168
	global_load_lds_dwordx4 v[158:159], off
	v_lshl_add_u64 v[144:145], s[6:7], 0, v[144:145]
	s_mov_b32 m0, s45
	s_nop 0
	global_load_lds_dwordx4 v[144:145], off
	s_waitcnt vmcnt(8)
	s_waitcnt lgkmcnt(0)
	s_barrier
	s_setprio 3
	v_mfma_f32_16x16x128_f8f6f4 v[28:31], v[170:177], v[202:209], v[28:31]
	v_mfma_f32_16x16x128_f8f6f4 v[32:35], v[178:185], v[202:209], v[32:35]
	v_mfma_f32_16x16x128_f8f6f4 v[20:23], v[170:177], v[210:217], v[20:23]
	v_mfma_f32_16x16x128_f8f6f4 v[24:27], v[178:185], v[210:217], v[24:27]
	v_mfma_f32_16x16x128_f8f6f4 v[12:15], v[170:177], v[218:225], v[12:15]
	v_mfma_f32_16x16x128_f8f6f4 v[16:19], v[178:185], v[218:225], v[16:19]
	v_mfma_f32_16x16x128_f8f6f4 v[4:7], v[170:177], v[226:233], v[4:7]
	v_mfma_f32_16x16x128_f8f6f4 v[8:11], v[178:185], v[226:233], v[8:11]
	v_mfma_f32_16x16x128_f8f6f4 v[60:63], v[186:193], v[202:209], v[60:63]
	v_mfma_f32_16x16x128_f8f6f4 v[64:67], v[194:201], v[202:209], v[64:67]
	v_mfma_f32_16x16x128_f8f6f4 v[52:55], v[186:193], v[210:217], v[52:55]
	v_mfma_f32_16x16x128_f8f6f4 v[56:59], v[194:201], v[210:217], v[56:59]
	v_mfma_f32_16x16x128_f8f6f4 v[44:47], v[186:193], v[218:225], v[44:47]
	v_mfma_f32_16x16x128_f8f6f4 v[48:51], v[194:201], v[218:225], v[48:51]
	v_mfma_f32_16x16x128_f8f6f4 v[36:39], v[186:193], v[226:233], v[36:39]
	v_mfma_f32_16x16x128_f8f6f4 v[40:43], v[194:201], v[226:233], v[40:43]
	s_setprio 0
	s_barrier
	s_mov_b32 m0, s42
	ds_read_b128 v[202:205], v163 offset:16384
	ds_read_b128 v[206:209], v163 offset:17408
	ds_read_b128 v[210:213], v163 offset:18432
	ds_read_b128 v[214:217], v163 offset:19456
	ds_read_b128 v[218:221], v163 offset:20480
	ds_read_b128 v[222:225], v163 offset:21504
	ds_read_b128 v[226:229], v163 offset:22528
	ds_read_b128 v[230:233], v163 offset:23552
	global_load_lds_dwordx4 v[154:155], off
	s_mov_b32 m0, s41
	s_nop 0
	global_load_lds_dwordx4 v[156:157], off
	s_mov_b32 m0, s44
	s_nop 0
	global_load_lds_dwordx4 v[152:153], off
	s_mov_b32 m0, s43
	s_nop 0
	global_load_lds_dwordx4 v[150:151], off
	s_mov_b32 m0, s4
	s_nop 0
	global_load_lds_dwordx4 v[148:149], off
	s_mov_b32 m0, s5
	s_nop 0
	global_load_lds_dwordx4 v[146:147], off
	s_waitcnt vmcnt(8)
	s_waitcnt lgkmcnt(0)
	s_barrier
; #define PG8_STAGE(bufoff, gbase, voff) do { _Pragma("unroll") for (int _i = 0; _i < 2; ++_i) \
;         __builtin_amdgcn_global_load_lds((const unsigned*)((const char*)(gbase) + (voff)[_i]), (PG8_LAS unsigned*)(lds + (bufoff) + ldsw + _i * 8192), 16, 0, 0); } while (0)
; #define PG8_LDA(dst, b, h) do { _Pragma("unroll") for (int m = 0; m < 4; ++m) Frag<F8>::load(dst[m], lds + PG8_SA(b, h) + aoff + m * 2048); } while (0)
; #define PG8_MMA(ai, bj, At, Bt) do { __builtin_amdgcn_s_setprio(3); _Pragma("unroll") for (int m = 0; m < 4; ++m) _Pragma("unroll") for (int n = 0; n < 2; ++n) Frag<F8>::mma(acc[ai][bj][m][n], Bt[n], At[m]); \
;         __builtin_amdgcn_s_setprio(0); } while (0)
; #define PG8_WAIT_V(n) asm volatile("s_waitcnt vmcnt(" #n ")" ::: "memory")
; #define PG8_WAIT_L(n) asm volatile("s_waitcnt lgkmcnt(" #n ")" ::: "memory")
; #define PG8_BAR __builtin_amdgcn_s_barrier()
; #define PG8_SCHED __builtin_amdgcn_sched_barrier(0)
; template <class Epi, class Sched, bool ALIGN_EPI = false, bool SP2 = false, bool F8 = false>
; __device__ __forceinline__ void gemm_phase(PG8_LAS unsigned char* lds, const Gemm g, const Sched& S, const Epi& E) {
;     ...
;             PG8_WAIT_V(8); PG8_WAIT_L(0); PG8_BAR; PG8_MMA(0, 0, At, B0); PG8_MMA(0, 1, At, B1); PG8_BAR; PG8_SCHED;
;             PG8_LDA(At, 1, 1); PG8_STAGE(PG8_SB(1, 0), b3, voffB); PG8_STAGE(PG8_SB(1, 1), b3 + hstep, voffB); PG8_STAGE(PG8_SA(1, 0), a3, voffA);
;             PG8_WAIT_V(8); PG8_WAIT_L(0); PG8_BAR; PG8_MMA(1, 0, At, B0); PG8_MMA(1, 1, At, B1); PG8_BAR; PG8_SCHED;
;     ...
;         }
;         if constexpr (ALIGN_EPI) { if (wr == 0) PG8_BAR; }
	s_setprio 3
	v_mfma_f32_16x16x128_f8f6f4 v[68:71], v[170:177], v[202:209], v[68:71]
	v_mfma_f32_16x16x128_f8f6f4 v[84:87], v[178:185], v[202:209], v[84:87]
	v_mfma_f32_16x16x128_f8f6f4 v[72:75], v[170:177], v[210:217], v[72:75]
	v_mfma_f32_16x16x128_f8f6f4 v[88:91], v[178:185], v[210:217], v[88:91]
	v_mfma_f32_16x16x128_f8f6f4 v[76:79], v[170:177], v[218:225], v[76:79]
	v_mfma_f32_16x16x128_f8f6f4 v[92:95], v[178:185], v[218:225], v[92:95]
	v_mfma_f32_16x16x128_f8f6f4 v[80:83], v[170:177], v[226:233], v[80:83]
	v_mfma_f32_16x16x128_f8f6f4 v[96:99], v[178:185], v[226:233], v[96:99]
	v_mfma_f32_16x16x128_f8f6f4 v[116:119], v[186:193], v[202:209], v[116:119]
	v_mfma_f32_16x16x128_f8f6f4 v[124:127], v[194:201], v[202:209], v[124:127]
	v_mfma_f32_16x16x128_f8f6f4 v[108:111], v[186:193], v[210:217], v[108:111]
	v_mfma_f32_16x16x128_f8f6f4 v[120:123], v[194:201], v[210:217], v[120:123]
	v_mfma_f32_16x16x128_f8f6f4 v[104:107], v[186:193], v[218:225], v[104:107]
	v_mfma_f32_16x16x128_f8f6f4 v[112:115], v[194:201], v[218:225], v[112:115]
	v_mfma_f32_16x16x128_f8f6f4 v[100:103], v[186:193], v[226:233], v[100:103]
	v_mfma_f32_16x16x128_f8f6f4 v[0:3], v[194:201], v[226:233], v[0:3]
	s_setprio 0
	s_barrier
	ds_read_b128 v[144:147], v166
	ds_read_b128 v[148:151], v166 offset:1024
	ds_read_b128 v[152:155], v166 offset:2048
	ds_read_b128 v[156:159], v166 offset:3072
	ds_read_b128 v[166:169], v165
	ds_read_b128 v[170:173], v165 offset:1024
	ds_read_b128 v[174:177], v165 offset:2048
	ds_read_b128 v[178:181], v165 offset:3072
	s_mov_b32 m0, s33
	ds_read_b128 v[182:185], v163 offset:32768
	ds_read_b128 v[186:189], v163 offset:33792
	ds_read_b128 v[190:193], v163 offset:34816
	ds_read_b128 v[194:197], v163 offset:35840
	ds_read_b128 v[198:201], v163 offset:36864
	ds_read_b128 v[202:205], v163 offset:37888
	ds_read_b128 v[206:209], v163 offset:38912
	ds_read_b128 v[210:213], v163 offset:39936
	global_load_lds_dwordx4 v[140:141], off
	s_mov_b32 m0, s40
	s_nop 0
	global_load_lds_dwordx4 v[142:143], off
	s_waitcnt vmcnt(8)
	s_waitcnt lgkmcnt(0)
	s_barrier
	s_setprio 3
	v_mfma_f32_16x16x128_f8f6f4 v[28:31], v[144:151], v[182:189], v[28:31]
	v_mfma_f32_16x16x128_f8f6f4 v[32:35], v[152:159], v[182:189], v[32:35]
	v_mfma_f32_16x16x128_f8f6f4 v[20:23], v[144:151], v[190:197], v[20:23]
	v_mfma_f32_16x16x128_f8f6f4 v[24:27], v[152:159], v[190:197], v[24:27]
	v_mfma_f32_16x16x128_f8f6f4 v[12:15], v[144:151], v[198:205], v[12:15]
	v_mfma_f32_16x16x128_f8f6f4 v[16:19], v[152:159], v[198:205], v[16:19]
	v_mfma_f32_16x16x128_f8f6f4 v[4:7], v[144:151], v[206:213], v[4:7]
	v_mfma_f32_16x16x128_f8f6f4 v[8:11], v[152:159], v[206:213], v[8:11]
	v_mfma_f32_16x16x128_f8f6f4 v[60:63], v[166:173], v[182:189], v[60:63]
	v_mfma_f32_16x16x128_f8f6f4 v[64:67], v[174:181], v[182:189], v[64:67]
	v_mfma_f32_16x16x128_f8f6f4 v[52:55], v[166:173], v[190:197], v[52:55]
	v_mfma_f32_16x16x128_f8f6f4 v[56:59], v[174:181], v[190:197], v[56:59]
	v_mfma_f32_16x16x128_f8f6f4 v[44:47], v[166:173], v[198:205], v[44:47]
	v_mfma_f32_16x16x128_f8f6f4 v[48:51], v[174:181], v[198:205], v[48:51]
	v_mfma_f32_16x16x128_f8f6f4 v[36:39], v[166:173], v[206:213], v[36:39]
	v_mfma_f32_16x16x128_f8f6f4 v[40:43], v[174:181], v[206:213], v[40:43]
	s_setprio 0
	s_barrier
	s_mov_b32 m0, s30
	ds_read_b128 v[182:185], v163 offset:49152
	ds_read_b128 v[186:189], v163 offset:50176
	ds_read_b128 v[190:193], v163 offset:51200
	ds_read_b128 v[194:197], v163 offset:52224
	ds_read_b128 v[198:201], v163 offset:53248
	ds_read_b128 v[202:205], v163 offset:54272
	ds_read_b128 v[206:209], v163 offset:55296
	ds_read_b128 v[210:213], v163 offset:56320
	global_load_lds_dwordx4 v[130:131], off
	s_mov_b32 m0, s36
	s_nop 0
	global_load_lds_dwordx4 v[132:133], off
	s_mov_b32 m0, s38
	s_nop 0
	global_load_lds_dwordx4 v[136:137], off
	s_mov_b32 m0, s39
	s_nop 0
	global_load_lds_dwordx4 v[138:139], off
	s_mov_b32 m0, s31
	s_nop 0
	global_load_lds_dwordx4 v[128:129], off
	s_mov_b32 m0, s37
	s_nop 0
	global_load_lds_dwordx4 v[134:135], off
	s_waitcnt vmcnt(8)
	s_waitcnt lgkmcnt(0)
	s_barrier
	s_setprio 3
	v_mfma_f32_16x16x128_f8f6f4 v[68:71], v[144:151], v[182:189], v[68:71]
	v_mfma_f32_16x16x128_f8f6f4 v[84:87], v[152:159], v[182:189], v[84:87]
	v_mfma_f32_16x16x128_f8f6f4 v[72:75], v[144:151], v[190:197], v[72:75]
	v_mfma_f32_16x16x128_f8f6f4 v[88:91], v[152:159], v[190:197], v[88:91]
	v_mfma_f32_16x16x128_f8f6f4 v[76:79], v[144:151], v[198:205], v[76:79]
	v_mfma_f32_16x16x128_f8f6f4 v[92:95], v[152:159], v[198:205], v[92:95]
	v_mfma_f32_16x16x128_f8f6f4 v[80:83], v[144:151], v[206:213], v[80:83]
	v_mfma_f32_16x16x128_f8f6f4 v[96:99], v[152:159], v[206:213], v[96:99]
	v_mfma_f32_16x16x128_f8f6f4 v[116:119], v[166:173], v[182:189], v[116:119]
	v_mfma_f32_16x16x128_f8f6f4 v[124:127], v[174:181], v[182:189], v[124:127]
	v_mfma_f32_16x16x128_f8f6f4 v[108:111], v[166:173], v[190:197], v[108:111]
	v_mfma_f32_16x16x128_f8f6f4 v[120:123], v[174:181], v[190:197], v[120:123]
	v_mfma_f32_16x16x128_f8f6f4 v[104:107], v[166:173], v[198:205], v[104:107]
	v_mfma_f32_16x16x128_f8f6f4 v[112:115], v[174:181], v[198:205], v[112:115]
	v_mfma_f32_16x16x128_f8f6f4 v[100:103], v[166:173], v[206:213], v[100:103]
	v_mfma_f32_16x16x128_f8f6f4 v[0:3], v[174:181], v[206:213], v[0:3]
	s_setprio 0
	s_barrier
	s_cbranch_scc1 .LBB0_1420
	s_barrier

.LBB0_1495:
	s_mov_b64 exec, -1
	s_waitcnt vmcnt(0) lgkmcnt(0)
	s_cmp_ge_u32 s98, 1
	s_cbranch_scc1 .Lprobe_done
	s_add_u32 s98, s98, 1
	s_barrier
	v_readfirstlane_b32 s3, v249
	s_nop 3
	s_lshr_b32 s3, s3, 6
	s_cmp_lg_u32 s3, 0
	s_cbranch_scc1 .Lprobe_wait
	buffer_wbl2 sc1
	s_waitcnt vmcnt(0)
	s_load_dwordx2 s[4:5], s[100:101], 0xb0
	s_waitcnt lgkmcnt(0)
	s_add_u32 s4, s4, 0xf000
	s_addc_u32 s5, s5, 0
	v_mov_b32_e32 v1, 0
	v_mov_b32_e32 v2, 1
	s_mov_b64 exec, 1
	global_atomic_add v1, v2, s[4:5]
	s_lshl_b32 s6, s98, 8
	s_mov_b32 s7, 0
.Lprobe_spin:
	s_sleep 2
	global_load_dword v3, v1, s[4:5] sc1
	s_waitcnt vmcnt(0)
	v_readfirstlane_b32 s8, v3
	s_add_u32 s7, s7, 1
	s_nop 1
	s_cmp_ge_u32 s8, s6
	s_cbranch_scc1 .Lprobe_spun
	s_cmp_lt_u32 s7, 0x8000
	s_cbranch_scc1 .Lprobe_spin
.Lprobe_spun:
	s_mov_b64 exec, -1
	buffer_inv sc1
	s_waitcnt vmcnt(0)
.Lprobe_wait:
	s_barrier
	s_mov_b64 s[0:1], s[100:101]
	s_mov_b32 s2, s99
	v_mov_b32_e32 v0, v249
	s_branch .Lprobe_tramp2

; #define LAS __attribute__((address_space(3)))
; __global__ void __launch_bounds__(NTHREADS, 2) fwd(Args args) {
;     extern __shared__ __attribute__((aligned(16))) unsigned char lds[];
;     Frame F;
;     F.lds = (LAS unsigned char*)lds; F.MISC = (volatile LAS unsigned*)(F.lds + MISC_OFF);
;     F.tid = threadIdx.x; F.lane = F.tid & 63; F.wave = __builtin_amdgcn_readfirstlane(F.tid >> 6); F.bid = blockIdx.x;
	.amdhsa_kernel _Z3fwd4Args
		.amdhsa_group_segment_fixed_size 0
		.amdhsa_private_segment_fixed_size 0
		.amdhsa_kernarg_size 448
		.amdhsa_user_sgpr_count 2
		.amdhsa_user_sgpr_dispatch_ptr 0
		.amdhsa_user_sgpr_queue_ptr 0
		.amdhsa_user_sgpr_kernarg_segment_ptr 1
		.amdhsa_user_sgpr_dispatch_id 0
		.amdhsa_user_sgpr_kernarg_preload_length 0
		.amdhsa_user_sgpr_kernarg_preload_offset 0
		.amdhsa_user_sgpr_private_segment_size 0
		.amdhsa_uses_dynamic_stack 0
		.amdhsa_enable_private_segment 0
		.amdhsa_system_sgpr_workgroup_id_x 1
		.amdhsa_system_sgpr_workgroup_id_y 0
		.amdhsa_system_sgpr_workgroup_id_z 0
		.amdhsa_system_sgpr_workgroup_info 0
		.amdhsa_system_vgpr_workitem_id 0
		.amdhsa_next_free_vgpr 250
		.amdhsa_next_free_sgpr 102
		.amdhsa_accum_offset 252
		.amdhsa_reserve_vcc 1
		.amdhsa_float_round_mode_32 0
		.amdhsa_float_round_mode_16_64 0
		.amdhsa_float_denorm_mode_32 3
		.amdhsa_float_denorm_mode_16_64 3
		.amdhsa_dx10_clamp 1
		.amdhsa_ieee_mode 1
		.amdhsa_fp16_overflow 0
		.amdhsa_tg_split 0
		.amdhsa_exception_fp_ieee_invalid_op 0
		.amdhsa_exception_fp_denorm_src 0
		.amdhsa_exception_fp_ieee_div_zero 0
		.amdhsa_exception_fp_ieee_overflow 0
		.amdhsa_exception_fp_ieee_underflow 0
		.amdhsa_exception_fp_ieee_inexact 0
		.amdhsa_exception_int_div_zero 0
	.end_amdhsa_kernel

; #define LAS __attribute__((address_space(3)))
; __global__ void __launch_bounds__(NTHREADS, 2) fwd(Args args) {
;     extern __shared__ __attribute__((aligned(16))) unsigned char lds[];
;     Frame F;
;     F.lds = (LAS unsigned char*)lds; F.MISC = (volatile LAS unsigned*)(F.lds + MISC_OFF);
;     F.tid = threadIdx.x; F.lane = F.tid & 63; F.wave = __builtin_amdgcn_readfirstlane(F.tid >> 6); F.bid = blockIdx.x;
amdhsa.kernels:
  - .agpr_count:     0
    .args:
      - .offset:         0
        .size:           192
        .value_kind:     by_value
      - .offset:         192
        .size:           4
        .value_kind:     hidden_block_count_x
      - .offset:         196
        .size:           4
        .value_kind:     hidden_block_count_y
      - .offset:         200
        .size:           4
        .value_kind:     hidden_block_count_z
      - .offset:         204
        .size:           2
        .value_kind:     hidden_group_size_x
      - .offset:         206
        .size:           2
        .value_kind:     hidden_group_size_y
      - .offset:         208
        .size:           2
        .value_kind:     hidden_group_size_z
      - .offset:         210
        .size:           2
        .value_kind:     hidden_remainder_x
      - .offset:         212
        .size:           2
        .value_kind:     hidden_remainder_y
      - .offset:         214
        .size:           2
        .value_kind:     hidden_remainder_z
      - .offset:         232
        .size:           8
        .value_kind:     hidden_global_offset_x
      - .offset:         240
        .size:           8
        .value_kind:     hidden_global_offset_y
      - .offset:         248
        .size:           8
        .value_kind:     hidden_global_offset_z
      - .offset:         256
        .size:           2
        .value_kind:     hidden_grid_dims
      - .offset:         312
        .size:           4
        .value_kind:     hidden_dynamic_lds_size
    .group_segment_fixed_size: 0
    .kernarg_segment_align: 8
    .kernarg_segment_size: 448
    .language:       OpenCL C
    .language_version:
      - 2
      - 0
    .max_flat_workgroup_size: 512
    .name:           _Z3fwd4Args
    .private_segment_fixed_size: 0
    .sgpr_count:     108
    .sgpr_spill_count: 10
    .symbol:         _Z3fwd4Args.kd
    .uniform_work_group_size: 1
    .uses_dynamic_stack: false
    .vgpr_count:     250
    .vgpr_spill_count: 0
    .wavefront_size: 64
